# write-through (sc0 sc1) epilogue stores in the G_in and KVQ/Q GEMMs, the phases that end in a grid barrier, so the barrier leader's L2 writeback finds less dirty data (on v16 chain)
# speedup vs baseline: 1.0054x; 1.0054x over previous
.LBB0_174:
	v_mbcnt_lo_u32_b32 v250, -1, 0
	v_mbcnt_hi_u32_b32 v250, -1, v250
	v_lshrrev_b32_e32 v251, 2, v250
	v_and_b32_e32 v250, 3, v250
	v_lshl_add_u32 v250, v250, 4, v251
	v_lshlrev_b32_e32 v250, 2, v250
	s_ashr_i32 s15, s60, 3
	s_add_i32 s62, s15, s75
	s_lshl_b32 s15, s60, 8
	s_and_b32 s15, s15, 0x700
	s_cmp_eq_u32 s62, 0
	v_lshl_add_u32 v174, s28, 8, v1
	s_cselect_b64 s[26:27], -1, 0
	v_or_b32_e32 v82, s15, v209
	s_and_b64 s[26:27], s[50:51], s[26:27]
	v_or_b32_e32 v180, 16, v174
	v_or_b32_e32 v178, 32, v174
	v_or_b32_e32 v176, 48, v174
	s_mov_b64 s[64:65], -1
	s_and_b64 vcc, exec, s[26:27]
	v_lshlrev_b32_e32 v114, 1, v82
	v_ashrrev_i32_e32 v175, 31, v174
	v_ashrrev_i32_e32 v181, 31, v180
	v_ashrrev_i32_e32 v179, 31, v178
	v_ashrrev_i32_e32 v177, 31, v176
	s_cbranch_vccnz .LBB0_177
	v_lshl_add_u32 v158, s14, 10, v210
	ds_read2_b32 v[88:89], v158 offset1:16
	s_ashr_i32 s63, s62, 31
	s_lshl_b64 s[26:27], s[62:63], 25
	s_add_u32 s26, s84, s26
	s_addc_u32 s27, s85, s27
	v_lshl_add_u64 v[90:91], s[26:27], 0, v[114:115]
	v_lshlrev_b64 v[82:83], 12, v[174:175]
	s_waitcnt lgkmcnt(0)
	v_pk_mul_f32 v[84:85], v[144:145], v[88:89] op_sel_hi:[1,0]
	v_lshl_add_u64 v[82:83], v[90:91], 0, v[82:83]
	v_pk_mul_f32 v[86:87], v[146:147], v[88:89] op_sel_hi:[1,0]
	v_cvt_pk_bf16_f32 v84, v84, v85
	v_pk_mul_f32 v[92:93], v[142:143], v[88:89] op_sel_hi:[1,0]
	v_cvt_pk_bf16_f32 v85, v86, v87
	v_pk_mul_f32 v[94:95], v[140:141], v[88:89] op_sel_hi:[1,0]
	v_cvt_pk_bf16_f32 v87, v92, v93
	v_pk_mul_f32 v[92:93], v[134:135], v[88:89] op_sel_hi:[1,0]
	v_cvt_pk_bf16_f32 v86, v94, v95
	ds_bpermute_b32 v232, v250, v84
	ds_bpermute_b32 v233, v250, v85
	ds_bpermute_b32 v234, v250, v86
	ds_bpermute_b32 v235, v250, v87
	ds_bpermute_b32 v236, v250, v82
	v_pk_mul_f32 v[94:95], v[132:133], v[88:89] op_sel_hi:[1,0]
	s_mov_b32 s15, 0x80000
	v_pk_mul_f32 v[84:85], v[136:137], v[88:89] op_sel_hi:[1,0]
	v_pk_mul_f32 v[86:87], v[138:139], v[88:89] op_sel_hi:[1,0]
	v_cvt_pk_bf16_f32 v84, v84, v85
	v_mov_b32_e32 v88, v89
	v_cvt_pk_bf16_f32 v85, v86, v87
	v_cvt_pk_bf16_f32 v86, v94, v95
	v_cvt_pk_bf16_f32 v87, v92, v93
	ds_bpermute_b32 v238, v250, v84
	ds_bpermute_b32 v239, v250, v85
	ds_bpermute_b32 v240, v250, v86
	ds_bpermute_b32 v241, v250, v87
	ds_bpermute_b32 v242, v250, v82
	v_pk_mul_f32 v[94:95], v[126:127], v[88:89] op_sel_hi:[1,0]
	v_pk_mul_f32 v[96:97], v[124:125], v[88:89] op_sel_hi:[1,0]
	v_lshlrev_b64 v[84:85], 12, v[180:181]
	v_lshl_add_u64 v[92:93], v[90:91], 0, v[84:85]
	v_pk_mul_f32 v[86:87], v[130:131], v[88:89] op_sel_hi:[1,0]
	v_pk_mul_f32 v[84:85], v[128:129], v[88:89] op_sel_hi:[1,0]
	s_mov_b64 s[16:17], 0x80000
	v_cvt_pk_bf16_f32 v84, v84, v85
	v_cvt_pk_bf16_f32 v85, v86, v87
	v_cvt_pk_bf16_f32 v86, v96, v97
	v_cvt_pk_bf16_f32 v87, v94, v95
	s_waitcnt lgkmcnt(5)
	v_subrev_u32_e32 v236, s82, v236
	global_store_dwordx4 v236, v[232:235], s[82:83] sc0 sc1
	ds_bpermute_b32 v244, v250, v84
	ds_bpermute_b32 v245, v250, v85
	ds_bpermute_b32 v246, v250, v86
	ds_bpermute_b32 v247, v250, v87
	ds_bpermute_b32 v248, v250, v92
	v_pk_mul_f32 v[94:95], v[118:119], v[88:89] op_sel_hi:[1,0]
	s_nop 0
	v_pk_mul_f32 v[86:87], v[122:123], v[88:89] op_sel_hi:[1,0]
	v_pk_mul_f32 v[84:85], v[120:121], v[88:89] op_sel_hi:[1,0]
	v_pk_mul_f32 v[88:89], v[116:117], v[88:89] op_sel_hi:[1,0]
	v_cvt_pk_bf16_f32 v84, v84, v85
	v_cvt_pk_bf16_f32 v85, v86, v87
	v_cvt_pk_bf16_f32 v87, v94, v95
	s_nop 0
	v_cvt_pk_bf16_f32 v86, v88, v89
	ds_read2_b32 v[88:89], v158 offset0:32 offset1:48
	s_waitcnt lgkmcnt(6)
	v_subrev_u32_e32 v242, s82, v242
	global_store_dwordx4 v242, v[238:241], s[82:83] offset:64 sc0 sc1
	ds_bpermute_b32 v232, v250, v84
	ds_bpermute_b32 v233, v250, v85
	ds_bpermute_b32 v234, v250, v86
	ds_bpermute_b32 v235, v250, v87
	ds_bpermute_b32 v236, v250, v92
	s_waitcnt lgkmcnt(0)
	v_pk_mul_f32 v[94:95], v[108:109], v[88:89] op_sel_hi:[1,0]
	v_lshlrev_b64 v[84:85], 12, v[178:179]
	v_lshl_add_u64 v[92:93], v[90:91], 0, v[84:85]
	v_pk_mul_f32 v[84:85], v[110:111], v[88:89] op_sel_hi:[1,0]
	v_pk_mul_f32 v[86:87], v[112:113], v[88:89] op_sel_hi:[1,0]
	v_cvt_pk_bf16_f32 v84, v84, v85
	v_pk_mul_f32 v[96:97], v[106:107], v[88:89] op_sel_hi:[1,0]
	v_cvt_pk_bf16_f32 v85, v86, v87
	v_cvt_pk_bf16_f32 v87, v94, v95
	v_pk_mul_f32 v[94:95], v[100:101], v[88:89] op_sel_hi:[1,0]
	v_cvt_pk_bf16_f32 v86, v96, v97
	s_waitcnt lgkmcnt(6)
	v_subrev_u32_e32 v248, s82, v248
	global_store_dwordx4 v248, v[244:247], s[82:83] sc0 sc1
	ds_bpermute_b32 v238, v250, v84
	ds_bpermute_b32 v239, v250, v85
	ds_bpermute_b32 v240, v250, v86
	ds_bpermute_b32 v241, v250, v87
	ds_bpermute_b32 v242, v250, v92
	v_pk_mul_f32 v[96:97], v[98:99], v[88:89] op_sel_hi:[1,0]
	s_nop 0
	v_pk_mul_f32 v[84:85], v[102:103], v[88:89] op_sel_hi:[1,0]
	v_pk_mul_f32 v[86:87], v[104:105], v[88:89] op_sel_hi:[1,0]
	v_cvt_pk_bf16_f32 v84, v84, v85
	v_mov_b32_e32 v88, v89
	v_cvt_pk_bf16_f32 v85, v86, v87
	v_cvt_pk_bf16_f32 v86, v96, v97
	v_cvt_pk_bf16_f32 v87, v94, v95
	s_waitcnt lgkmcnt(5)
	v_subrev_u32_e32 v236, s82, v236
	global_store_dwordx4 v236, v[232:235], s[82:83] offset:64 sc0 sc1
	ds_bpermute_b32 v244, v250, v84
	ds_bpermute_b32 v245, v250, v85
	ds_bpermute_b32 v246, v250, v86
	ds_bpermute_b32 v247, v250, v87
	ds_bpermute_b32 v248, v250, v92
	v_pk_mul_f32 v[94:95], v[74:75], v[88:89] op_sel_hi:[1,0]
	v_pk_mul_f32 v[92:93], v[76:77], v[88:89] op_sel_hi:[1,0]
	v_lshlrev_b64 v[84:85], 12, v[176:177]
	v_lshl_add_u64 v[90:91], v[90:91], 0, v[84:85]
	v_pk_mul_f32 v[86:87], v[80:81], v[88:89] op_sel_hi:[1,0]
	v_pk_mul_f32 v[84:85], v[78:79], v[88:89] op_sel_hi:[1,0]
	s_nop 0
	v_cvt_pk_bf16_f32 v84, v84, v85
	v_cvt_pk_bf16_f32 v85, v86, v87
	v_cvt_pk_bf16_f32 v86, v94, v95
	ds_read2_b32 v[94:95], v158 offset0:128 offset1:144
	v_cvt_pk_bf16_f32 v87, v92, v93
	s_waitcnt lgkmcnt(6)
	v_subrev_u32_e32 v242, s82, v242
	global_store_dwordx4 v242, v[238:241], s[82:83] sc0 sc1
	ds_bpermute_b32 v232, v250, v84
	ds_bpermute_b32 v233, v250, v85
	ds_bpermute_b32 v234, v250, v86
	ds_bpermute_b32 v235, v250, v87
	ds_bpermute_b32 v236, v250, v90
	v_pk_mul_f32 v[92:93], v[68:69], v[88:89] op_sel_hi:[1,0]
	s_nop 0
	v_pk_mul_f32 v[86:87], v[72:73], v[88:89] op_sel_hi:[1,0]
	v_pk_mul_f32 v[84:85], v[70:71], v[88:89] op_sel_hi:[1,0]
	v_pk_mul_f32 v[88:89], v[66:67], v[88:89] op_sel_hi:[1,0]
	v_cvt_pk_bf16_f32 v84, v84, v85
	v_cvt_pk_bf16_f32 v85, v86, v87
	v_cvt_pk_bf16_f32 v87, v92, v93
	s_waitcnt lgkmcnt(0)
	v_pk_mul_f32 v[92:93], v[58:59], v[94:95] op_sel_hi:[1,0]
	v_cvt_pk_bf16_f32 v86, v88, v89
	s_waitcnt lgkmcnt(6)
	v_subrev_u32_e32 v248, s82, v248
	global_store_dwordx4 v248, v[244:247], s[82:83] offset:64 sc0 sc1
	ds_bpermute_b32 v238, v250, v84
	ds_bpermute_b32 v239, v250, v85
	ds_bpermute_b32 v240, v250, v86
	ds_bpermute_b32 v241, v250, v87
	ds_bpermute_b32 v242, v250, v90
	v_pk_mul_f32 v[90:91], v[60:61], v[94:95] op_sel_hi:[1,0]
	v_lshl_add_u64 v[88:89], v[82:83], 0, s[16:17]
	v_pk_mul_f32 v[86:87], v[64:65], v[94:95] op_sel_hi:[1,0]
	v_pk_mul_f32 v[84:85], v[62:63], v[94:95] op_sel_hi:[1,0]
	s_mov_b64 s[16:17], 0x90000
	v_cvt_pk_bf16_f32 v84, v84, v85
	v_cvt_pk_bf16_f32 v85, v86, v87
	v_cvt_pk_bf16_f32 v87, v90, v91
	v_add_co_u32_e32 v90, vcc, s15, v82
	v_cvt_pk_bf16_f32 v86, v92, v93
	v_pk_mul_f32 v[92:93], v[50:51], v[94:95] op_sel_hi:[1,0]
	s_nop 0
	v_addc_co_u32_e32 v91, vcc, 0, v83, vcc
	s_waitcnt lgkmcnt(5)
	v_subrev_u32_e32 v236, s82, v236
	global_store_dwordx4 v236, v[232:235], s[82:83] sc0 sc1
	ds_bpermute_b32 v244, v250, v84
	ds_bpermute_b32 v245, v250, v85
	ds_bpermute_b32 v246, v250, v86
	ds_bpermute_b32 v247, v250, v87
	ds_bpermute_b32 v248, v250, v90
	v_pk_mul_f32 v[90:91], v[52:53], v[94:95] op_sel_hi:[1,0]
	s_mov_b32 s15, 0x90000
	v_pk_mul_f32 v[86:87], v[56:57], v[94:95] op_sel_hi:[1,0]
	v_pk_mul_f32 v[84:85], v[54:55], v[94:95] op_sel_hi:[1,0]
	s_nop 0
	v_cvt_pk_bf16_f32 v84, v84, v85
	v_cvt_pk_bf16_f32 v85, v86, v87
	v_cvt_pk_bf16_f32 v86, v92, v93
	v_cvt_pk_bf16_f32 v87, v90, v91
	v_mov_b32_e32 v90, v95
	s_waitcnt lgkmcnt(5)
	v_subrev_u32_e32 v242, s82, v242
	global_store_dwordx4 v242, v[238:241], s[82:83] offset:64 sc0 sc1
	ds_bpermute_b32 v232, v250, v84
	ds_bpermute_b32 v233, v250, v85
	ds_bpermute_b32 v234, v250, v86
	ds_bpermute_b32 v235, v250, v87
	ds_bpermute_b32 v236, v250, v88
	v_pk_mul_f32 v[94:95], v[42:43], v[90:91] op_sel_hi:[1,0]
	v_pk_mul_f32 v[92:93], v[44:45], v[90:91] op_sel_hi:[1,0]
	v_pk_mul_f32 v[86:87], v[48:49], v[90:91] op_sel_hi:[1,0]
	v_pk_mul_f32 v[84:85], v[46:47], v[90:91] op_sel_hi:[1,0]
	v_lshl_add_u64 v[88:89], v[82:83], 0, s[16:17]
	v_cvt_pk_bf16_f32 v84, v84, v85
	v_cvt_pk_bf16_f32 v85, v86, v87
	v_cvt_pk_bf16_f32 v86, v94, v95
	ds_read2_b32 v[94:95], v158 offset0:160 offset1:176
	v_cvt_pk_bf16_f32 v87, v92, v93
	v_add_co_u32_e32 v92, vcc, s15, v82
	s_mov_b32 s15, 0xa0000
	s_nop 0
	v_addc_co_u32_e32 v93, vcc, 0, v83, vcc
	s_waitcnt lgkmcnt(6)
	v_subrev_u32_e32 v248, s82, v248
	global_store_dwordx4 v248, v[244:247], s[82:83] sc0 sc1
	ds_bpermute_b32 v238, v250, v84
	ds_bpermute_b32 v239, v250, v85
	ds_bpermute_b32 v240, v250, v86
	ds_bpermute_b32 v241, v250, v87
	ds_bpermute_b32 v242, v250, v92
	v_pk_mul_f32 v[92:93], v[36:37], v[90:91] op_sel_hi:[1,0]
	s_mov_b64 s[16:17], 0xa0000
	v_pk_mul_f32 v[86:87], v[40:41], v[90:91] op_sel_hi:[1,0]
	v_pk_mul_f32 v[84:85], v[38:39], v[90:91] op_sel_hi:[1,0]
	v_pk_mul_f32 v[90:91], v[34:35], v[90:91] op_sel_hi:[1,0]
	v_cvt_pk_bf16_f32 v84, v84, v85
	v_cvt_pk_bf16_f32 v85, v86, v87
	v_cvt_pk_bf16_f32 v87, v92, v93
	s_waitcnt lgkmcnt(0)
	v_pk_mul_f32 v[92:93], v[26:27], v[94:95] op_sel_hi:[1,0]
	v_cvt_pk_bf16_f32 v86, v90, v91
	s_waitcnt lgkmcnt(6)
	v_subrev_u32_e32 v236, s82, v236
	global_store_dwordx4 v236, v[232:235], s[82:83] offset:64 sc0 sc1
	ds_bpermute_b32 v244, v250, v84
	ds_bpermute_b32 v245, v250, v85
	ds_bpermute_b32 v246, v250, v86
	ds_bpermute_b32 v247, v250, v87
	ds_bpermute_b32 v248, v250, v88
	v_pk_mul_f32 v[90:91], v[28:29], v[94:95] op_sel_hi:[1,0]
	v_lshl_add_u64 v[88:89], v[82:83], 0, s[16:17]
	v_pk_mul_f32 v[86:87], v[32:33], v[94:95] op_sel_hi:[1,0]
	v_pk_mul_f32 v[84:85], v[30:31], v[94:95] op_sel_hi:[1,0]
	s_mov_b64 s[16:17], 0xb0000
	v_cvt_pk_bf16_f32 v84, v84, v85
	v_cvt_pk_bf16_f32 v85, v86, v87
	v_cvt_pk_bf16_f32 v87, v90, v91
	v_add_co_u32_e32 v90, vcc, s15, v82
	v_cvt_pk_bf16_f32 v86, v92, v93
	s_mov_b32 s15, 0xb0000
	s_nop 0
	v_addc_co_u32_e32 v91, vcc, 0, v83, vcc
	s_waitcnt lgkmcnt(5)
	v_subrev_u32_e32 v242, s82, v242
	global_store_dwordx4 v242, v[238:241], s[82:83] sc0 sc1
	ds_bpermute_b32 v232, v250, v84
	ds_bpermute_b32 v233, v250, v85
	ds_bpermute_b32 v234, v250, v86
	ds_bpermute_b32 v235, v250, v87
	ds_bpermute_b32 v236, v250, v90
	v_pk_mul_f32 v[90:91], v[20:21], v[94:95] op_sel_hi:[1,0]
	v_pk_mul_f32 v[92:93], v[18:19], v[94:95] op_sel_hi:[1,0]
	v_pk_mul_f32 v[86:87], v[24:25], v[94:95] op_sel_hi:[1,0]
	v_pk_mul_f32 v[84:85], v[22:23], v[94:95] op_sel_hi:[1,0]
	s_nop 0
	v_cvt_pk_bf16_f32 v84, v84, v85
	v_cvt_pk_bf16_f32 v85, v86, v87
	v_cvt_pk_bf16_f32 v87, v90, v91
	v_mov_b32_e32 v90, v95
	v_cvt_pk_bf16_f32 v86, v92, v93
	s_waitcnt lgkmcnt(5)
	v_subrev_u32_e32 v248, s82, v248
	global_store_dwordx4 v248, v[244:247], s[82:83] offset:64 sc0 sc1
	ds_bpermute_b32 v238, v250, v84
	ds_bpermute_b32 v239, v250, v85
	ds_bpermute_b32 v240, v250, v86
	ds_bpermute_b32 v241, v250, v87
	ds_bpermute_b32 v242, v250, v88
	v_lshl_add_u64 v[88:89], v[82:83], 0, s[16:17]
	v_add_co_u32_e32 v82, vcc, s15, v82
	v_pk_mul_f32 v[84:85], v[14:15], v[90:91] op_sel_hi:[1,0]
	v_pk_mul_f32 v[86:87], v[16:17], v[90:91] op_sel_hi:[1,0]
	v_cvt_pk_bf16_f32 v84, v84, v85
	v_addc_co_u32_e32 v83, vcc, 0, v83, vcc
	v_cvt_pk_bf16_f32 v85, v86, v87
	v_pk_mul_f32 v[92:93], v[12:13], v[90:91] op_sel_hi:[1,0]
	v_pk_mul_f32 v[94:95], v[10:11], v[90:91] op_sel_hi:[1,0]
	v_cvt_pk_bf16_f32 v87, v92, v93
	s_nop 0
	v_cvt_pk_bf16_f32 v86, v94, v95
	s_waitcnt lgkmcnt(5)
	v_subrev_u32_e32 v236, s82, v236
	global_store_dwordx4 v236, v[232:235], s[82:83] sc0 sc1
	ds_bpermute_b32 v244, v250, v84
	ds_bpermute_b32 v245, v250, v85
	ds_bpermute_b32 v246, v250, v86
	ds_bpermute_b32 v247, v250, v87
	ds_bpermute_b32 v248, v250, v82
	v_pk_mul_f32 v[82:83], v[6:7], v[90:91] op_sel_hi:[1,0]
	s_nop 0
	v_pk_mul_f32 v[84:85], v[8:9], v[90:91] op_sel_hi:[1,0]
	v_pk_mul_f32 v[86:87], v[4:5], v[90:91] op_sel_hi:[1,0]
	v_pk_mul_f32 v[90:91], v[2:3], v[90:91] op_sel_hi:[1,0]
	v_cvt_pk_bf16_f32 v82, v82, v83
	v_cvt_pk_bf16_f32 v83, v84, v85
	v_cvt_pk_bf16_f32 v85, v86, v87
	s_nop 0
	v_cvt_pk_bf16_f32 v84, v90, v91
	s_waitcnt lgkmcnt(5)
	v_subrev_u32_e32 v242, s82, v242
	global_store_dwordx4 v242, v[238:241], s[82:83] offset:64 sc0 sc1
	ds_bpermute_b32 v232, v250, v82
	ds_bpermute_b32 v233, v250, v83
	ds_bpermute_b32 v234, v250, v84
	ds_bpermute_b32 v235, v250, v85
	ds_bpermute_b32 v236, v250, v88
	s_waitcnt lgkmcnt(5)
	v_subrev_u32_e32 v248, s82, v248
	global_store_dwordx4 v248, v[244:247], s[82:83] sc0 sc1
	s_waitcnt lgkmcnt(0)
	v_subrev_u32_e32 v236, s82, v236
	global_store_dwordx4 v236, v[232:235], s[82:83] offset:64 sc0 sc1
	s_cbranch_execz .LBB0_178

.LBB0_178:
	s_lshl_b32 s14, s14, 10
	v_add_u32_e32 v213, s14, v211
	ds_read_b32 v82, v213
	s_waitcnt lgkmcnt(0)
	v_pk_mul_f32 v[84:85], v[146:147], v[82:83] op_sel_hi:[1,0]
	v_pk_mul_f32 v[86:87], v[144:145], v[82:83] op_sel_hi:[1,0]
	v_pk_mul_f32 v[84:85], v[84:85], v[84:85]
	v_pk_mul_f32 v[88:89], v[140:141], v[82:83] op_sel_hi:[1,0]
	v_pk_fma_f32 v[84:85], v[86:87], v[86:87], v[84:85]
	v_pk_mul_f32 v[86:87], v[142:143], v[82:83] op_sel_hi:[1,0]
	s_nop 0
	v_pk_mul_f32 v[86:87], v[86:87], v[86:87]
	s_nop 0
	v_pk_fma_f32 v[86:87], v[88:89], v[88:89], v[86:87]
	v_pk_mul_f32 v[88:89], v[136:137], v[82:83] op_sel_hi:[1,0]
	v_pk_add_f32 v[84:85], v[84:85], v[86:87]
	v_pk_mul_f32 v[86:87], v[138:139], v[82:83] op_sel_hi:[1,0]
	s_nop 0
	v_pk_mul_f32 v[86:87], v[86:87], v[86:87]
	s_nop 0
	v_pk_fma_f32 v[86:87], v[88:89], v[88:89], v[86:87]
	s_nop 0
	v_pk_add_f32 v[84:85], v[86:87], v[84:85]
	v_pk_mul_f32 v[86:87], v[134:135], v[82:83] op_sel_hi:[1,0]
	v_pk_mul_f32 v[82:83], v[132:133], v[82:83] op_sel_hi:[1,0]
	v_pk_mul_f32 v[86:87], v[86:87], v[86:87]
	s_nop 0
	v_pk_fma_f32 v[82:83], v[82:83], v[82:83], v[86:87]
	s_nop 0
	v_pk_add_f32 v[82:83], v[82:83], v[84:85]
	s_nop 0
	v_add_f32_e32 v82, v82, v83
	ds_swizzle_b32 v83, v82 offset:swizzle(SWAP,16)
	s_waitcnt lgkmcnt(0)
	v_add_f32_e32 v82, v82, v83
	v_mov_b32_e32 v83, v82
	s_nop 1
	v_permlane32_swap_b32_e32 v82, v83
	s_and_saveexec_b64 s[62:63], s[38:39]
	v_add_f32_e32 v82, v82, v83
	ds_write_b32 v183, v82
	s_or_b64 exec, exec, s[62:63]
	ds_read_b32 v82, v213 offset:64
	s_waitcnt lgkmcnt(0)
	v_pk_mul_f32 v[84:85], v[130:131], v[82:83] op_sel_hi:[1,0]
	v_pk_mul_f32 v[86:87], v[128:129], v[82:83] op_sel_hi:[1,0]
	v_pk_mul_f32 v[84:85], v[84:85], v[84:85]
	v_pk_mul_f32 v[88:89], v[124:125], v[82:83] op_sel_hi:[1,0]
	v_pk_fma_f32 v[84:85], v[86:87], v[86:87], v[84:85]
	v_pk_mul_f32 v[86:87], v[126:127], v[82:83] op_sel_hi:[1,0]
	s_nop 0
	v_pk_mul_f32 v[86:87], v[86:87], v[86:87]
	s_nop 0
	v_pk_fma_f32 v[86:87], v[88:89], v[88:89], v[86:87]
	v_pk_mul_f32 v[88:89], v[120:121], v[82:83] op_sel_hi:[1,0]
	v_pk_add_f32 v[84:85], v[84:85], v[86:87]
	v_pk_mul_f32 v[86:87], v[122:123], v[82:83] op_sel_hi:[1,0]
	s_nop 0
	v_pk_mul_f32 v[86:87], v[86:87], v[86:87]
	s_nop 0
	v_pk_fma_f32 v[86:87], v[88:89], v[88:89], v[86:87]
	s_nop 0
	v_pk_add_f32 v[84:85], v[86:87], v[84:85]
	v_pk_mul_f32 v[86:87], v[118:119], v[82:83] op_sel_hi:[1,0]
	v_pk_mul_f32 v[82:83], v[116:117], v[82:83] op_sel_hi:[1,0]
	v_pk_mul_f32 v[86:87], v[86:87], v[86:87]
	s_nop 0
	v_pk_fma_f32 v[82:83], v[82:83], v[82:83], v[86:87]
	s_nop 0
	v_pk_add_f32 v[82:83], v[82:83], v[84:85]
	s_nop 0
	v_add_f32_e32 v82, v82, v83
	ds_swizzle_b32 v83, v82 offset:swizzle(SWAP,16)
	s_waitcnt lgkmcnt(0)
	v_add_f32_e32 v82, v82, v83
	v_mov_b32_e32 v83, v82
	s_nop 1
	v_permlane32_swap_b32_e32 v82, v83
	s_and_saveexec_b64 s[62:63], s[38:39]
	v_add_f32_e32 v82, v82, v83
	ds_write_b32 v195, v82
	s_or_b64 exec, exec, s[62:63]
	ds_read_b32 v82, v213 offset:128
	s_waitcnt lgkmcnt(0)
	v_pk_mul_f32 v[84:85], v[112:113], v[82:83] op_sel_hi:[1,0]
	v_pk_mul_f32 v[86:87], v[110:111], v[82:83] op_sel_hi:[1,0]
	v_pk_mul_f32 v[84:85], v[84:85], v[84:85]
	v_pk_mul_f32 v[88:89], v[106:107], v[82:83] op_sel_hi:[1,0]
	v_pk_fma_f32 v[84:85], v[86:87], v[86:87], v[84:85]
	v_pk_mul_f32 v[86:87], v[108:109], v[82:83] op_sel_hi:[1,0]
	s_nop 0
	v_pk_mul_f32 v[86:87], v[86:87], v[86:87]
	s_nop 0
	v_pk_fma_f32 v[86:87], v[88:89], v[88:89], v[86:87]
	v_pk_mul_f32 v[88:89], v[102:103], v[82:83] op_sel_hi:[1,0]
	v_pk_add_f32 v[84:85], v[84:85], v[86:87]
	v_pk_mul_f32 v[86:87], v[104:105], v[82:83] op_sel_hi:[1,0]
	s_nop 0
	v_pk_mul_f32 v[86:87], v[86:87], v[86:87]
	s_nop 0
	v_pk_fma_f32 v[86:87], v[88:89], v[88:89], v[86:87]
	s_nop 0
	v_pk_add_f32 v[84:85], v[86:87], v[84:85]
	v_pk_mul_f32 v[86:87], v[100:101], v[82:83] op_sel_hi:[1,0]
	v_pk_mul_f32 v[82:83], v[98:99], v[82:83] op_sel_hi:[1,0]
	v_pk_mul_f32 v[86:87], v[86:87], v[86:87]
	s_nop 0
	v_pk_fma_f32 v[82:83], v[82:83], v[82:83], v[86:87]
	s_nop 0
	v_pk_add_f32 v[82:83], v[82:83], v[84:85]
	s_nop 0
	v_add_f32_e32 v82, v82, v83
	ds_swizzle_b32 v83, v82 offset:swizzle(SWAP,16)
	s_waitcnt lgkmcnt(0)
	v_add_f32_e32 v82, v82, v83
	v_mov_b32_e32 v83, v82
	s_nop 1
	v_permlane32_swap_b32_e32 v82, v83
	s_and_saveexec_b64 s[62:63], s[38:39]
	v_add_f32_e32 v82, v82, v83
	ds_write_b32 v197, v82
	s_or_b64 exec, exec, s[62:63]
	ds_read_b32 v82, v213 offset:192
	s_waitcnt lgkmcnt(0)
	v_pk_mul_f32 v[84:85], v[80:81], v[82:83] op_sel_hi:[1,0]
	v_pk_mul_f32 v[86:87], v[78:79], v[82:83] op_sel_hi:[1,0]
	v_pk_mul_f32 v[84:85], v[84:85], v[84:85]
	v_pk_mul_f32 v[88:89], v[74:75], v[82:83] op_sel_hi:[1,0]
	v_pk_fma_f32 v[84:85], v[86:87], v[86:87], v[84:85]
	v_pk_mul_f32 v[86:87], v[76:77], v[82:83] op_sel_hi:[1,0]
	s_nop 0
	v_pk_mul_f32 v[86:87], v[86:87], v[86:87]
	s_nop 0
	v_pk_fma_f32 v[86:87], v[88:89], v[88:89], v[86:87]
	v_pk_mul_f32 v[88:89], v[70:71], v[82:83] op_sel_hi:[1,0]
	v_pk_add_f32 v[84:85], v[84:85], v[86:87]
	v_pk_mul_f32 v[86:87], v[72:73], v[82:83] op_sel_hi:[1,0]
	s_nop 0
	v_pk_mul_f32 v[86:87], v[86:87], v[86:87]
	s_nop 0
	v_pk_fma_f32 v[86:87], v[88:89], v[88:89], v[86:87]
	s_nop 0
	v_pk_add_f32 v[84:85], v[86:87], v[84:85]
	v_pk_mul_f32 v[86:87], v[68:69], v[82:83] op_sel_hi:[1,0]
	v_pk_mul_f32 v[82:83], v[66:67], v[82:83] op_sel_hi:[1,0]
	v_pk_mul_f32 v[86:87], v[86:87], v[86:87]
	s_nop 0
	v_pk_fma_f32 v[82:83], v[82:83], v[82:83], v[86:87]
	s_nop 0
	v_pk_add_f32 v[82:83], v[82:83], v[84:85]
	s_nop 0
	v_add_f32_e32 v82, v82, v83
	ds_swizzle_b32 v83, v82 offset:swizzle(SWAP,16)
	s_waitcnt lgkmcnt(0)
	v_add_f32_e32 v82, v82, v83
	v_mov_b32_e32 v83, v82
	s_nop 1
	v_permlane32_swap_b32_e32 v82, v83
	s_and_saveexec_b64 s[62:63], s[38:39]
	v_add_f32_e32 v82, v82, v83
	ds_write_b32 v199, v82
	s_or_b64 exec, exec, s[62:63]
	ds_read_b32 v82, v213 offset:512
	s_waitcnt lgkmcnt(0)
	v_pk_mul_f32 v[84:85], v[64:65], v[82:83] op_sel_hi:[1,0]
	v_pk_mul_f32 v[86:87], v[62:63], v[82:83] op_sel_hi:[1,0]
	v_pk_mul_f32 v[84:85], v[84:85], v[84:85]
	v_pk_mul_f32 v[88:89], v[58:59], v[82:83] op_sel_hi:[1,0]
	v_pk_fma_f32 v[84:85], v[86:87], v[86:87], v[84:85]
	v_pk_mul_f32 v[86:87], v[60:61], v[82:83] op_sel_hi:[1,0]
	s_nop 0
	v_pk_mul_f32 v[86:87], v[86:87], v[86:87]
	s_nop 0
	v_pk_fma_f32 v[86:87], v[88:89], v[88:89], v[86:87]
	v_pk_mul_f32 v[88:89], v[54:55], v[82:83] op_sel_hi:[1,0]
	v_pk_add_f32 v[84:85], v[84:85], v[86:87]
	v_pk_mul_f32 v[86:87], v[56:57], v[82:83] op_sel_hi:[1,0]
	s_nop 0
	v_pk_mul_f32 v[86:87], v[86:87], v[86:87]
	s_nop 0
	v_pk_fma_f32 v[86:87], v[88:89], v[88:89], v[86:87]
	s_nop 0
	v_pk_add_f32 v[84:85], v[86:87], v[84:85]
	v_pk_mul_f32 v[86:87], v[52:53], v[82:83] op_sel_hi:[1,0]
	v_pk_mul_f32 v[82:83], v[50:51], v[82:83] op_sel_hi:[1,0]
	v_pk_mul_f32 v[86:87], v[86:87], v[86:87]
	s_nop 0
	v_pk_fma_f32 v[82:83], v[82:83], v[82:83], v[86:87]
	s_nop 0
	v_pk_add_f32 v[82:83], v[82:83], v[84:85]
	s_nop 0
	v_add_f32_e32 v82, v82, v83
	ds_swizzle_b32 v83, v82 offset:swizzle(SWAP,16)
	s_waitcnt lgkmcnt(0)
	v_add_f32_e32 v82, v82, v83
	v_mov_b32_e32 v83, v82
	s_nop 1
	v_permlane32_swap_b32_e32 v82, v83
	s_and_saveexec_b64 s[62:63], s[38:39]
	v_add_f32_e32 v82, v82, v83
	ds_write_b32 v201, v82
	s_or_b64 exec, exec, s[62:63]
	ds_read_b32 v82, v213 offset:576
	s_waitcnt lgkmcnt(0)
	v_pk_mul_f32 v[84:85], v[48:49], v[82:83] op_sel_hi:[1,0]
	v_pk_mul_f32 v[86:87], v[46:47], v[82:83] op_sel_hi:[1,0]
	v_pk_mul_f32 v[84:85], v[84:85], v[84:85]
	v_pk_mul_f32 v[88:89], v[42:43], v[82:83] op_sel_hi:[1,0]
	v_pk_fma_f32 v[84:85], v[86:87], v[86:87], v[84:85]
	v_pk_mul_f32 v[86:87], v[44:45], v[82:83] op_sel_hi:[1,0]
	s_nop 0
	v_pk_mul_f32 v[86:87], v[86:87], v[86:87]
	s_nop 0
	v_pk_fma_f32 v[86:87], v[88:89], v[88:89], v[86:87]
	v_pk_mul_f32 v[88:89], v[38:39], v[82:83] op_sel_hi:[1,0]
	v_pk_add_f32 v[84:85], v[84:85], v[86:87]
	v_pk_mul_f32 v[86:87], v[40:41], v[82:83] op_sel_hi:[1,0]
	s_nop 0
	v_pk_mul_f32 v[86:87], v[86:87], v[86:87]
	s_nop 0
	v_pk_fma_f32 v[86:87], v[88:89], v[88:89], v[86:87]
	s_nop 0
	v_pk_add_f32 v[84:85], v[86:87], v[84:85]
	v_pk_mul_f32 v[86:87], v[36:37], v[82:83] op_sel_hi:[1,0]
	v_pk_mul_f32 v[82:83], v[34:35], v[82:83] op_sel_hi:[1,0]
	v_pk_mul_f32 v[86:87], v[86:87], v[86:87]
	s_nop 0
	v_pk_fma_f32 v[82:83], v[82:83], v[82:83], v[86:87]
	s_nop 0
	v_pk_add_f32 v[82:83], v[82:83], v[84:85]
	s_nop 0
	v_add_f32_e32 v82, v82, v83
	ds_swizzle_b32 v83, v82 offset:swizzle(SWAP,16)
	s_waitcnt lgkmcnt(0)
	v_add_f32_e32 v82, v82, v83
	v_mov_b32_e32 v83, v82
	s_nop 1
	v_permlane32_swap_b32_e32 v82, v83
	s_and_saveexec_b64 s[62:63], s[38:39]
	v_add_f32_e32 v82, v82, v83
	ds_write_b32 v203, v82
	s_or_b64 exec, exec, s[62:63]
	ds_read_b32 v82, v213 offset:640
	s_waitcnt lgkmcnt(0)
	v_pk_mul_f32 v[84:85], v[32:33], v[82:83] op_sel_hi:[1,0]
	v_pk_mul_f32 v[86:87], v[30:31], v[82:83] op_sel_hi:[1,0]
	v_pk_mul_f32 v[84:85], v[84:85], v[84:85]
	v_pk_mul_f32 v[88:89], v[26:27], v[82:83] op_sel_hi:[1,0]
	v_pk_fma_f32 v[84:85], v[86:87], v[86:87], v[84:85]
	v_pk_mul_f32 v[86:87], v[28:29], v[82:83] op_sel_hi:[1,0]
	s_nop 0
	v_pk_mul_f32 v[86:87], v[86:87], v[86:87]
	s_nop 0
	v_pk_fma_f32 v[86:87], v[88:89], v[88:89], v[86:87]
	v_pk_mul_f32 v[88:89], v[22:23], v[82:83] op_sel_hi:[1,0]
	v_pk_add_f32 v[84:85], v[84:85], v[86:87]
	v_pk_mul_f32 v[86:87], v[24:25], v[82:83] op_sel_hi:[1,0]
	s_nop 0
	v_pk_mul_f32 v[86:87], v[86:87], v[86:87]
	s_nop 0
	v_pk_fma_f32 v[86:87], v[88:89], v[88:89], v[86:87]
	s_nop 0
	v_pk_add_f32 v[84:85], v[86:87], v[84:85]
	v_pk_mul_f32 v[86:87], v[20:21], v[82:83] op_sel_hi:[1,0]
	v_pk_mul_f32 v[82:83], v[18:19], v[82:83] op_sel_hi:[1,0]
	v_pk_mul_f32 v[86:87], v[86:87], v[86:87]
	s_nop 0
	v_pk_fma_f32 v[82:83], v[82:83], v[82:83], v[86:87]
	s_nop 0
	v_pk_add_f32 v[82:83], v[82:83], v[84:85]
	s_nop 0
	v_add_f32_e32 v82, v82, v83
	ds_swizzle_b32 v83, v82 offset:swizzle(SWAP,16)
	s_waitcnt lgkmcnt(0)
	v_add_f32_e32 v82, v82, v83
	v_mov_b32_e32 v83, v82
	s_nop 1
	v_permlane32_swap_b32_e32 v82, v83
	s_and_saveexec_b64 s[62:63], s[38:39]
	v_add_f32_e32 v82, v82, v83
	ds_write_b32 v205, v82
	s_or_b64 exec, exec, s[62:63]
	ds_read_b32 v82, v213 offset:704
	s_waitcnt lgkmcnt(0)
	v_pk_mul_f32 v[84:85], v[16:17], v[82:83] op_sel_hi:[1,0]
	v_pk_mul_f32 v[86:87], v[14:15], v[82:83] op_sel_hi:[1,0]
	v_pk_mul_f32 v[84:85], v[84:85], v[84:85]
	v_pk_mul_f32 v[88:89], v[10:11], v[82:83] op_sel_hi:[1,0]
	v_pk_fma_f32 v[84:85], v[86:87], v[86:87], v[84:85]
	v_pk_mul_f32 v[86:87], v[12:13], v[82:83] op_sel_hi:[1,0]
	s_nop 0
	v_pk_mul_f32 v[86:87], v[86:87], v[86:87]
	s_nop 0
	v_pk_fma_f32 v[86:87], v[88:89], v[88:89], v[86:87]
	v_pk_mul_f32 v[88:89], v[6:7], v[82:83] op_sel_hi:[1,0]
	v_pk_add_f32 v[84:85], v[84:85], v[86:87]
	v_pk_mul_f32 v[86:87], v[8:9], v[82:83] op_sel_hi:[1,0]
	s_nop 0
	v_pk_mul_f32 v[86:87], v[86:87], v[86:87]
	s_nop 0
	v_pk_fma_f32 v[86:87], v[88:89], v[88:89], v[86:87]
	s_nop 0
	v_pk_add_f32 v[84:85], v[86:87], v[84:85]
	v_pk_mul_f32 v[86:87], v[4:5], v[82:83] op_sel_hi:[1,0]
	v_pk_mul_f32 v[82:83], v[2:3], v[82:83] op_sel_hi:[1,0]
	v_pk_mul_f32 v[86:87], v[86:87], v[86:87]
	s_nop 0
	v_pk_fma_f32 v[82:83], v[82:83], v[82:83], v[86:87]
	s_nop 0
	v_pk_add_f32 v[82:83], v[82:83], v[84:85]
	s_nop 0
	v_add_f32_e32 v82, v82, v83
	ds_swizzle_b32 v83, v82 offset:swizzle(SWAP,16)
	s_waitcnt lgkmcnt(0)
	v_add_f32_e32 v82, v82, v83
	v_mov_b32_e32 v83, v82
	s_nop 1
	v_permlane32_swap_b32_e32 v82, v83
	s_and_saveexec_b64 s[62:63], s[38:39]
	v_add_f32_e32 v82, v82, v83
	ds_write_b32 v207, v82
	s_or_b64 exec, exec, s[62:63]
	s_waitcnt lgkmcnt(0)
	s_barrier
	global_load_dwordx4 v[94:97], v[168:169], off offset:16
	global_load_dwordx4 v[90:93], v[168:169], off
	global_load_dwordx4 v[82:85], v[168:169], off offset:144
	global_load_dwordx4 v[86:89], v[168:169], off offset:128
	ds_read_b32 v158, v183
	ds_read_b32 v159, v194
	s_lshl_b32 s14, s60, 1
	s_and_b32 s14, s14, 14
	s_lshl_b32 s15, s28, 1
	s_or_b32 s14, s88, s14
	s_waitcnt lgkmcnt(0)
	v_add_f32_e32 v158, v158, v159
	v_fmamk_f32 v158, v158, 0x3c000000, v185
	v_rsq_f32_e32 v160, v158
	ds_read2_b32 v[158:159], v213 offset1:16
	s_and_b32 s15, s15, 0x7fffff0
	s_or_b32 s14, s15, s14
	s_lshl_b32 s15, s28, 2
	s_and_b32 s15, s15, 28
	s_waitcnt lgkmcnt(0)
	v_mul_f32_e32 v158, v158, v160
	v_lshlrev_b64 v[160:161], 12, v[174:175]
	v_lshl_add_u64 v[160:161], s[46:47], 0, v[160:161]
	v_pk_mul_f32 v[144:145], v[144:145], v[158:159] op_sel_hi:[1,0]
	v_pk_mul_f32 v[146:147], v[146:147], v[158:159] op_sel_hi:[1,0]
	v_pk_mul_f32 v[218:219], v[140:141], v[158:159] op_sel_hi:[1,0]
	v_lshl_add_u64 v[160:161], v[160:161], 0, v[114:115]
	v_pk_mul_f32 v[140:141], v[142:143], v[158:159] op_sel_hi:[1,0]
	s_lshl_b32 s14, s14, 5
	s_add_i32 s15, s15, s8
	s_add_i32 s28, s15, s14
	s_ashr_i32 s29, s28, 31
	s_lshl_b64 s[14:15], s[28:29], 9
	s_waitcnt vmcnt(0)
	v_pk_mul_f32 v[142:143], v[94:95], v[218:219]
	v_pk_mul_f32 v[214:215], v[92:93], v[146:147]
	v_pk_mul_f32 v[216:217], v[90:91], v[144:145]
	v_pk_fma_f32 v[218:219], v[90:91], v[144:145], 0 op_sel_hi:[1,1,0]
	v_cvt_pk_bf16_f32 v144, v216, v217
	v_cvt_pk_bf16_f32 v145, v214, v215
	v_pk_mul_f32 v[140:141], v[96:97], v[140:141]
	v_pk_fma_f32 v[220:221], v[92:93], v[146:147], 0 op_sel_hi:[1,1,0]
	v_cvt_pk_bf16_f32 v146, v142, v143
	v_cvt_pk_bf16_f32 v147, v140, v141
	ds_bpermute_b32 v238, v250, v144
	ds_bpermute_b32 v239, v250, v145
	ds_bpermute_b32 v240, v250, v146
	ds_bpermute_b32 v241, v250, v147
	ds_bpermute_b32 v242, v250, v160
	s_nop 1
	v_pk_mul_f32 v[144:145], v[136:137], v[158:159] op_sel_hi:[1,0]
	v_pk_mul_f32 v[136:137], v[138:139], v[158:159] op_sel_hi:[1,0]
	v_pk_mul_f32 v[138:139], v[86:87], v[144:145]
	v_pk_mul_f32 v[144:145], v[132:133], v[158:159] op_sel_hi:[1,0]
	v_pk_mul_f32 v[132:133], v[134:135], v[158:159] op_sel_hi:[1,0]
	v_pk_mul_f32 v[136:137], v[88:89], v[136:137]
	v_pk_mul_f32 v[132:133], v[84:85], v[132:133]
	v_pk_mul_f32 v[134:135], v[82:83], v[144:145]
	v_cvt_pk_bf16_f32 v144, v138, v139
	v_cvt_pk_bf16_f32 v145, v136, v137
	v_cvt_pk_bf16_f32 v147, v132, v133
	s_nop 0
	v_cvt_pk_bf16_f32 v146, v134, v135
	ds_bpermute_b32 v244, v250, v144
	ds_bpermute_b32 v245, v250, v145
	ds_bpermute_b32 v246, v250, v146
	ds_bpermute_b32 v247, v250, v147
	ds_bpermute_b32 v248, v250, v160
	ds_read_b32 v144, v195
	ds_read_b32 v145, v196
	v_lshlrev_b64 v[146:147], 12, v[180:181]
	v_lshl_add_u64 v[146:147], s[46:47], 0, v[146:147]
	v_lshl_add_u64 v[146:147], v[146:147], 0, v[114:115]
	s_waitcnt lgkmcnt(0)
	v_add_f32_e32 v144, v144, v145
	v_fmamk_f32 v144, v144, 0x3c000000, v185
	v_rsq_f32_e32 v144, v144
	s_nop 0
	v_mul_f32_e32 v144, v159, v144
	v_pk_mul_f32 v[128:129], v[128:129], v[144:145] op_sel_hi:[1,0]
	v_pk_mul_f32 v[130:131], v[130:131], v[144:145] op_sel_hi:[1,0]
	v_pk_mul_f32 v[160:161], v[90:91], v[128:129]
	v_pk_mul_f32 v[158:159], v[92:93], v[130:131]
	v_pk_mul_f32 v[180:181], v[124:125], v[144:145] op_sel_hi:[1,0]
	v_pk_mul_f32 v[124:125], v[126:127], v[144:145] op_sel_hi:[1,0]
	v_pk_fma_f32 v[214:215], v[90:91], v[128:129], v[218:219]
	v_cvt_pk_bf16_f32 v128, v160, v161
	v_cvt_pk_bf16_f32 v129, v158, v159
	v_pk_mul_f32 v[124:125], v[96:97], v[124:125]
	v_pk_mul_f32 v[126:127], v[94:95], v[180:181]
	v_pk_fma_f32 v[180:181], v[92:93], v[130:131], v[220:221]
	v_cvt_pk_bf16_f32 v130, v126, v127
	v_cvt_pk_bf16_f32 v131, v124, v125
	s_waitcnt lgkmcnt(7)
	v_subrev_u32_e32 v242, s82, v242
	global_store_dwordx4 v242, v[238:241], s[82:83] sc0 sc1
	ds_bpermute_b32 v232, v250, v128
	ds_bpermute_b32 v233, v250, v129
	ds_bpermute_b32 v234, v250, v130
	ds_bpermute_b32 v235, v250, v131
	ds_bpermute_b32 v236, v250, v146
	s_nop 1
	v_pk_mul_f32 v[128:129], v[120:121], v[144:145] op_sel_hi:[1,0]
	v_pk_mul_f32 v[120:121], v[122:123], v[144:145] op_sel_hi:[1,0]
	v_pk_mul_f32 v[122:123], v[86:87], v[128:129]
	v_pk_mul_f32 v[128:129], v[116:117], v[144:145] op_sel_hi:[1,0]
	v_pk_mul_f32 v[116:117], v[118:119], v[144:145] op_sel_hi:[1,0]
	v_pk_mul_f32 v[120:121], v[88:89], v[120:121]
	v_pk_mul_f32 v[116:117], v[84:85], v[116:117]
	v_pk_mul_f32 v[118:119], v[82:83], v[128:129]
	v_cvt_pk_bf16_f32 v128, v122, v123
	v_cvt_pk_bf16_f32 v129, v120, v121
	v_cvt_pk_bf16_f32 v131, v116, v117
	s_nop 0
	v_cvt_pk_bf16_f32 v130, v118, v119
	s_waitcnt lgkmcnt(7)
	v_subrev_u32_e32 v248, s82, v248
	global_store_dwordx4 v248, v[244:247], s[82:83] offset:64 sc0 sc1
	ds_bpermute_b32 v238, v250, v128
	ds_bpermute_b32 v239, v250, v129
	ds_bpermute_b32 v240, v250, v130
	ds_bpermute_b32 v241, v250, v131
	ds_bpermute_b32 v242, v250, v146
	ds_read_b32 v128, v197
	ds_read_b32 v129, v198
	s_waitcnt lgkmcnt(0)
	v_add_f32_e32 v128, v128, v129
	v_fmamk_f32 v128, v128, 0x3c000000, v185
	v_rsq_f32_e32 v130, v128
	ds_read2_b32 v[128:129], v213 offset0:32 offset1:48
	s_waitcnt lgkmcnt(0)
	v_mul_f32_e32 v128, v128, v130
	v_lshlrev_b64 v[130:131], 12, v[178:179]
	v_pk_mul_f32 v[110:111], v[110:111], v[128:129] op_sel_hi:[1,0]
	v_lshl_add_u64 v[130:131], s[46:47], 0, v[130:131]
	v_pk_mul_f32 v[112:113], v[112:113], v[128:129] op_sel_hi:[1,0]
	v_pk_mul_f32 v[144:145], v[90:91], v[110:111]
	v_lshl_add_u64 v[130:131], v[130:131], 0, v[114:115]
	v_pk_mul_f32 v[146:147], v[92:93], v[112:113]
	v_pk_mul_f32 v[158:159], v[106:107], v[128:129] op_sel_hi:[1,0]
	v_pk_mul_f32 v[106:107], v[108:109], v[128:129] op_sel_hi:[1,0]
	v_cvt_pk_bf16_f32 v144, v144, v145
	v_cvt_pk_bf16_f32 v145, v146, v147
	v_pk_mul_f32 v[108:109], v[94:95], v[158:159]
	v_pk_mul_f32 v[106:107], v[96:97], v[106:107]
	v_cvt_pk_bf16_f32 v146, v108, v109
	v_pk_fma_f32 v[110:111], v[90:91], v[110:111], v[214:215]
	v_cvt_pk_bf16_f32 v147, v106, v107
	s_waitcnt lgkmcnt(8)
	v_subrev_u32_e32 v236, s82, v236
	global_store_dwordx4 v236, v[232:235], s[82:83] sc0 sc1
	ds_bpermute_b32 v244, v250, v144
	ds_bpermute_b32 v245, v250, v145
	ds_bpermute_b32 v246, v250, v146
	ds_bpermute_b32 v247, v250, v147
	ds_bpermute_b32 v248, v250, v130
	v_pk_fma_f32 v[112:113], v[92:93], v[112:113], v[180:181]
	s_nop 0
	v_pk_mul_f32 v[144:145], v[102:103], v[128:129] op_sel_hi:[1,0]
	v_pk_mul_f32 v[102:103], v[104:105], v[128:129] op_sel_hi:[1,0]
	v_pk_mul_f32 v[104:105], v[86:87], v[144:145]
	v_pk_mul_f32 v[144:145], v[98:99], v[128:129] op_sel_hi:[1,0]
	v_pk_mul_f32 v[98:99], v[100:101], v[128:129] op_sel_hi:[1,0]
	v_pk_mul_f32 v[102:103], v[88:89], v[102:103]
	v_pk_mul_f32 v[98:99], v[84:85], v[98:99]
	v_pk_mul_f32 v[100:101], v[82:83], v[144:145]
	v_cvt_pk_bf16_f32 v144, v104, v105
	v_cvt_pk_bf16_f32 v145, v102, v103
	v_cvt_pk_bf16_f32 v147, v98, v99
	s_nop 0
	v_cvt_pk_bf16_f32 v146, v100, v101
	s_waitcnt lgkmcnt(8)
	v_subrev_u32_e32 v242, s82, v242
	global_store_dwordx4 v242, v[238:241], s[82:83] offset:64 sc0 sc1
	ds_bpermute_b32 v232, v250, v144
	ds_bpermute_b32 v233, v250, v145
	ds_bpermute_b32 v234, v250, v146
	ds_bpermute_b32 v235, v250, v147
	ds_bpermute_b32 v236, v250, v130
	ds_read_b32 v128, v199
	ds_read_b32 v130, v200
	s_waitcnt lgkmcnt(0)
	v_add_f32_e32 v128, v128, v130
	v_fmamk_f32 v128, v128, 0x3c000000, v185
	v_rsq_f32_e32 v128, v128
	v_lshlrev_b64 v[130:131], 12, v[176:177]
	v_lshl_add_u64 v[130:131], s[46:47], 0, v[130:131]
	v_lshl_add_u64 v[130:131], v[130:131], 0, v[114:115]
	v_mul_f32_e32 v128, v129, v128
	v_pk_mul_f32 v[144:145], v[78:79], v[128:129] op_sel_hi:[1,0]
	v_pk_mul_f32 v[80:81], v[80:81], v[128:129] op_sel_hi:[1,0]
	v_pk_mul_f32 v[74:75], v[74:75], v[128:129] op_sel_hi:[1,0]
	v_pk_mul_f32 v[76:77], v[76:77], v[128:129] op_sel_hi:[1,0]
	v_pk_mul_f32 v[146:147], v[92:93], v[80:81]
	v_pk_mul_f32 v[158:159], v[90:91], v[144:145]
	v_pk_mul_f32 v[76:77], v[96:97], v[76:77]
	v_pk_mul_f32 v[78:79], v[94:95], v[74:75]
	v_pk_fma_f32 v[160:161], v[92:93], v[80:81], v[112:113]
	v_pk_fma_f32 v[80:81], v[90:91], v[144:145], v[110:111]
	v_cvt_pk_bf16_f32 v110, v158, v159
	v_cvt_pk_bf16_f32 v111, v146, v147
	v_cvt_pk_bf16_f32 v112, v78, v79
	v_cvt_pk_bf16_f32 v113, v76, v77
	v_pk_mul_f32 v[70:71], v[70:71], v[128:129] op_sel_hi:[1,0]
	v_pk_mul_f32 v[72:73], v[72:73], v[128:129] op_sel_hi:[1,0]
	v_pk_mul_f32 v[66:67], v[66:67], v[128:129] op_sel_hi:[1,0]
	v_pk_mul_f32 v[68:69], v[68:69], v[128:129] op_sel_hi:[1,0]
	s_waitcnt lgkmcnt(7)
	v_subrev_u32_e32 v248, s82, v248
	global_store_dwordx4 v248, v[244:247], s[82:83] sc0 sc1
	ds_bpermute_b32 v238, v250, v110
	ds_bpermute_b32 v239, v250, v111
	ds_bpermute_b32 v240, v250, v112
	ds_bpermute_b32 v241, v250, v113
	ds_bpermute_b32 v242, v250, v130
	v_pk_mul_f32 v[72:73], v[88:89], v[72:73]
	v_pk_mul_f32 v[74:75], v[86:87], v[70:71]
	v_pk_mul_f32 v[68:69], v[84:85], v[68:69]
	v_pk_mul_f32 v[70:71], v[82:83], v[66:67]
	v_cvt_pk_bf16_f32 v110, v74, v75
	v_cvt_pk_bf16_f32 v111, v72, v73
	v_cvt_pk_bf16_f32 v113, v68, v69
	v_lshl_add_u64 v[66:67], v[166:167], 0, s[14:15]
	v_cvt_pk_bf16_f32 v112, v70, v71
	s_waitcnt lgkmcnt(7)
	v_subrev_u32_e32 v236, s82, v236
	global_store_dwordx4 v236, v[232:235], s[82:83] offset:64 sc0 sc1
	ds_bpermute_b32 v244, v250, v110
	ds_bpermute_b32 v245, v250, v111
	ds_bpermute_b32 v246, v250, v112
	ds_bpermute_b32 v247, v250, v113
	ds_bpermute_b32 v248, v250, v130
	ds_swizzle_b32 v110, v80 offset:swizzle(SWAP,1)
	ds_swizzle_b32 v111, v81 offset:swizzle(SWAP,1)
	ds_swizzle_b32 v112, v160 offset:swizzle(SWAP,1)
	ds_swizzle_b32 v113, v161 offset:swizzle(SWAP,1)
	s_waitcnt lgkmcnt(2)
	v_pk_add_f32 v[80:81], v[80:81], v[110:111]
	ds_swizzle_b32 v110, v80 offset:swizzle(SWAP,2)
	s_waitcnt lgkmcnt(1)
	v_pk_add_f32 v[112:113], v[160:161], v[112:113]
	ds_swizzle_b32 v111, v81 offset:swizzle(SWAP,2)
	ds_swizzle_b32 v128, v112 offset:swizzle(SWAP,2)
	ds_swizzle_b32 v129, v113 offset:swizzle(SWAP,2)
	s_waitcnt lgkmcnt(2)
	v_pk_add_f32 v[80:81], v[80:81], v[110:111]
	ds_swizzle_b32 v110, v80 offset:swizzle(SWAP,4)
	s_waitcnt lgkmcnt(1)
	v_pk_add_f32 v[112:113], v[112:113], v[128:129]
	ds_swizzle_b32 v111, v81 offset:swizzle(SWAP,4)
	ds_swizzle_b32 v128, v112 offset:swizzle(SWAP,4)
	ds_swizzle_b32 v129, v113 offset:swizzle(SWAP,4)
	s_waitcnt lgkmcnt(2)
	v_pk_add_f32 v[80:81], v[80:81], v[110:111]
	ds_swizzle_b32 v110, v80 offset:swizzle(SWAP,8)
	s_waitcnt lgkmcnt(1)
	v_pk_add_f32 v[112:113], v[112:113], v[128:129]
	ds_swizzle_b32 v111, v81 offset:swizzle(SWAP,8)
	ds_swizzle_b32 v128, v112 offset:swizzle(SWAP,8)
	ds_swizzle_b32 v129, v113 offset:swizzle(SWAP,8)
	s_waitcnt lgkmcnt(15)
	v_subrev_u32_e32 v242, s82, v242
	global_store_dwordx4 v242, v[238:241], s[82:83] sc0 sc1
	s_waitcnt lgkmcnt(15)
	v_subrev_u32_e32 v248, s82, v248
	global_store_dwordx4 v248, v[244:247], s[82:83] offset:64 sc0 sc1
	s_and_saveexec_b64 s[60:61], s[40:41]
	s_cbranch_execz .LBB0_196
	s_waitcnt lgkmcnt(0)
	v_pk_add_f32 v[112:113], v[112:113], v[128:129]
	v_pk_add_f32 v[110:111], v[80:81], v[110:111]
	global_store_dwordx4 v[66:67], v[110:113], off

.LBB0_202:
	s_or_b64 exec, exec, s[60:61]
	ds_read_b32 v66, v201
	ds_read_b32 v67, v202
	ds_read2_b32 v[68:69], v213 offset0:128 offset1:144
	s_mov_b64 s[14:15], 0x80000
	s_waitcnt lgkmcnt(1)
	v_add_f32_e32 v66, v66, v67
	v_fmamk_f32 v66, v66, 0x3c000000, v185
	v_rsq_f32_e32 v66, v66
	s_waitcnt lgkmcnt(0)
	v_mul_f32_e32 v68, v68, v66
	v_lshlrev_b64 v[66:67], 12, v[174:175]
	v_lshl_add_u64 v[66:67], s[46:47], 0, v[66:67]
	v_lshl_add_u64 v[66:67], v[66:67], 0, v[114:115]
	v_pk_mul_f32 v[64:65], v[64:65], v[68:69] op_sel_hi:[1,0]
	v_lshl_add_u64 v[70:71], v[66:67], 0, s[14:15]
	v_pk_mul_f32 v[62:63], v[62:63], v[68:69] op_sel_hi:[1,0]
	v_pk_mul_f32 v[72:73], v[92:93], v[64:65]
	v_pk_mul_f32 v[76:77], v[58:59], v[68:69] op_sel_hi:[1,0]
	s_mov_b32 s14, 0x80000
	v_pk_mul_f32 v[74:75], v[90:91], v[62:63]
	v_pk_mul_f32 v[58:59], v[60:61], v[68:69] op_sel_hi:[1,0]
	v_pk_mul_f32 v[60:61], v[94:95], v[76:77]
	v_pk_fma_f32 v[76:77], v[90:91], v[62:63], 0 op_sel_hi:[1,1,0]
	v_cvt_pk_bf16_f32 v63, v72, v73
	v_add_co_u32_e32 v72, vcc, s14, v66
	v_cvt_pk_bf16_f32 v62, v74, v75
	v_pk_mul_f32 v[58:59], v[96:97], v[58:59]
	s_nop 0
	v_addc_co_u32_e32 v73, vcc, 0, v67, vcc
	v_pk_fma_f32 v[78:79], v[92:93], v[64:65], 0 op_sel_hi:[1,1,0]
	v_cvt_pk_bf16_f32 v64, v60, v61
	v_cvt_pk_bf16_f32 v65, v58, v59
	ds_bpermute_b32 v232, v250, v62
	ds_bpermute_b32 v233, v250, v63
	ds_bpermute_b32 v234, v250, v64
	ds_bpermute_b32 v235, v250, v65
	ds_bpermute_b32 v236, v250, v72
	s_mov_b64 s[14:15], 0x90000
	s_nop 0
	v_pk_mul_f32 v[62:63], v[54:55], v[68:69] op_sel_hi:[1,0]
	v_pk_mul_f32 v[54:55], v[56:57], v[68:69] op_sel_hi:[1,0]
	v_pk_mul_f32 v[56:57], v[86:87], v[62:63]
	v_pk_mul_f32 v[62:63], v[50:51], v[68:69] op_sel_hi:[1,0]
	v_pk_mul_f32 v[50:51], v[52:53], v[68:69] op_sel_hi:[1,0]
	v_pk_mul_f32 v[54:55], v[88:89], v[54:55]
	v_pk_mul_f32 v[50:51], v[84:85], v[50:51]
	v_pk_mul_f32 v[52:53], v[82:83], v[62:63]
	v_cvt_pk_bf16_f32 v62, v56, v57
	v_cvt_pk_bf16_f32 v63, v54, v55
	v_cvt_pk_bf16_f32 v65, v50, v51
	s_nop 0
	v_cvt_pk_bf16_f32 v64, v52, v53
	ds_bpermute_b32 v238, v250, v62
	ds_bpermute_b32 v239, v250, v63
	ds_bpermute_b32 v240, v250, v64
	ds_bpermute_b32 v241, v250, v65
	ds_bpermute_b32 v242, v250, v70
	ds_read_b32 v62, v203
	ds_read_b32 v63, v204
	v_lshl_add_u64 v[64:65], v[66:67], 0, s[14:15]
	s_mov_b32 s14, 0x90000
	s_waitcnt lgkmcnt(0)
	v_add_f32_e32 v62, v62, v63
	v_fmamk_f32 v62, v62, 0x3c000000, v185
	v_rsq_f32_e32 v62, v62
	s_nop 0
	v_mul_f32_e32 v62, v69, v62
	v_pk_mul_f32 v[48:49], v[48:49], v[62:63] op_sel_hi:[1,0]
	v_pk_mul_f32 v[46:47], v[46:47], v[62:63] op_sel_hi:[1,0]
	v_pk_mul_f32 v[68:69], v[92:93], v[48:49]
	v_pk_mul_f32 v[70:71], v[90:91], v[46:47]
	v_pk_fma_f32 v[74:75], v[90:91], v[46:47], v[76:77]
	v_cvt_pk_bf16_f32 v47, v68, v69
	v_add_co_u32_e32 v68, vcc, s14, v66
	v_pk_mul_f32 v[72:73], v[42:43], v[62:63] op_sel_hi:[1,0]
	v_pk_mul_f32 v[42:43], v[44:45], v[62:63] op_sel_hi:[1,0]
	v_cvt_pk_bf16_f32 v46, v70, v71
	v_addc_co_u32_e32 v69, vcc, 0, v67, vcc
	v_pk_mul_f32 v[42:43], v[96:97], v[42:43]
	v_pk_mul_f32 v[44:45], v[94:95], v[72:73]
	v_pk_fma_f32 v[72:73], v[92:93], v[48:49], v[78:79]
	v_cvt_pk_bf16_f32 v48, v44, v45
	v_cvt_pk_bf16_f32 v49, v42, v43
	s_waitcnt lgkmcnt(7)
	v_subrev_u32_e32 v236, s82, v236
	global_store_dwordx4 v236, v[232:235], s[82:83] sc0 sc1
	ds_bpermute_b32 v244, v250, v46
	ds_bpermute_b32 v245, v250, v47
	ds_bpermute_b32 v246, v250, v48
	ds_bpermute_b32 v247, v250, v49
	ds_bpermute_b32 v248, v250, v68
	s_mov_b64 s[14:15], 0xa0000
	s_nop 0
	v_pk_mul_f32 v[46:47], v[38:39], v[62:63] op_sel_hi:[1,0]
	v_pk_mul_f32 v[38:39], v[40:41], v[62:63] op_sel_hi:[1,0]
	v_pk_mul_f32 v[40:41], v[86:87], v[46:47]
	v_pk_mul_f32 v[46:47], v[34:35], v[62:63] op_sel_hi:[1,0]
	v_pk_mul_f32 v[34:35], v[36:37], v[62:63] op_sel_hi:[1,0]
	v_pk_mul_f32 v[38:39], v[88:89], v[38:39]
	v_pk_mul_f32 v[34:35], v[84:85], v[34:35]
	v_pk_mul_f32 v[36:37], v[82:83], v[46:47]
	v_cvt_pk_bf16_f32 v46, v40, v41
	v_cvt_pk_bf16_f32 v47, v38, v39
	v_cvt_pk_bf16_f32 v49, v34, v35
	s_nop 0
	v_cvt_pk_bf16_f32 v48, v36, v37
	s_waitcnt lgkmcnt(7)
	v_subrev_u32_e32 v242, s82, v242
	global_store_dwordx4 v242, v[238:241], s[82:83] offset:64 sc0 sc1
	ds_bpermute_b32 v232, v250, v46
	ds_bpermute_b32 v233, v250, v47
	ds_bpermute_b32 v234, v250, v48
	ds_bpermute_b32 v235, v250, v49
	ds_bpermute_b32 v236, v250, v64
	ds_read_b32 v46, v205
	ds_read_b32 v47, v206
	s_waitcnt lgkmcnt(0)
	v_add_f32_e32 v46, v46, v47
	v_fmamk_f32 v46, v46, 0x3c000000, v185
	v_rsq_f32_e32 v48, v46
	ds_read2_b32 v[46:47], v213 offset0:160 offset1:176
	s_waitcnt lgkmcnt(0)
	v_mul_f32_e32 v46, v46, v48
	v_lshl_add_u64 v[48:49], v[66:67], 0, s[14:15]
	v_pk_mul_f32 v[30:31], v[30:31], v[46:47] op_sel_hi:[1,0]
	v_pk_mul_f32 v[68:69], v[26:27], v[46:47] op_sel_hi:[1,0]
	s_mov_b32 s14, 0xa0000
	v_pk_mul_f32 v[32:33], v[32:33], v[46:47] op_sel_hi:[1,0]
	v_pk_mul_f32 v[62:63], v[90:91], v[30:31]
	v_pk_mul_f32 v[26:27], v[28:29], v[46:47] op_sel_hi:[1,0]
	v_pk_mul_f32 v[28:29], v[94:95], v[68:69]
	v_add_co_u32_e32 v68, vcc, s14, v66
	v_pk_mul_f32 v[64:65], v[92:93], v[32:33]
	v_cvt_pk_bf16_f32 v62, v62, v63
	s_nop 0
	v_addc_co_u32_e32 v69, vcc, 0, v67, vcc
	v_cvt_pk_bf16_f32 v63, v64, v65
	v_pk_mul_f32 v[26:27], v[96:97], v[26:27]
	v_cvt_pk_bf16_f32 v64, v28, v29
	s_mov_b64 s[14:15], 0xb0000
	v_cvt_pk_bf16_f32 v65, v26, v27
	s_waitcnt lgkmcnt(8)
	v_subrev_u32_e32 v248, s82, v248
	global_store_dwordx4 v248, v[244:247], s[82:83] sc0 sc1
	ds_bpermute_b32 v238, v250, v62
	ds_bpermute_b32 v239, v250, v63
	ds_bpermute_b32 v240, v250, v64
	ds_bpermute_b32 v241, v250, v65
	ds_bpermute_b32 v242, v250, v68
	v_pk_fma_f32 v[30:31], v[90:91], v[30:31], v[74:75]
	v_pk_fma_f32 v[32:33], v[92:93], v[32:33], v[72:73]
	v_pk_mul_f32 v[62:63], v[22:23], v[46:47] op_sel_hi:[1,0]
	v_pk_mul_f32 v[22:23], v[24:25], v[46:47] op_sel_hi:[1,0]
	v_pk_mul_f32 v[24:25], v[86:87], v[62:63]
	v_pk_mul_f32 v[62:63], v[18:19], v[46:47] op_sel_hi:[1,0]
	v_pk_mul_f32 v[18:19], v[20:21], v[46:47] op_sel_hi:[1,0]
	v_pk_mul_f32 v[22:23], v[88:89], v[22:23]
	v_pk_mul_f32 v[18:19], v[84:85], v[18:19]
	v_pk_mul_f32 v[20:21], v[82:83], v[62:63]
	v_cvt_pk_bf16_f32 v62, v24, v25
	v_cvt_pk_bf16_f32 v63, v22, v23
	v_cvt_pk_bf16_f32 v65, v18, v19
	s_nop 0
	v_cvt_pk_bf16_f32 v64, v20, v21
	s_waitcnt lgkmcnt(8)
	v_subrev_u32_e32 v236, s82, v236
	global_store_dwordx4 v236, v[232:235], s[82:83] offset:64 sc0 sc1
	ds_bpermute_b32 v244, v250, v62
	ds_bpermute_b32 v245, v250, v63
	ds_bpermute_b32 v246, v250, v64
	ds_bpermute_b32 v247, v250, v65
	ds_bpermute_b32 v248, v250, v48
	ds_read_b32 v46, v207
	ds_read_b32 v48, v208
	s_waitcnt lgkmcnt(0)
	v_add_f32_e32 v46, v46, v48
	v_fmamk_f32 v46, v46, 0x3c000000, v185
	v_rsq_f32_e32 v46, v46
	v_lshl_add_u64 v[48:49], v[66:67], 0, s[14:15]
	s_mov_b32 s14, 0xb0000
	v_mul_f32_e32 v46, v47, v46
	v_pk_mul_f32 v[10:11], v[10:11], v[46:47] op_sel_hi:[1,0]
	v_pk_mul_f32 v[62:63], v[14:15], v[46:47] op_sel_hi:[1,0]
	v_pk_mul_f32 v[16:17], v[16:17], v[46:47] op_sel_hi:[1,0]
	v_pk_mul_f32 v[12:13], v[12:13], v[46:47] op_sel_hi:[1,0]
	v_pk_mul_f32 v[14:15], v[94:95], v[10:11]
	v_add_co_u32_e32 v10, vcc, s14, v66
	v_pk_mul_f32 v[64:65], v[92:93], v[16:17]
	v_pk_mul_f32 v[68:69], v[90:91], v[62:63]
	v_pk_mul_f32 v[12:13], v[96:97], v[12:13]
	v_pk_fma_f32 v[70:71], v[92:93], v[16:17], v[32:33]
	v_pk_fma_f32 v[16:17], v[90:91], v[62:63], v[30:31]
	v_cvt_pk_bf16_f32 v30, v68, v69
	v_cvt_pk_bf16_f32 v31, v64, v65
	v_cvt_pk_bf16_f32 v32, v14, v15
	v_cvt_pk_bf16_f32 v33, v12, v13
	v_addc_co_u32_e32 v11, vcc, 0, v67, vcc
	v_pk_mul_f32 v[6:7], v[6:7], v[46:47] op_sel_hi:[1,0]
	v_pk_mul_f32 v[8:9], v[8:9], v[46:47] op_sel_hi:[1,0]
	v_pk_mul_f32 v[2:3], v[2:3], v[46:47] op_sel_hi:[1,0]
	v_pk_mul_f32 v[4:5], v[4:5], v[46:47] op_sel_hi:[1,0]
	s_waitcnt lgkmcnt(7)
	v_subrev_u32_e32 v242, s82, v242
	global_store_dwordx4 v242, v[238:241], s[82:83] sc0 sc1
	ds_bpermute_b32 v232, v250, v30
	ds_bpermute_b32 v233, v250, v31
	ds_bpermute_b32 v234, v250, v32
	ds_bpermute_b32 v235, v250, v33
	ds_bpermute_b32 v236, v250, v10
	v_pk_mul_f32 v[8:9], v[88:89], v[8:9]
	v_pk_mul_f32 v[10:11], v[86:87], v[6:7]
	v_pk_mul_f32 v[4:5], v[84:85], v[4:5]
	v_pk_mul_f32 v[6:7], v[82:83], v[2:3]
	v_cvt_pk_bf16_f32 v30, v10, v11
	v_cvt_pk_bf16_f32 v31, v8, v9
	v_cvt_pk_bf16_f32 v33, v4, v5
	s_add_i32 s14, s28, 2
	v_cvt_pk_bf16_f32 v32, v6, v7
	s_waitcnt lgkmcnt(7)
	v_subrev_u32_e32 v248, s82, v248
	global_store_dwordx4 v248, v[244:247], s[82:83] offset:64 sc0 sc1
	ds_bpermute_b32 v238, v250, v30
	ds_bpermute_b32 v239, v250, v31
	ds_bpermute_b32 v240, v250, v32
	ds_bpermute_b32 v241, v250, v33
	ds_bpermute_b32 v242, v250, v48
	ds_swizzle_b32 v30, v16 offset:swizzle(SWAP,1)
	ds_swizzle_b32 v31, v17 offset:swizzle(SWAP,1)
	ds_swizzle_b32 v32, v70 offset:swizzle(SWAP,1)
	ds_swizzle_b32 v33, v71 offset:swizzle(SWAP,1)
	s_ashr_i32 s15, s14, 31
	s_lshl_b64 s[14:15], s[14:15], 9
	s_waitcnt lgkmcnt(2)
	v_pk_add_f32 v[16:17], v[16:17], v[30:31]
	ds_swizzle_b32 v30, v16 offset:swizzle(SWAP,2)
	s_waitcnt lgkmcnt(1)
	v_pk_add_f32 v[32:33], v[70:71], v[32:33]
	ds_swizzle_b32 v31, v17 offset:swizzle(SWAP,2)
	ds_swizzle_b32 v46, v32 offset:swizzle(SWAP,2)
	ds_swizzle_b32 v47, v33 offset:swizzle(SWAP,2)
	v_lshl_add_u64 v[2:3], v[166:167], 0, s[14:15]
	s_waitcnt lgkmcnt(2)
	v_pk_add_f32 v[16:17], v[16:17], v[30:31]
	ds_swizzle_b32 v30, v16 offset:swizzle(SWAP,4)
	s_waitcnt lgkmcnt(1)
	v_pk_add_f32 v[32:33], v[32:33], v[46:47]
	ds_swizzle_b32 v31, v17 offset:swizzle(SWAP,4)
	ds_swizzle_b32 v46, v32 offset:swizzle(SWAP,4)
	ds_swizzle_b32 v47, v33 offset:swizzle(SWAP,4)
	s_waitcnt lgkmcnt(2)
	v_pk_add_f32 v[16:17], v[16:17], v[30:31]
	ds_swizzle_b32 v30, v16 offset:swizzle(SWAP,8)
	s_waitcnt lgkmcnt(1)
	v_pk_add_f32 v[32:33], v[32:33], v[46:47]
	ds_swizzle_b32 v31, v17 offset:swizzle(SWAP,8)
	ds_swizzle_b32 v46, v32 offset:swizzle(SWAP,8)
	ds_swizzle_b32 v47, v33 offset:swizzle(SWAP,8)
	s_waitcnt lgkmcnt(15)
	v_subrev_u32_e32 v236, s82, v236
	global_store_dwordx4 v236, v[232:235], s[82:83] sc0 sc1
	s_waitcnt lgkmcnt(15)
	v_subrev_u32_e32 v242, s82, v242
	global_store_dwordx4 v242, v[238:241], s[82:83] offset:64 sc0 sc1
	s_and_saveexec_b64 s[28:29], s[40:41]
	s_cbranch_execz .LBB0_204
	s_waitcnt lgkmcnt(0)
	v_pk_add_f32 v[32:33], v[32:33], v[46:47]
	v_pk_add_f32 v[30:31], v[16:17], v[30:31]
	global_store_dwordx4 v[2:3], v[30:33], off

.LBB0_352:
	s_ashr_i32 s59, s58, 31
	s_lshl_b64 s[14:15], s[58:59], 25
	s_add_u32 s14, s37, s14
	s_addc_u32 s15, s64, s15
	v_lshlrev_b32_e32 v114, 1, v177
	v_ashrrev_i32_e32 v153, 31, v152
	v_lshl_add_u64 v[132:133], s[14:15], 0, v[114:115]
	v_lshlrev_b64 v[136:137], 12, v[152:153]
	v_mov_b32_e32 v155, v154
	v_lshl_add_u64 v[136:137], v[132:133], 0, v[136:137]
	v_cvt_pk_bf16_f32 v166, v166, v167
	v_cvt_pk_bf16_f32 v167, v134, v135
	v_cvt_pk_bf16_f32 v168, v168, v169
	v_cvt_pk_bf16_f32 v169, v138, v139
	v_mov_b32_e32 v158, v154
	v_mov_b32_e32 v159, v154
	v_cndmask_b32_e64 v114, 0, 1, s[56:57]
	ds_bpermute_b32 v232, v250, v166
	ds_bpermute_b32 v233, v250, v167
	ds_bpermute_b32 v234, v250, v168
	ds_bpermute_b32 v235, v250, v169
	ds_bpermute_b32 v236, v250, v136
	v_pk_mul_f32 v[138:139], v[122:123], v[158:159]
	v_pk_mul_f32 v[134:135], v[120:121], v[154:155]
	v_pk_mul_f32 v[166:167], v[118:119], v[158:159]
	v_cmp_ne_u32_e64 s[40:41], 1, v114
	s_andn2_b64 vcc, exec, s[56:57]
	v_pk_mul_f32 v[168:169], v[116:117], v[154:155]
	s_waitcnt lgkmcnt(0)
	v_subrev_u32_e32 v236, s82, v236
	global_store_dwordx4 v236, v[232:235], s[82:83] sc0 sc1
	s_cbranch_vccnz .LBB0_354
	v_max_f32_e32 v114, v134, v134
	v_max_f32_e32 v134, 0xc2a00000, v114
	v_max_f32_e32 v114, v168, v168
	v_max_f32_e32 v158, 0xc2a00000, v114
	v_mul_f32_e32 v114, 0xbfb8aa3b, v134
	v_exp_f32_e32 v114, v114
	v_mul_f32_e32 v155, 0xbfb8aa3b, v158
	v_exp_f32_e32 v155, v155
	v_max_f32_e32 v135, v135, v135
	v_add_f32_e32 v114, 1.0, v114
	v_rcp_f32_e32 v160, v114
	v_add_f32_e32 v114, 1.0, v155
	v_max_f32_e32 v135, 0xc2a00000, v135
	v_max_f32_e32 v155, v169, v169
	v_max_f32_e32 v159, 0xc2a00000, v155
	v_mul_f32_e32 v155, 0xbfb8aa3b, v135
	v_exp_f32_e32 v155, v155
	v_mul_f32_e32 v161, 0xbfb8aa3b, v159
	v_exp_f32_e32 v169, v161
	v_max_f32_e32 v138, v138, v138
	v_rcp_f32_e32 v168, v114
	v_add_f32_e32 v114, 1.0, v155
	v_max_f32_e32 v138, 0xc2a00000, v138
	v_max_f32_e32 v155, v166, v166
	v_max_f32_e32 v166, 0xc2a00000, v155
	v_mul_f32_e32 v155, 0xbfb8aa3b, v138
	v_exp_f32_e32 v155, v155
	v_rcp_f32_e32 v161, v114
	v_add_f32_e32 v114, 1.0, v169
	v_mul_f32_e32 v169, 0xbfb8aa3b, v166
	v_exp_f32_e32 v171, v169
	v_max_f32_e32 v139, v139, v139
	v_rcp_f32_e32 v169, v114
	v_add_f32_e32 v114, 1.0, v155
	v_max_f32_e32 v139, 0xc2a00000, v139
	v_max_f32_e32 v155, v167, v167
	v_max_f32_e32 v167, 0xc2a00000, v155
	v_mul_f32_e32 v155, 0xbfb8aa3b, v139
	v_rcp_f32_e32 v170, v114
	v_add_f32_e32 v114, 1.0, v171
	v_exp_f32_e32 v155, v155
	v_mul_f32_e32 v171, 0xbfb8aa3b, v167
	v_exp_f32_e32 v179, v171
	v_rcp_f32_e32 v178, v114
	v_add_f32_e32 v114, 1.0, v155
	v_rcp_f32_e32 v171, v114
	v_add_f32_e32 v114, 1.0, v179
	v_rcp_f32_e32 v179, v114
	v_pk_mul_f32 v[134:135], v[134:135], v[160:161]
	v_pk_mul_f32 v[138:139], v[138:139], v[170:171]
	v_pk_mul_f32 v[168:169], v[158:159], v[168:169]
	v_pk_mul_f32 v[166:167], v[166:167], v[178:179]
.LBB0_354:
	v_cvt_pk_bf16_f32 v178, v134, v135
	ds_read_b32 v134, v176 offset:64
	v_cvt_pk_bf16_f32 v179, v138, v139
	v_cvt_pk_bf16_f32 v180, v168, v169
	v_cvt_pk_bf16_f32 v181, v166, v167
	s_and_b64 vcc, exec, s[40:41]
	s_waitcnt lgkmcnt(0)
	v_pk_mul_f32 v[138:139], v[112:113], v[134:135] op_sel_hi:[1,0]
	v_pk_mul_f32 v[168:169], v[110:111], v[134:135] op_sel_hi:[1,0]
	v_pk_mul_f32 v[166:167], v[108:109], v[134:135] op_sel_hi:[1,0]
	v_pk_mul_f32 v[170:171], v[106:107], v[134:135] op_sel_hi:[1,0]
	ds_bpermute_b32 v238, v250, v178
	ds_bpermute_b32 v239, v250, v179
	ds_bpermute_b32 v240, v250, v180
	ds_bpermute_b32 v241, v250, v181
	ds_bpermute_b32 v242, v250, v136
	s_waitcnt lgkmcnt(0)
	v_subrev_u32_e32 v242, s82, v242
	global_store_dwordx4 v242, v[238:241], s[82:83] offset:64 sc0 sc1
	s_cbranch_vccnz .LBB0_356
	v_max_f32_e32 v114, v168, v168
	v_max_f32_e32 v136, 0xc2a00000, v114
	v_max_f32_e32 v114, v170, v170
	v_max_f32_e32 v158, 0xc2a00000, v114
	v_mul_f32_e32 v114, 0xbfb8aa3b, v136
	v_exp_f32_e32 v114, v114
	v_mul_f32_e32 v135, 0xbfb8aa3b, v158
	v_exp_f32_e32 v135, v135
	v_add_f32_e32 v114, 1.0, v114
	v_rcp_f32_e32 v160, v114
	v_add_f32_e32 v114, 1.0, v135
	v_max_f32_e32 v135, v169, v169
	v_max_f32_e32 v137, 0xc2a00000, v135
	v_max_f32_e32 v135, v171, v171
	v_max_f32_e32 v159, 0xc2a00000, v135
	v_mul_f32_e32 v135, 0xbfb8aa3b, v137
	v_exp_f32_e32 v135, v135
	v_mul_f32_e32 v155, 0xbfb8aa3b, v159
	v_rcp_f32_e32 v170, v114
	v_exp_f32_e32 v155, v155
	v_add_f32_e32 v114, 1.0, v135
	v_max_f32_e32 v135, v138, v138
	v_max_f32_e32 v138, 0xc2a00000, v135
	v_max_f32_e32 v135, v166, v166
	v_max_f32_e32 v166, 0xc2a00000, v135
	v_mul_f32_e32 v135, 0xbfb8aa3b, v138
	v_exp_f32_e32 v135, v135
	v_rcp_f32_e32 v161, v114
	v_add_f32_e32 v114, 1.0, v155
	v_mul_f32_e32 v155, 0xbfb8aa3b, v166
	v_exp_f32_e32 v155, v155
	v_rcp_f32_e32 v171, v114
	v_add_f32_e32 v114, 1.0, v135
	v_max_f32_e32 v135, v139, v139
	v_max_f32_e32 v139, 0xc2a00000, v135
	v_max_f32_e32 v135, v167, v167
	v_max_f32_e32 v167, 0xc2a00000, v135
	v_mul_f32_e32 v135, 0xbfb8aa3b, v139
	v_rcp_f32_e32 v178, v114
	v_add_f32_e32 v114, 1.0, v155
	v_exp_f32_e32 v135, v135
	v_mul_f32_e32 v155, 0xbfb8aa3b, v167
	v_exp_f32_e32 v155, v155
	v_rcp_f32_e32 v180, v114
	v_add_f32_e32 v114, 1.0, v135
	v_rcp_f32_e32 v179, v114
	v_add_f32_e32 v114, 1.0, v155
	v_rcp_f32_e32 v181, v114
	v_pk_mul_f32 v[168:169], v[136:137], v[160:161]
	v_pk_mul_f32 v[138:139], v[138:139], v[178:179]
	v_pk_mul_f32 v[170:171], v[158:159], v[170:171]
	v_pk_mul_f32 v[166:167], v[166:167], v[180:181]
.LBB0_356:
	v_or_b32_e32 v136, 16, v152
	v_ashrrev_i32_e32 v137, 31, v136
	v_lshlrev_b64 v[136:137], 12, v[136:137]
	v_mov_b32_e32 v135, v134
	v_lshl_add_u64 v[136:137], v[132:133], 0, v[136:137]
	v_cvt_pk_bf16_f32 v168, v168, v169
	v_cvt_pk_bf16_f32 v169, v138, v139
	v_cvt_pk_bf16_f32 v170, v170, v171
	v_cvt_pk_bf16_f32 v171, v166, v167
	v_mov_b32_e32 v158, v134
	v_mov_b32_e32 v159, v134
	ds_bpermute_b32 v244, v250, v168
	ds_bpermute_b32 v245, v250, v169
	ds_bpermute_b32 v246, v250, v170
	ds_bpermute_b32 v247, v250, v171
	ds_bpermute_b32 v248, v250, v136
	v_pk_mul_f32 v[138:139], v[104:105], v[158:159]
	v_pk_mul_f32 v[166:167], v[100:101], v[158:159]
	v_pk_mul_f32 v[168:169], v[102:103], v[134:135]
	s_and_b64 vcc, exec, s[40:41]
	v_pk_mul_f32 v[170:171], v[98:99], v[134:135]
	s_waitcnt lgkmcnt(0)
	v_subrev_u32_e32 v248, s82, v248
	global_store_dwordx4 v248, v[244:247], s[82:83] sc0 sc1
	s_cbranch_vccnz .LBB0_358
	v_max_f32_e32 v114, v168, v168
	v_max_f32_e32 v134, 0xc2a00000, v114
	v_max_f32_e32 v114, v170, v170
	v_max_f32_e32 v158, 0xc2a00000, v114
	v_mul_f32_e32 v114, 0xbfb8aa3b, v134
	v_exp_f32_e32 v114, v114
	v_mul_f32_e32 v135, 0xbfb8aa3b, v158
	v_exp_f32_e32 v135, v135
	v_max_f32_e32 v155, v171, v171
	v_add_f32_e32 v114, 1.0, v114
	v_rcp_f32_e32 v160, v114
	v_add_f32_e32 v114, 1.0, v135
	v_max_f32_e32 v135, v169, v169
	v_max_f32_e32 v135, 0xc2a00000, v135
	v_max_f32_e32 v159, 0xc2a00000, v155
	v_mul_f32_e32 v155, 0xbfb8aa3b, v135
	v_exp_f32_e32 v155, v155
	v_mul_f32_e32 v161, 0xbfb8aa3b, v159
	v_exp_f32_e32 v168, v161
	v_max_f32_e32 v138, v138, v138
	v_rcp_f32_e32 v170, v114
	v_add_f32_e32 v114, 1.0, v155
	v_max_f32_e32 v138, 0xc2a00000, v138
	v_max_f32_e32 v155, v166, v166
	v_max_f32_e32 v166, 0xc2a00000, v155
	v_mul_f32_e32 v155, 0xbfb8aa3b, v138
	v_exp_f32_e32 v155, v155
	v_rcp_f32_e32 v161, v114
	v_add_f32_e32 v114, 1.0, v168
	v_mul_f32_e32 v168, 0xbfb8aa3b, v166
	v_exp_f32_e32 v168, v168
	v_max_f32_e32 v139, v139, v139
	v_rcp_f32_e32 v171, v114
	v_add_f32_e32 v114, 1.0, v155
	v_max_f32_e32 v139, 0xc2a00000, v139
	v_max_f32_e32 v155, v167, v167
	v_max_f32_e32 v167, 0xc2a00000, v155
	v_mul_f32_e32 v155, 0xbfb8aa3b, v139
	v_rcp_f32_e32 v178, v114
	v_add_f32_e32 v114, 1.0, v168
	v_exp_f32_e32 v155, v155
	v_mul_f32_e32 v168, 0xbfb8aa3b, v167
	v_exp_f32_e32 v168, v168
	v_rcp_f32_e32 v180, v114
	v_add_f32_e32 v114, 1.0, v155
	v_rcp_f32_e32 v179, v114
	v_add_f32_e32 v114, 1.0, v168
	v_rcp_f32_e32 v181, v114
	v_pk_mul_f32 v[168:169], v[134:135], v[160:161]
	v_pk_mul_f32 v[138:139], v[138:139], v[178:179]
	v_pk_mul_f32 v[170:171], v[158:159], v[170:171]
	v_pk_mul_f32 v[166:167], v[166:167], v[180:181]
.LBB0_358:
	ds_read_b32 v134, v176 offset:128
	v_cvt_pk_bf16_f32 v168, v168, v169
	v_cvt_pk_bf16_f32 v169, v138, v139
	v_cvt_pk_bf16_f32 v170, v170, v171
	v_cvt_pk_bf16_f32 v171, v166, v167
	ds_bpermute_b32 v232, v250, v168
	ds_bpermute_b32 v233, v250, v169
	ds_bpermute_b32 v234, v250, v170
	ds_bpermute_b32 v235, v250, v171
	ds_bpermute_b32 v236, v250, v136
	s_waitcnt lgkmcnt(0)
	v_pk_mul_f32 v[138:139], v[96:97], v[134:135] op_sel_hi:[1,0]
	v_pk_mul_f32 v[166:167], v[92:93], v[134:135] op_sel_hi:[1,0]
	v_pk_mul_f32 v[168:169], v[94:95], v[134:135] op_sel_hi:[1,0]
	s_and_b64 vcc, exec, s[40:41]
	v_pk_mul_f32 v[170:171], v[90:91], v[134:135] op_sel_hi:[1,0]
	s_waitcnt lgkmcnt(0)
	v_subrev_u32_e32 v236, s82, v236
	global_store_dwordx4 v236, v[232:235], s[82:83] offset:64 sc0 sc1
	s_cbranch_vccnz .LBB0_360
	v_max_f32_e32 v114, v168, v168
	v_max_f32_e32 v136, 0xc2a00000, v114
	v_max_f32_e32 v114, v170, v170
	v_max_f32_e32 v158, 0xc2a00000, v114
	v_mul_f32_e32 v114, 0xbfb8aa3b, v136
	v_exp_f32_e32 v114, v114
	v_mul_f32_e32 v135, 0xbfb8aa3b, v158
	v_exp_f32_e32 v135, v135
	v_add_f32_e32 v114, 1.0, v114
	v_rcp_f32_e32 v160, v114
	v_add_f32_e32 v114, 1.0, v135
	v_max_f32_e32 v135, v169, v169
	v_max_f32_e32 v137, 0xc2a00000, v135
	v_max_f32_e32 v135, v171, v171
	v_max_f32_e32 v159, 0xc2a00000, v135
	v_mul_f32_e32 v135, 0xbfb8aa3b, v137
	v_exp_f32_e32 v135, v135
	v_mul_f32_e32 v155, 0xbfb8aa3b, v159
	v_rcp_f32_e32 v170, v114
	v_exp_f32_e32 v155, v155
	v_add_f32_e32 v114, 1.0, v135
	v_max_f32_e32 v135, v138, v138
	v_max_f32_e32 v138, 0xc2a00000, v135
	v_max_f32_e32 v135, v166, v166
	v_max_f32_e32 v166, 0xc2a00000, v135
	v_mul_f32_e32 v135, 0xbfb8aa3b, v138
	v_exp_f32_e32 v135, v135
	v_rcp_f32_e32 v161, v114
	v_add_f32_e32 v114, 1.0, v155
	v_mul_f32_e32 v155, 0xbfb8aa3b, v166
	v_exp_f32_e32 v155, v155
	v_rcp_f32_e32 v171, v114
	v_add_f32_e32 v114, 1.0, v135
	v_max_f32_e32 v135, v139, v139
	v_max_f32_e32 v139, 0xc2a00000, v135
	v_max_f32_e32 v135, v167, v167
	v_max_f32_e32 v167, 0xc2a00000, v135
	v_mul_f32_e32 v135, 0xbfb8aa3b, v139
	v_rcp_f32_e32 v178, v114
	v_add_f32_e32 v114, 1.0, v155
	v_exp_f32_e32 v135, v135
	v_mul_f32_e32 v155, 0xbfb8aa3b, v167
	v_exp_f32_e32 v155, v155
	v_rcp_f32_e32 v180, v114
	v_add_f32_e32 v114, 1.0, v135
	v_rcp_f32_e32 v179, v114
	v_add_f32_e32 v114, 1.0, v155
	v_rcp_f32_e32 v181, v114
	v_pk_mul_f32 v[168:169], v[136:137], v[160:161]
	v_pk_mul_f32 v[138:139], v[138:139], v[178:179]
	v_pk_mul_f32 v[170:171], v[158:159], v[170:171]
	v_pk_mul_f32 v[166:167], v[166:167], v[180:181]
.LBB0_360:
	v_or_b32_e32 v136, 32, v152
	v_ashrrev_i32_e32 v137, 31, v136
	v_lshlrev_b64 v[136:137], 12, v[136:137]
	v_mov_b32_e32 v135, v134
	v_lshl_add_u64 v[136:137], v[132:133], 0, v[136:137]
	v_cvt_pk_bf16_f32 v168, v168, v169
	v_cvt_pk_bf16_f32 v169, v138, v139
	v_cvt_pk_bf16_f32 v170, v170, v171
	v_cvt_pk_bf16_f32 v171, v166, v167
	v_mov_b32_e32 v158, v134
	v_mov_b32_e32 v159, v134
	ds_bpermute_b32 v238, v250, v168
	ds_bpermute_b32 v239, v250, v169
	ds_bpermute_b32 v240, v250, v170
	ds_bpermute_b32 v241, v250, v171
	ds_bpermute_b32 v242, v250, v136
	v_pk_mul_f32 v[138:139], v[88:89], v[158:159]
	v_pk_mul_f32 v[166:167], v[84:85], v[158:159]
	v_pk_mul_f32 v[168:169], v[86:87], v[134:135]
	s_and_b64 vcc, exec, s[40:41]
	v_pk_mul_f32 v[170:171], v[82:83], v[134:135]
	s_waitcnt lgkmcnt(0)
	v_subrev_u32_e32 v242, s82, v242
	global_store_dwordx4 v242, v[238:241], s[82:83] sc0 sc1
	s_cbranch_vccnz .LBB0_362
	v_max_f32_e32 v114, v168, v168
	v_max_f32_e32 v134, 0xc2a00000, v114
	v_max_f32_e32 v114, v170, v170
	v_max_f32_e32 v158, 0xc2a00000, v114
	v_mul_f32_e32 v114, 0xbfb8aa3b, v134
	v_exp_f32_e32 v114, v114
	v_mul_f32_e32 v135, 0xbfb8aa3b, v158
	v_exp_f32_e32 v135, v135
	v_max_f32_e32 v155, v171, v171
	v_add_f32_e32 v114, 1.0, v114
	v_rcp_f32_e32 v160, v114
	v_add_f32_e32 v114, 1.0, v135
	v_max_f32_e32 v135, v169, v169
	v_max_f32_e32 v135, 0xc2a00000, v135
	v_max_f32_e32 v159, 0xc2a00000, v155
	v_mul_f32_e32 v155, 0xbfb8aa3b, v135
	v_exp_f32_e32 v155, v155
	v_mul_f32_e32 v161, 0xbfb8aa3b, v159
	v_exp_f32_e32 v168, v161
	v_max_f32_e32 v138, v138, v138
	v_rcp_f32_e32 v170, v114
	v_add_f32_e32 v114, 1.0, v155
	v_max_f32_e32 v138, 0xc2a00000, v138
	v_max_f32_e32 v155, v166, v166
	v_max_f32_e32 v166, 0xc2a00000, v155
	v_mul_f32_e32 v155, 0xbfb8aa3b, v138
	v_exp_f32_e32 v155, v155
	v_rcp_f32_e32 v161, v114
	v_add_f32_e32 v114, 1.0, v168
	v_mul_f32_e32 v168, 0xbfb8aa3b, v166
	v_exp_f32_e32 v168, v168
	v_max_f32_e32 v139, v139, v139
	v_rcp_f32_e32 v171, v114
	v_add_f32_e32 v114, 1.0, v155
	v_max_f32_e32 v139, 0xc2a00000, v139
	v_max_f32_e32 v155, v167, v167
	v_max_f32_e32 v167, 0xc2a00000, v155
	v_mul_f32_e32 v155, 0xbfb8aa3b, v139
	v_rcp_f32_e32 v178, v114
	v_add_f32_e32 v114, 1.0, v168
	v_exp_f32_e32 v155, v155
	v_mul_f32_e32 v168, 0xbfb8aa3b, v167
	v_exp_f32_e32 v168, v168
	v_rcp_f32_e32 v180, v114
	v_add_f32_e32 v114, 1.0, v155
	v_rcp_f32_e32 v179, v114
	v_add_f32_e32 v114, 1.0, v168
	v_rcp_f32_e32 v181, v114
	v_pk_mul_f32 v[168:169], v[134:135], v[160:161]
	v_pk_mul_f32 v[138:139], v[138:139], v[178:179]
	v_pk_mul_f32 v[170:171], v[158:159], v[170:171]
	v_pk_mul_f32 v[166:167], v[166:167], v[180:181]
.LBB0_362:
	ds_read_b32 v134, v176 offset:192
	v_cvt_pk_bf16_f32 v168, v168, v169
	v_cvt_pk_bf16_f32 v169, v138, v139
	v_cvt_pk_bf16_f32 v170, v170, v171
	v_cvt_pk_bf16_f32 v171, v166, v167
	ds_bpermute_b32 v244, v250, v168
	ds_bpermute_b32 v245, v250, v169
	ds_bpermute_b32 v246, v250, v170
	ds_bpermute_b32 v247, v250, v171
	ds_bpermute_b32 v248, v250, v136
	s_waitcnt lgkmcnt(0)
	v_pk_mul_f32 v[138:139], v[80:81], v[134:135] op_sel_hi:[1,0]
	v_pk_mul_f32 v[166:167], v[76:77], v[134:135] op_sel_hi:[1,0]
	v_pk_mul_f32 v[168:169], v[78:79], v[134:135] op_sel_hi:[1,0]
	s_and_b64 vcc, exec, s[40:41]
	v_pk_mul_f32 v[170:171], v[74:75], v[134:135] op_sel_hi:[1,0]
	s_waitcnt lgkmcnt(0)
	v_subrev_u32_e32 v248, s82, v248
	global_store_dwordx4 v248, v[244:247], s[82:83] offset:64 sc0 sc1
	s_cbranch_vccnz .LBB0_364
	v_max_f32_e32 v114, v168, v168
	v_max_f32_e32 v136, 0xc2a00000, v114
	v_max_f32_e32 v114, v170, v170
	v_max_f32_e32 v158, 0xc2a00000, v114
	v_mul_f32_e32 v114, 0xbfb8aa3b, v136
	v_exp_f32_e32 v114, v114
	v_mul_f32_e32 v135, 0xbfb8aa3b, v158
	v_exp_f32_e32 v135, v135
	v_add_f32_e32 v114, 1.0, v114
	v_rcp_f32_e32 v160, v114
	v_add_f32_e32 v114, 1.0, v135
	v_max_f32_e32 v135, v169, v169
	v_max_f32_e32 v137, 0xc2a00000, v135
	v_max_f32_e32 v135, v171, v171
	v_max_f32_e32 v159, 0xc2a00000, v135
	v_mul_f32_e32 v135, 0xbfb8aa3b, v137
	v_exp_f32_e32 v135, v135
	v_mul_f32_e32 v155, 0xbfb8aa3b, v159
	v_rcp_f32_e32 v170, v114
	v_exp_f32_e32 v155, v155
	v_add_f32_e32 v114, 1.0, v135
	v_max_f32_e32 v135, v138, v138
	v_max_f32_e32 v138, 0xc2a00000, v135
	v_max_f32_e32 v135, v166, v166
	v_max_f32_e32 v166, 0xc2a00000, v135
	v_mul_f32_e32 v135, 0xbfb8aa3b, v138
	v_exp_f32_e32 v135, v135
	v_rcp_f32_e32 v161, v114
	v_add_f32_e32 v114, 1.0, v155
	v_mul_f32_e32 v155, 0xbfb8aa3b, v166
	v_exp_f32_e32 v155, v155
	v_rcp_f32_e32 v171, v114
	v_add_f32_e32 v114, 1.0, v135
	v_max_f32_e32 v135, v139, v139
	v_max_f32_e32 v139, 0xc2a00000, v135
	v_max_f32_e32 v135, v167, v167
	v_max_f32_e32 v167, 0xc2a00000, v135
	v_mul_f32_e32 v135, 0xbfb8aa3b, v139
	v_rcp_f32_e32 v178, v114
	v_add_f32_e32 v114, 1.0, v155
	v_exp_f32_e32 v135, v135
	v_mul_f32_e32 v155, 0xbfb8aa3b, v167
	v_exp_f32_e32 v155, v155
	v_rcp_f32_e32 v180, v114
	v_add_f32_e32 v114, 1.0, v135
	v_rcp_f32_e32 v179, v114
	v_add_f32_e32 v114, 1.0, v155
	v_rcp_f32_e32 v181, v114
	v_pk_mul_f32 v[168:169], v[136:137], v[160:161]
	v_pk_mul_f32 v[138:139], v[138:139], v[178:179]
	v_pk_mul_f32 v[170:171], v[158:159], v[170:171]
	v_pk_mul_f32 v[166:167], v[166:167], v[180:181]
.LBB0_364:
	v_or_b32_e32 v136, 48, v152
	v_ashrrev_i32_e32 v137, 31, v136
	v_lshlrev_b64 v[136:137], 12, v[136:137]
	v_mov_b32_e32 v135, v134
	v_lshl_add_u64 v[136:137], v[132:133], 0, v[136:137]
	v_cvt_pk_bf16_f32 v168, v168, v169
	v_cvt_pk_bf16_f32 v169, v138, v139
	v_cvt_pk_bf16_f32 v170, v170, v171
	v_cvt_pk_bf16_f32 v171, v166, v167
	v_mov_b32_e32 v158, v134
	v_mov_b32_e32 v159, v134
	ds_bpermute_b32 v232, v250, v168
	ds_bpermute_b32 v233, v250, v169
	ds_bpermute_b32 v234, v250, v170
	ds_bpermute_b32 v235, v250, v171
	ds_bpermute_b32 v236, v250, v136
	v_pk_mul_f32 v[138:139], v[72:73], v[158:159]
	v_pk_mul_f32 v[166:167], v[68:69], v[158:159]
	v_pk_mul_f32 v[168:169], v[70:71], v[134:135]
	s_and_b64 vcc, exec, s[40:41]
	v_pk_mul_f32 v[170:171], v[66:67], v[134:135]
	s_waitcnt lgkmcnt(0)
	v_subrev_u32_e32 v236, s82, v236
	global_store_dwordx4 v236, v[232:235], s[82:83] sc0 sc1
	s_cbranch_vccnz .LBB0_366
	v_max_f32_e32 v114, v168, v168
	v_max_f32_e32 v134, 0xc2a00000, v114
	v_max_f32_e32 v114, v170, v170
	v_max_f32_e32 v158, 0xc2a00000, v114
	v_mul_f32_e32 v114, 0xbfb8aa3b, v134
	v_exp_f32_e32 v114, v114
	v_mul_f32_e32 v135, 0xbfb8aa3b, v158
	v_exp_f32_e32 v135, v135
	v_max_f32_e32 v155, v171, v171
	v_add_f32_e32 v114, 1.0, v114
	v_rcp_f32_e32 v160, v114
	v_add_f32_e32 v114, 1.0, v135
	v_max_f32_e32 v135, v169, v169
	v_max_f32_e32 v135, 0xc2a00000, v135
	v_max_f32_e32 v159, 0xc2a00000, v155
	v_mul_f32_e32 v155, 0xbfb8aa3b, v135
	v_exp_f32_e32 v155, v155
	v_mul_f32_e32 v161, 0xbfb8aa3b, v159
	v_exp_f32_e32 v168, v161
	v_max_f32_e32 v138, v138, v138
	v_rcp_f32_e32 v170, v114
	v_add_f32_e32 v114, 1.0, v155
	v_max_f32_e32 v138, 0xc2a00000, v138
	v_max_f32_e32 v155, v166, v166
	v_max_f32_e32 v166, 0xc2a00000, v155
	v_mul_f32_e32 v155, 0xbfb8aa3b, v138
	v_exp_f32_e32 v155, v155
	v_rcp_f32_e32 v161, v114
	v_add_f32_e32 v114, 1.0, v168
	v_mul_f32_e32 v168, 0xbfb8aa3b, v166
	v_exp_f32_e32 v168, v168
	v_max_f32_e32 v139, v139, v139
	v_rcp_f32_e32 v171, v114
	v_add_f32_e32 v114, 1.0, v155
	v_max_f32_e32 v139, 0xc2a00000, v139
	v_max_f32_e32 v155, v167, v167
	v_max_f32_e32 v167, 0xc2a00000, v155
	v_mul_f32_e32 v155, 0xbfb8aa3b, v139
	v_rcp_f32_e32 v178, v114
	v_add_f32_e32 v114, 1.0, v168
	v_exp_f32_e32 v155, v155
	v_mul_f32_e32 v168, 0xbfb8aa3b, v167
	v_exp_f32_e32 v168, v168
	v_rcp_f32_e32 v180, v114
	v_add_f32_e32 v114, 1.0, v155
	v_rcp_f32_e32 v179, v114
	v_add_f32_e32 v114, 1.0, v168
	v_rcp_f32_e32 v181, v114
	v_pk_mul_f32 v[168:169], v[134:135], v[160:161]
	v_pk_mul_f32 v[138:139], v[138:139], v[178:179]
	v_pk_mul_f32 v[170:171], v[158:159], v[170:171]
	v_pk_mul_f32 v[166:167], v[166:167], v[180:181]
.LBB0_366:
	ds_read_b32 v134, v176 offset:512
	v_cvt_pk_bf16_f32 v168, v168, v169
	v_cvt_pk_bf16_f32 v169, v138, v139
	v_cvt_pk_bf16_f32 v170, v170, v171
	v_cvt_pk_bf16_f32 v171, v166, v167
	ds_bpermute_b32 v238, v250, v168
	ds_bpermute_b32 v239, v250, v169
	ds_bpermute_b32 v240, v250, v170
	ds_bpermute_b32 v241, v250, v171
	ds_bpermute_b32 v242, v250, v136
	s_waitcnt lgkmcnt(0)
	v_pk_mul_f32 v[138:139], v[64:65], v[134:135] op_sel_hi:[1,0]
	v_pk_mul_f32 v[166:167], v[60:61], v[134:135] op_sel_hi:[1,0]
	v_pk_mul_f32 v[168:169], v[62:63], v[134:135] op_sel_hi:[1,0]
	s_and_b64 vcc, exec, s[40:41]
	v_pk_mul_f32 v[170:171], v[58:59], v[134:135] op_sel_hi:[1,0]
	s_waitcnt lgkmcnt(0)
	v_subrev_u32_e32 v242, s82, v242
	global_store_dwordx4 v242, v[238:241], s[82:83] offset:64 sc0 sc1
	s_cbranch_vccnz .LBB0_368
	v_max_f32_e32 v114, v168, v168
	v_max_f32_e32 v136, 0xc2a00000, v114
	v_max_f32_e32 v114, v170, v170
	v_max_f32_e32 v158, 0xc2a00000, v114
	v_mul_f32_e32 v114, 0xbfb8aa3b, v136
	v_exp_f32_e32 v114, v114
	v_mul_f32_e32 v135, 0xbfb8aa3b, v158
	v_exp_f32_e32 v135, v135
	v_add_f32_e32 v114, 1.0, v114
	v_rcp_f32_e32 v160, v114
	v_add_f32_e32 v114, 1.0, v135
	v_max_f32_e32 v135, v169, v169
	v_max_f32_e32 v137, 0xc2a00000, v135
	v_max_f32_e32 v135, v171, v171
	v_max_f32_e32 v159, 0xc2a00000, v135
	v_mul_f32_e32 v135, 0xbfb8aa3b, v137
	v_exp_f32_e32 v135, v135
	v_mul_f32_e32 v155, 0xbfb8aa3b, v159
	v_rcp_f32_e32 v170, v114
	v_exp_f32_e32 v155, v155
	v_add_f32_e32 v114, 1.0, v135
	v_max_f32_e32 v135, v138, v138
	v_max_f32_e32 v138, 0xc2a00000, v135
	v_max_f32_e32 v135, v166, v166
	v_max_f32_e32 v166, 0xc2a00000, v135
	v_mul_f32_e32 v135, 0xbfb8aa3b, v138
	v_exp_f32_e32 v135, v135
	v_rcp_f32_e32 v161, v114
	v_add_f32_e32 v114, 1.0, v155
	v_mul_f32_e32 v155, 0xbfb8aa3b, v166
	v_exp_f32_e32 v155, v155
	v_rcp_f32_e32 v171, v114
	v_add_f32_e32 v114, 1.0, v135
	v_max_f32_e32 v135, v139, v139
	v_max_f32_e32 v139, 0xc2a00000, v135
	v_max_f32_e32 v135, v167, v167
	v_max_f32_e32 v167, 0xc2a00000, v135
	v_mul_f32_e32 v135, 0xbfb8aa3b, v139
	v_rcp_f32_e32 v178, v114
	v_add_f32_e32 v114, 1.0, v155
	v_exp_f32_e32 v135, v135
	v_mul_f32_e32 v155, 0xbfb8aa3b, v167
	v_exp_f32_e32 v155, v155
	v_rcp_f32_e32 v180, v114
	v_add_f32_e32 v114, 1.0, v135
	v_rcp_f32_e32 v179, v114
	v_add_f32_e32 v114, 1.0, v155
	v_rcp_f32_e32 v181, v114
	v_pk_mul_f32 v[168:169], v[136:137], v[160:161]
	v_pk_mul_f32 v[138:139], v[138:139], v[178:179]
	v_pk_mul_f32 v[170:171], v[158:159], v[170:171]
	v_pk_mul_f32 v[166:167], v[166:167], v[180:181]
.LBB0_368:
	v_lshlrev_b64 v[136:137], 12, v[152:153]
	v_lshl_add_u64 v[136:137], v[132:133], 0, v[136:137]
	s_mov_b32 s14, 0x80000
	v_cvt_pk_bf16_f32 v168, v168, v169
	v_cvt_pk_bf16_f32 v169, v138, v139
	v_add_co_u32_e32 v138, vcc, s14, v136
	v_mov_b32_e32 v135, v134
	v_cvt_pk_bf16_f32 v170, v170, v171
	v_cvt_pk_bf16_f32 v171, v166, v167
	s_nop 0
	v_addc_co_u32_e32 v139, vcc, 0, v137, vcc
	v_mov_b32_e32 v158, v134
	v_mov_b32_e32 v159, v134
	ds_bpermute_b32 v244, v250, v168
	ds_bpermute_b32 v245, v250, v169
	ds_bpermute_b32 v246, v250, v170
	ds_bpermute_b32 v247, v250, v171
	ds_bpermute_b32 v248, v250, v138
	v_pk_mul_f32 v[138:139], v[56:57], v[158:159]
	v_pk_mul_f32 v[166:167], v[52:53], v[158:159]
	v_pk_mul_f32 v[168:169], v[54:55], v[134:135]
	s_and_b64 vcc, exec, s[40:41]
	v_pk_mul_f32 v[170:171], v[50:51], v[134:135]
	s_waitcnt lgkmcnt(0)
	v_subrev_u32_e32 v248, s82, v248
	global_store_dwordx4 v248, v[244:247], s[82:83] sc0 sc1
	s_cbranch_vccnz .LBB0_370
	v_max_f32_e32 v114, v168, v168
	v_max_f32_e32 v134, 0xc2a00000, v114
	v_max_f32_e32 v114, v170, v170
	v_max_f32_e32 v158, 0xc2a00000, v114
	v_mul_f32_e32 v114, 0xbfb8aa3b, v134
	v_exp_f32_e32 v114, v114
	v_mul_f32_e32 v135, 0xbfb8aa3b, v158
	v_exp_f32_e32 v135, v135
	v_max_f32_e32 v155, v171, v171
	v_add_f32_e32 v114, 1.0, v114
	v_rcp_f32_e32 v160, v114
	v_add_f32_e32 v114, 1.0, v135
	v_max_f32_e32 v135, v169, v169
	v_max_f32_e32 v135, 0xc2a00000, v135
	v_max_f32_e32 v159, 0xc2a00000, v155
	v_mul_f32_e32 v155, 0xbfb8aa3b, v135
	v_exp_f32_e32 v155, v155
	v_mul_f32_e32 v161, 0xbfb8aa3b, v159
	v_exp_f32_e32 v168, v161
	v_max_f32_e32 v138, v138, v138
	v_rcp_f32_e32 v170, v114
	v_add_f32_e32 v114, 1.0, v155
	v_max_f32_e32 v138, 0xc2a00000, v138
	v_max_f32_e32 v155, v166, v166
	v_max_f32_e32 v166, 0xc2a00000, v155
	v_mul_f32_e32 v155, 0xbfb8aa3b, v138
	v_exp_f32_e32 v155, v155
	v_rcp_f32_e32 v161, v114
	v_add_f32_e32 v114, 1.0, v168
	v_mul_f32_e32 v168, 0xbfb8aa3b, v166
	v_exp_f32_e32 v168, v168
	v_max_f32_e32 v139, v139, v139
	v_rcp_f32_e32 v171, v114
	v_add_f32_e32 v114, 1.0, v155
	v_max_f32_e32 v139, 0xc2a00000, v139
	v_max_f32_e32 v155, v167, v167
	v_max_f32_e32 v167, 0xc2a00000, v155
	v_mul_f32_e32 v155, 0xbfb8aa3b, v139
	v_rcp_f32_e32 v178, v114
	v_add_f32_e32 v114, 1.0, v168
	v_exp_f32_e32 v155, v155
	v_mul_f32_e32 v168, 0xbfb8aa3b, v167
	v_exp_f32_e32 v168, v168
	v_rcp_f32_e32 v180, v114
	v_add_f32_e32 v114, 1.0, v155
	v_rcp_f32_e32 v179, v114
	v_add_f32_e32 v114, 1.0, v168
	v_rcp_f32_e32 v181, v114
	v_pk_mul_f32 v[168:169], v[134:135], v[160:161]
	v_pk_mul_f32 v[138:139], v[138:139], v[178:179]
	v_pk_mul_f32 v[170:171], v[158:159], v[170:171]
	v_pk_mul_f32 v[166:167], v[166:167], v[180:181]
.LBB0_370:
	ds_read_b32 v134, v176 offset:576
	s_mov_b64 s[14:15], 0x80000
	v_lshl_add_u64 v[158:159], v[136:137], 0, s[14:15]
	v_cvt_pk_bf16_f32 v137, v138, v139
	v_cvt_pk_bf16_f32 v138, v170, v171
	v_cvt_pk_bf16_f32 v139, v166, v167
	v_cvt_pk_bf16_f32 v136, v168, v169
	ds_bpermute_b32 v232, v250, v136
	ds_bpermute_b32 v233, v250, v137
	ds_bpermute_b32 v234, v250, v138
	ds_bpermute_b32 v235, v250, v139
	ds_bpermute_b32 v236, v250, v158
	s_waitcnt lgkmcnt(0)
	v_pk_mul_f32 v[168:169], v[46:47], v[134:135] op_sel_hi:[1,0]
	v_pk_mul_f32 v[166:167], v[44:45], v[134:135] op_sel_hi:[1,0]
	v_pk_mul_f32 v[138:139], v[48:49], v[134:135] op_sel_hi:[1,0]
	s_and_b64 vcc, exec, s[40:41]
	v_pk_mul_f32 v[170:171], v[42:43], v[134:135] op_sel_hi:[1,0]
	s_waitcnt lgkmcnt(0)
	v_subrev_u32_e32 v236, s82, v236
	global_store_dwordx4 v236, v[232:235], s[82:83] offset:64 sc0 sc1
	s_cbranch_vccnz .LBB0_372
	v_max_f32_e32 v114, v168, v168
	v_max_f32_e32 v136, 0xc2a00000, v114
	v_max_f32_e32 v114, v170, v170
	v_max_f32_e32 v158, 0xc2a00000, v114
	v_mul_f32_e32 v114, 0xbfb8aa3b, v136
	v_exp_f32_e32 v114, v114
	v_mul_f32_e32 v135, 0xbfb8aa3b, v158
	v_exp_f32_e32 v135, v135
	v_add_f32_e32 v114, 1.0, v114
	v_rcp_f32_e32 v160, v114
	v_add_f32_e32 v114, 1.0, v135
	v_max_f32_e32 v135, v169, v169
	v_max_f32_e32 v137, 0xc2a00000, v135
	v_max_f32_e32 v135, v171, v171
	v_max_f32_e32 v159, 0xc2a00000, v135
	v_mul_f32_e32 v135, 0xbfb8aa3b, v137
	v_exp_f32_e32 v135, v135
	v_mul_f32_e32 v155, 0xbfb8aa3b, v159
	v_rcp_f32_e32 v170, v114
	v_exp_f32_e32 v155, v155
	v_add_f32_e32 v114, 1.0, v135
	v_max_f32_e32 v135, v138, v138
	v_max_f32_e32 v138, 0xc2a00000, v135
	v_max_f32_e32 v135, v166, v166
	v_max_f32_e32 v166, 0xc2a00000, v135
	v_mul_f32_e32 v135, 0xbfb8aa3b, v138
	v_exp_f32_e32 v135, v135
	v_rcp_f32_e32 v161, v114
	v_add_f32_e32 v114, 1.0, v155
	v_mul_f32_e32 v155, 0xbfb8aa3b, v166
	v_exp_f32_e32 v155, v155
	v_rcp_f32_e32 v171, v114
	v_add_f32_e32 v114, 1.0, v135
	v_max_f32_e32 v135, v139, v139
	v_max_f32_e32 v139, 0xc2a00000, v135
	v_max_f32_e32 v135, v167, v167
	v_max_f32_e32 v167, 0xc2a00000, v135
	v_mul_f32_e32 v135, 0xbfb8aa3b, v139
	v_rcp_f32_e32 v178, v114
	v_add_f32_e32 v114, 1.0, v155
	v_exp_f32_e32 v135, v135
	v_mul_f32_e32 v155, 0xbfb8aa3b, v167
	v_exp_f32_e32 v155, v155
	v_rcp_f32_e32 v180, v114
	v_add_f32_e32 v114, 1.0, v135
	v_rcp_f32_e32 v179, v114
	v_add_f32_e32 v114, 1.0, v155
	v_rcp_f32_e32 v181, v114
	v_pk_mul_f32 v[168:169], v[136:137], v[160:161]
	v_pk_mul_f32 v[138:139], v[138:139], v[178:179]
	v_pk_mul_f32 v[170:171], v[158:159], v[170:171]
	v_pk_mul_f32 v[166:167], v[166:167], v[180:181]
.LBB0_372:
	v_lshlrev_b64 v[136:137], 12, v[152:153]
	v_lshl_add_u64 v[136:137], v[132:133], 0, v[136:137]
	s_mov_b32 s14, 0x90000
	v_cvt_pk_bf16_f32 v168, v168, v169
	v_cvt_pk_bf16_f32 v169, v138, v139
	v_add_co_u32_e32 v138, vcc, s14, v136
	v_mov_b32_e32 v135, v134
	v_cvt_pk_bf16_f32 v170, v170, v171
	v_cvt_pk_bf16_f32 v171, v166, v167
	s_nop 0
	v_addc_co_u32_e32 v139, vcc, 0, v137, vcc
	v_mov_b32_e32 v158, v134
	v_mov_b32_e32 v159, v134
	ds_bpermute_b32 v238, v250, v168
	ds_bpermute_b32 v239, v250, v169
	ds_bpermute_b32 v240, v250, v170
	ds_bpermute_b32 v241, v250, v171
	ds_bpermute_b32 v242, v250, v138
	v_pk_mul_f32 v[138:139], v[40:41], v[158:159]
	v_pk_mul_f32 v[166:167], v[36:37], v[158:159]
	v_pk_mul_f32 v[168:169], v[38:39], v[134:135]
	s_and_b64 vcc, exec, s[40:41]
	v_pk_mul_f32 v[170:171], v[34:35], v[134:135]
	s_waitcnt lgkmcnt(0)
	v_subrev_u32_e32 v242, s82, v242
	global_store_dwordx4 v242, v[238:241], s[82:83] sc0 sc1
	s_cbranch_vccnz .LBB0_374
	v_max_f32_e32 v114, v168, v168
	v_max_f32_e32 v134, 0xc2a00000, v114
	v_max_f32_e32 v114, v170, v170
	v_max_f32_e32 v158, 0xc2a00000, v114
	v_mul_f32_e32 v114, 0xbfb8aa3b, v134
	v_exp_f32_e32 v114, v114
	v_mul_f32_e32 v135, 0xbfb8aa3b, v158
	v_exp_f32_e32 v135, v135
	v_max_f32_e32 v155, v171, v171
	v_add_f32_e32 v114, 1.0, v114
	v_rcp_f32_e32 v160, v114
	v_add_f32_e32 v114, 1.0, v135
	v_max_f32_e32 v135, v169, v169
	v_max_f32_e32 v135, 0xc2a00000, v135
	v_max_f32_e32 v159, 0xc2a00000, v155
	v_mul_f32_e32 v155, 0xbfb8aa3b, v135
	v_exp_f32_e32 v155, v155
	v_mul_f32_e32 v161, 0xbfb8aa3b, v159
	v_exp_f32_e32 v168, v161
	v_max_f32_e32 v138, v138, v138
	v_rcp_f32_e32 v170, v114
	v_add_f32_e32 v114, 1.0, v155
	v_max_f32_e32 v138, 0xc2a00000, v138
	v_max_f32_e32 v155, v166, v166
	v_max_f32_e32 v166, 0xc2a00000, v155
	v_mul_f32_e32 v155, 0xbfb8aa3b, v138
	v_exp_f32_e32 v155, v155
	v_rcp_f32_e32 v161, v114
	v_add_f32_e32 v114, 1.0, v168
	v_mul_f32_e32 v168, 0xbfb8aa3b, v166
	v_exp_f32_e32 v168, v168
	v_max_f32_e32 v139, v139, v139
	v_rcp_f32_e32 v171, v114
	v_add_f32_e32 v114, 1.0, v155
	v_max_f32_e32 v139, 0xc2a00000, v139
	v_max_f32_e32 v155, v167, v167
	v_max_f32_e32 v167, 0xc2a00000, v155
	v_mul_f32_e32 v155, 0xbfb8aa3b, v139
	v_rcp_f32_e32 v178, v114
	v_add_f32_e32 v114, 1.0, v168
	v_exp_f32_e32 v155, v155
	v_mul_f32_e32 v168, 0xbfb8aa3b, v167
	v_exp_f32_e32 v168, v168
	v_rcp_f32_e32 v180, v114
	v_add_f32_e32 v114, 1.0, v155
	v_rcp_f32_e32 v179, v114
	v_add_f32_e32 v114, 1.0, v168
	v_rcp_f32_e32 v181, v114
	v_pk_mul_f32 v[168:169], v[134:135], v[160:161]
	v_pk_mul_f32 v[138:139], v[138:139], v[178:179]
	v_pk_mul_f32 v[170:171], v[158:159], v[170:171]
	v_pk_mul_f32 v[166:167], v[166:167], v[180:181]
.LBB0_374:
	ds_read_b32 v134, v176 offset:640
	s_mov_b64 s[14:15], 0x90000
	v_lshl_add_u64 v[158:159], v[136:137], 0, s[14:15]
	v_cvt_pk_bf16_f32 v137, v138, v139
	v_cvt_pk_bf16_f32 v138, v170, v171
	v_cvt_pk_bf16_f32 v139, v166, v167
	v_cvt_pk_bf16_f32 v136, v168, v169
	ds_bpermute_b32 v244, v250, v136
	ds_bpermute_b32 v245, v250, v137
	ds_bpermute_b32 v246, v250, v138
	ds_bpermute_b32 v247, v250, v139
	ds_bpermute_b32 v248, v250, v158
	s_waitcnt lgkmcnt(0)
	v_pk_mul_f32 v[168:169], v[30:31], v[134:135] op_sel_hi:[1,0]
	v_pk_mul_f32 v[166:167], v[28:29], v[134:135] op_sel_hi:[1,0]
	v_pk_mul_f32 v[138:139], v[32:33], v[134:135] op_sel_hi:[1,0]
	s_and_b64 vcc, exec, s[40:41]
	v_pk_mul_f32 v[170:171], v[26:27], v[134:135] op_sel_hi:[1,0]
	s_waitcnt lgkmcnt(0)
	v_subrev_u32_e32 v248, s82, v248
	global_store_dwordx4 v248, v[244:247], s[82:83] offset:64 sc0 sc1
	s_cbranch_vccnz .LBB0_376
	v_max_f32_e32 v114, v168, v168
	v_max_f32_e32 v136, 0xc2a00000, v114
	v_max_f32_e32 v114, v170, v170
	v_max_f32_e32 v158, 0xc2a00000, v114
	v_mul_f32_e32 v114, 0xbfb8aa3b, v136
	v_exp_f32_e32 v114, v114
	v_mul_f32_e32 v135, 0xbfb8aa3b, v158
	v_exp_f32_e32 v135, v135
	v_add_f32_e32 v114, 1.0, v114
	v_rcp_f32_e32 v160, v114
	v_add_f32_e32 v114, 1.0, v135
	v_max_f32_e32 v135, v169, v169
	v_max_f32_e32 v137, 0xc2a00000, v135
	v_max_f32_e32 v135, v171, v171
	v_max_f32_e32 v159, 0xc2a00000, v135
	v_mul_f32_e32 v135, 0xbfb8aa3b, v137
	v_exp_f32_e32 v135, v135
	v_mul_f32_e32 v155, 0xbfb8aa3b, v159
	v_rcp_f32_e32 v170, v114
	v_exp_f32_e32 v155, v155
	v_add_f32_e32 v114, 1.0, v135
	v_max_f32_e32 v135, v138, v138
	v_max_f32_e32 v138, 0xc2a00000, v135
	v_max_f32_e32 v135, v166, v166
	v_max_f32_e32 v166, 0xc2a00000, v135
	v_mul_f32_e32 v135, 0xbfb8aa3b, v138
	v_exp_f32_e32 v135, v135
	v_rcp_f32_e32 v161, v114
	v_add_f32_e32 v114, 1.0, v155
	v_mul_f32_e32 v155, 0xbfb8aa3b, v166
	v_exp_f32_e32 v155, v155
	v_rcp_f32_e32 v171, v114
	v_add_f32_e32 v114, 1.0, v135
	v_max_f32_e32 v135, v139, v139
	v_max_f32_e32 v139, 0xc2a00000, v135
	v_max_f32_e32 v135, v167, v167
	v_max_f32_e32 v167, 0xc2a00000, v135
	v_mul_f32_e32 v135, 0xbfb8aa3b, v139
	v_rcp_f32_e32 v178, v114
	v_add_f32_e32 v114, 1.0, v155
	v_exp_f32_e32 v135, v135
	v_mul_f32_e32 v155, 0xbfb8aa3b, v167
	v_exp_f32_e32 v155, v155
	v_rcp_f32_e32 v180, v114
	v_add_f32_e32 v114, 1.0, v135
	v_rcp_f32_e32 v179, v114
	v_add_f32_e32 v114, 1.0, v155
	v_rcp_f32_e32 v181, v114
	v_pk_mul_f32 v[168:169], v[136:137], v[160:161]
	v_pk_mul_f32 v[138:139], v[138:139], v[178:179]
	v_pk_mul_f32 v[170:171], v[158:159], v[170:171]
	v_pk_mul_f32 v[166:167], v[166:167], v[180:181]
.LBB0_376:
	v_lshlrev_b64 v[136:137], 12, v[152:153]
	v_lshl_add_u64 v[136:137], v[132:133], 0, v[136:137]
	s_mov_b32 s14, 0xa0000
	v_cvt_pk_bf16_f32 v168, v168, v169
	v_cvt_pk_bf16_f32 v169, v138, v139
	v_add_co_u32_e32 v138, vcc, s14, v136
	v_mov_b32_e32 v135, v134
	v_cvt_pk_bf16_f32 v170, v170, v171
	v_cvt_pk_bf16_f32 v171, v166, v167
	s_nop 0
	v_addc_co_u32_e32 v139, vcc, 0, v137, vcc
	v_mov_b32_e32 v158, v134
	v_mov_b32_e32 v159, v134
	ds_bpermute_b32 v232, v250, v168
	ds_bpermute_b32 v233, v250, v169
	ds_bpermute_b32 v234, v250, v170
	ds_bpermute_b32 v235, v250, v171
	ds_bpermute_b32 v236, v250, v138
	v_pk_mul_f32 v[138:139], v[24:25], v[158:159]
	v_pk_mul_f32 v[166:167], v[20:21], v[158:159]
	v_pk_mul_f32 v[168:169], v[22:23], v[134:135]
	s_and_b64 vcc, exec, s[40:41]
	v_pk_mul_f32 v[170:171], v[18:19], v[134:135]
	s_waitcnt lgkmcnt(0)
	v_subrev_u32_e32 v236, s82, v236
	global_store_dwordx4 v236, v[232:235], s[82:83] sc0 sc1
	s_cbranch_vccnz .LBB0_378
	v_max_f32_e32 v114, v168, v168
	v_max_f32_e32 v134, 0xc2a00000, v114
	v_max_f32_e32 v114, v170, v170
	v_max_f32_e32 v158, 0xc2a00000, v114
	v_mul_f32_e32 v114, 0xbfb8aa3b, v134
	v_exp_f32_e32 v114, v114
	v_mul_f32_e32 v135, 0xbfb8aa3b, v158
	v_exp_f32_e32 v135, v135
	v_max_f32_e32 v155, v171, v171
	v_add_f32_e32 v114, 1.0, v114
	v_rcp_f32_e32 v160, v114
	v_add_f32_e32 v114, 1.0, v135
	v_max_f32_e32 v135, v169, v169
	v_max_f32_e32 v135, 0xc2a00000, v135
	v_max_f32_e32 v159, 0xc2a00000, v155
	v_mul_f32_e32 v155, 0xbfb8aa3b, v135
	v_exp_f32_e32 v155, v155
	v_mul_f32_e32 v161, 0xbfb8aa3b, v159
	v_exp_f32_e32 v168, v161
	v_max_f32_e32 v138, v138, v138
	v_rcp_f32_e32 v170, v114
	v_add_f32_e32 v114, 1.0, v155
	v_max_f32_e32 v138, 0xc2a00000, v138
	v_max_f32_e32 v155, v166, v166
	v_max_f32_e32 v166, 0xc2a00000, v155
	v_mul_f32_e32 v155, 0xbfb8aa3b, v138
	v_exp_f32_e32 v155, v155
	v_rcp_f32_e32 v161, v114
	v_add_f32_e32 v114, 1.0, v168
	v_mul_f32_e32 v168, 0xbfb8aa3b, v166
	v_exp_f32_e32 v168, v168
	v_max_f32_e32 v139, v139, v139
	v_rcp_f32_e32 v171, v114
	v_add_f32_e32 v114, 1.0, v155
	v_max_f32_e32 v139, 0xc2a00000, v139
	v_max_f32_e32 v155, v167, v167
	v_max_f32_e32 v167, 0xc2a00000, v155
	v_mul_f32_e32 v155, 0xbfb8aa3b, v139
	v_rcp_f32_e32 v178, v114
	v_add_f32_e32 v114, 1.0, v168
	v_exp_f32_e32 v155, v155
	v_mul_f32_e32 v168, 0xbfb8aa3b, v167
	v_exp_f32_e32 v168, v168
	v_rcp_f32_e32 v180, v114
	v_add_f32_e32 v114, 1.0, v155
	v_rcp_f32_e32 v179, v114
	v_add_f32_e32 v114, 1.0, v168
	v_rcp_f32_e32 v181, v114
	v_pk_mul_f32 v[168:169], v[134:135], v[160:161]
	v_pk_mul_f32 v[138:139], v[138:139], v[178:179]
	v_pk_mul_f32 v[170:171], v[158:159], v[170:171]
	v_pk_mul_f32 v[166:167], v[166:167], v[180:181]
.LBB0_378:
	ds_read_b32 v134, v176 offset:704
	s_mov_b64 s[14:15], 0xa0000
	v_lshl_add_u64 v[158:159], v[136:137], 0, s[14:15]
	v_cvt_pk_bf16_f32 v136, v168, v169
	v_cvt_pk_bf16_f32 v137, v138, v139
	v_cvt_pk_bf16_f32 v138, v170, v171
	v_cvt_pk_bf16_f32 v139, v166, v167
	ds_bpermute_b32 v238, v250, v136
	ds_bpermute_b32 v239, v250, v137
	ds_bpermute_b32 v240, v250, v138
	ds_bpermute_b32 v241, v250, v139
	ds_bpermute_b32 v242, v250, v158
	s_waitcnt lgkmcnt(0)
	v_pk_mul_f32 v[166:167], v[14:15], v[134:135] op_sel_hi:[1,0]
	s_and_b64 vcc, exec, s[40:41]
	v_pk_mul_f32 v[136:137], v[16:17], v[134:135] op_sel_hi:[1,0]
	v_pk_mul_f32 v[138:139], v[12:13], v[134:135] op_sel_hi:[1,0]
	v_pk_mul_f32 v[168:169], v[10:11], v[134:135] op_sel_hi:[1,0]
	s_waitcnt lgkmcnt(0)
	v_subrev_u32_e32 v242, s82, v242
	global_store_dwordx4 v242, v[238:241], s[82:83] offset:64 sc0 sc1
	s_cbranch_vccnz .LBB0_380
	v_max_f32_e32 v114, v166, v166
	v_max_f32_e32 v158, 0xc2a00000, v114
	v_max_f32_e32 v114, v168, v168
	v_max_f32_e32 v160, 0xc2a00000, v114
	v_mul_f32_e32 v114, 0xbfb8aa3b, v158
	v_exp_f32_e32 v114, v114
	v_mul_f32_e32 v135, 0xbfb8aa3b, v160
	v_exp_f32_e32 v135, v135
	v_add_f32_e32 v114, 1.0, v114
	v_rcp_f32_e32 v166, v114
	v_add_f32_e32 v114, 1.0, v135
	v_max_f32_e32 v135, v167, v167
	v_max_f32_e32 v159, 0xc2a00000, v135
	v_max_f32_e32 v135, v169, v169
	v_max_f32_e32 v161, 0xc2a00000, v135
	v_mul_f32_e32 v135, 0xbfb8aa3b, v159
	v_exp_f32_e32 v135, v135
	v_mul_f32_e32 v155, 0xbfb8aa3b, v161
	v_rcp_f32_e32 v168, v114
	v_exp_f32_e32 v155, v155
	v_add_f32_e32 v114, 1.0, v135
	v_max_f32_e32 v135, v136, v136
	v_max_f32_e32 v136, 0xc2a00000, v135
	v_max_f32_e32 v135, v138, v138
	v_max_f32_e32 v138, 0xc2a00000, v135
	v_mul_f32_e32 v135, 0xbfb8aa3b, v136
	v_exp_f32_e32 v135, v135
	v_rcp_f32_e32 v167, v114
	v_add_f32_e32 v114, 1.0, v155
	v_mul_f32_e32 v155, 0xbfb8aa3b, v138
	v_exp_f32_e32 v155, v155
	v_rcp_f32_e32 v169, v114
	v_add_f32_e32 v114, 1.0, v135
	v_max_f32_e32 v135, v137, v137
	v_max_f32_e32 v137, 0xc2a00000, v135
	v_max_f32_e32 v135, v139, v139
	v_max_f32_e32 v139, 0xc2a00000, v135
	v_mul_f32_e32 v135, 0xbfb8aa3b, v137
	v_rcp_f32_e32 v170, v114
	v_add_f32_e32 v114, 1.0, v155
	v_exp_f32_e32 v135, v135
	v_mul_f32_e32 v155, 0xbfb8aa3b, v139
	v_exp_f32_e32 v155, v155
	v_rcp_f32_e32 v178, v114
	v_add_f32_e32 v114, 1.0, v135
	v_rcp_f32_e32 v171, v114
	v_add_f32_e32 v114, 1.0, v155
	v_rcp_f32_e32 v179, v114
	v_pk_mul_f32 v[166:167], v[158:159], v[166:167]
	v_pk_mul_f32 v[136:137], v[136:137], v[170:171]
	v_pk_mul_f32 v[168:169], v[160:161], v[168:169]
	v_pk_mul_f32 v[138:139], v[138:139], v[178:179]
.LBB0_380:
	v_lshlrev_b64 v[158:159], 12, v[152:153]
	v_lshl_add_u64 v[132:133], v[132:133], 0, v[158:159]
	s_mov_b32 s14, 0xb0000
	v_cvt_pk_bf16_f32 v166, v166, v167
	v_cvt_pk_bf16_f32 v167, v136, v137
	v_add_co_u32_e32 v136, vcc, s14, v132
	v_mov_b32_e32 v135, v134
	s_nop 0
	v_addc_co_u32_e32 v137, vcc, 0, v133, vcc
	v_cvt_pk_bf16_f32 v168, v168, v169
	v_cvt_pk_bf16_f32 v169, v138, v139
	ds_bpermute_b32 v244, v250, v166
	ds_bpermute_b32 v245, v250, v167
	ds_bpermute_b32 v246, v250, v168
	ds_bpermute_b32 v247, v250, v169
	ds_bpermute_b32 v248, v250, v136
	v_mov_b32_e32 v136, v134
	v_mov_b32_e32 v137, v134
	v_pk_mul_f32 v[138:139], v[8:9], v[136:137]
	v_pk_mul_f32 v[168:169], v[6:7], v[134:135]
	v_pk_mul_f32 v[166:167], v[4:5], v[136:137]
	s_and_b64 vcc, exec, s[40:41]
	v_pk_mul_f32 v[134:135], v[2:3], v[134:135]
	s_waitcnt lgkmcnt(0)
	v_subrev_u32_e32 v248, s82, v248
	global_store_dwordx4 v248, v[244:247], s[82:83] sc0 sc1
	s_cbranch_vccnz .LBB0_382
	v_max_f32_e32 v114, v168, v168
	v_max_f32_e32 v136, 0xc2a00000, v114
	v_max_f32_e32 v114, v134, v134
	v_max_f32_e32 v134, 0xc2a00000, v114
	v_mul_f32_e32 v114, 0xbfb8aa3b, v136
	v_exp_f32_e32 v114, v114
	v_mul_f32_e32 v137, 0xbfb8aa3b, v134
	v_exp_f32_e32 v137, v137
	v_max_f32_e32 v135, v135, v135
	v_add_f32_e32 v114, 1.0, v114
	v_rcp_f32_e32 v158, v114
	v_add_f32_e32 v114, 1.0, v137
	v_max_f32_e32 v137, v169, v169
	v_max_f32_e32 v137, 0xc2a00000, v137
	v_mul_f32_e32 v153, 0xbfb8aa3b, v137
	v_exp_f32_e32 v153, v153
	v_max_f32_e32 v135, 0xc2a00000, v135
	v_mul_f32_e32 v155, 0xbfb8aa3b, v135
	v_exp_f32_e32 v155, v155
	v_max_f32_e32 v138, v138, v138
	v_rcp_f32_e32 v160, v114
	v_add_f32_e32 v114, 1.0, v153
	v_max_f32_e32 v138, 0xc2a00000, v138
	v_max_f32_e32 v153, v166, v166
	v_max_f32_e32 v166, 0xc2a00000, v153
	v_mul_f32_e32 v153, 0xbfb8aa3b, v138
	v_exp_f32_e32 v153, v153
	v_rcp_f32_e32 v159, v114
	v_add_f32_e32 v114, 1.0, v155
	v_mul_f32_e32 v155, 0xbfb8aa3b, v166
	v_exp_f32_e32 v155, v155
	v_max_f32_e32 v139, v139, v139
	v_rcp_f32_e32 v161, v114
	v_add_f32_e32 v114, 1.0, v153
	v_max_f32_e32 v139, 0xc2a00000, v139
	v_max_f32_e32 v153, v167, v167
	v_max_f32_e32 v167, 0xc2a00000, v153
	v_mul_f32_e32 v153, 0xbfb8aa3b, v139
	v_rcp_f32_e32 v170, v114
	v_add_f32_e32 v114, 1.0, v155
	v_exp_f32_e32 v153, v153
	v_mul_f32_e32 v155, 0xbfb8aa3b, v167
	v_exp_f32_e32 v155, v155
	v_rcp_f32_e32 v178, v114
	v_add_f32_e32 v114, 1.0, v153
	v_rcp_f32_e32 v171, v114
	v_add_f32_e32 v114, 1.0, v155
	v_rcp_f32_e32 v179, v114
	v_pk_mul_f32 v[168:169], v[136:137], v[158:159]
	v_pk_mul_f32 v[138:139], v[138:139], v[170:171]
	v_pk_mul_f32 v[134:135], v[134:135], v[160:161]
	v_pk_mul_f32 v[166:167], v[166:167], v[178:179]

.LBB0_383:
	s_andn2_b64 vcc, exec, s[38:39]
	s_mov_b64 s[28:29], -1
	ds_bpermute_b32 v232, v250, v132
	ds_bpermute_b32 v233, v250, v133
	ds_bpermute_b32 v234, v250, v134
	ds_bpermute_b32 v235, v250, v135
	ds_bpermute_b32 v236, v250, v136
	s_waitcnt lgkmcnt(0)
	v_subrev_u32_e32 v236, s82, v236
	global_store_dwordx4 v236, v[232:235], s[82:83] offset:64 sc0 sc1
	s_cbranch_vccnz .LBB0_338
	s_branch .LBB0_386
.LBB0_384:
	s_and_b64 vcc, exec, s[40:41]
	s_cbranch_vccz .LBB0_383
	v_lshlrev_b32_e32 v155, 2, v177
	global_load_dwordx4 v[136:139], v155, s[44:45]
	global_load_dwordx4 v[132:135], v155, s[44:45] offset:16
	s_waitcnt lgkmcnt(0)
	v_mul_f32_e32 v160, v128, v154
	v_mul_f32_e32 v161, v129, v154
	v_mul_f32_e32 v166, v130, v154
	v_mul_f32_e32 v167, v131, v154
	v_mul_f32_e32 v168, v124, v154
	v_mul_f32_e32 v169, v125, v154
	v_mul_f32_e32 v170, v126, v154
	v_mul_f32_e32 v171, v127, v154
	global_load_dwordx4 v[124:127], v155, s[44:45] offset:144
	global_load_dwordx4 v[128:131], v155, s[44:45] offset:128
	v_ashrrev_i32_e32 v153, 31, v152
	v_lshlrev_b64 v[158:159], 12, v[152:153]
	v_max_f32_e32 v153, 0xc2a00000, v160
	v_max_f32_e32 v155, 0xc2a00000, v161
	v_max_f32_e32 v160, 0xc2a00000, v166
	v_max_f32_e32 v161, 0xc2a00000, v167
	v_max_f32_e32 v166, 0xc2a00000, v168
	v_max_f32_e32 v167, 0xc2a00000, v169
	v_max_f32_e32 v168, 0xc2a00000, v170
	v_max_f32_e32 v169, 0xc2a00000, v171
	v_mul_f32_e32 v153, 0xbfb8aa3b, v153
	v_mul_f32_e32 v155, 0xbfb8aa3b, v155
	v_mul_f32_e32 v168, 0xbfb8aa3b, v168
	v_mul_f32_e32 v169, 0xbfb8aa3b, v169
	v_exp_f32_e32 v153, v153
	v_exp_f32_e32 v155, v155
	v_mul_f32_e32 v160, 0xbfb8aa3b, v160
	v_mul_f32_e32 v161, 0xbfb8aa3b, v161
	v_exp_f32_e32 v168, v168
	v_exp_f32_e32 v169, v169
	v_exp_f32_e32 v160, v160
	v_exp_f32_e32 v161, v161
	v_mul_f32_e32 v120, v120, v154
	v_max_f32_e32 v120, 0xc2a00000, v120
	v_add_f32_e32 v153, 1.0, v153
	v_add_f32_e32 v155, 1.0, v155
	v_mul_f32_e32 v121, v121, v154
	v_lshlrev_b32_e32 v114, 1, v177
	v_mul_f32_e32 v166, 0xbfb8aa3b, v166
	v_mul_f32_e32 v167, 0xbfb8aa3b, v167
	v_lshl_add_u64 v[158:159], s[42:43], 0, v[158:159]
	v_add_f32_e32 v168, 1.0, v168
	v_add_f32_e32 v169, 1.0, v169
	v_rcp_f32_e32 v153, v153
	v_rcp_f32_e32 v181, v155
	v_mul_f32_e32 v120, 0xbfb8aa3b, v120
	v_max_f32_e32 v121, 0xc2a00000, v121
	v_exp_f32_e32 v170, v166
	v_exp_f32_e32 v171, v167
	v_lshl_add_u64 v[166:167], v[158:159], 0, v[114:115]
	v_add_f32_e32 v158, 1.0, v160
	v_add_f32_e32 v159, 1.0, v161
	v_rcp_f32_e32 v168, v168
	v_rcp_f32_e32 v182, v169
	v_exp_f32_e32 v120, v120
	v_mul_f32_e32 v121, 0xbfb8aa3b, v121
	v_rcp_f32_e32 v158, v158
	v_rcp_f32_e32 v159, v159
	v_exp_f32_e32 v121, v121
	v_add_f32_e32 v120, 1.0, v120
	v_rcp_f32_e32 v120, v120
	v_mul_f32_e32 v116, v116, v154
	v_add_f32_e32 v121, 1.0, v121
	v_rcp_f32_e32 v121, v121
	v_add_f32_e32 v160, 1.0, v170
	v_add_f32_e32 v161, 1.0, v171
	v_max_f32_e32 v116, 0xc2a00000, v116
	v_mul_f32_e32 v117, v117, v154
	v_rcp_f32_e32 v160, v160
	v_rcp_f32_e32 v161, v161
	v_mul_f32_e32 v116, 0xbfb8aa3b, v116
	v_max_f32_e32 v117, 0xc2a00000, v117
	v_exp_f32_e32 v116, v116
	v_mul_f32_e32 v117, 0xbfb8aa3b, v117
	v_exp_f32_e32 v117, v117
	s_mov_b64 s[14:15], 0x80000
	v_add_f32_e32 v116, 1.0, v116
	v_rcp_f32_e32 v116, v116
	v_add_f32_e32 v117, 1.0, v117
	s_waitcnt vmcnt(0)
	v_sub_f32_e32 v180, 1.0, v136
	v_sub_f32_e32 v179, 1.0, v137
	v_sub_f32_e32 v169, 1.0, v134
	v_sub_f32_e32 v155, 1.0, v135
	v_fma_f32 v153, v180, v153, v136
	v_fma_f32 v181, v179, v181, v137
	v_sub_f32_e32 v178, 1.0, v138
	v_sub_f32_e32 v177, 1.0, v139
	v_fma_f32 v168, v169, v168, v134
	v_fma_f32 v182, v155, v182, v135
	v_log_f32_e32 v153, v153
	v_log_f32_e32 v181, v181
	v_fma_f32 v158, v178, v158, v138
	v_fma_f32 v159, v177, v159, v139
	v_log_f32_e32 v168, v168
	v_log_f32_e32 v182, v182
	v_log_f32_e32 v158, v158
	v_log_f32_e32 v159, v159
	v_cvt_pk_f16_f32 v194, v153, v181
	v_sub_f32_e32 v153, 1.0, v128
	v_cvt_pk_f16_f32 v197, v168, v182
	v_fma_f32 v120, v153, v120, v128
	v_sub_f32_e32 v168, 1.0, v129
	v_cvt_pk_f16_f32 v195, v158, v159
	v_log_f32_e32 v158, v120
	v_fma_f32 v120, v168, v121, v129
	v_log_f32_e32 v159, v120
	v_mul_f32_e32 v120, v122, v154
	v_max_f32_e32 v120, 0xc2a00000, v120
	v_mul_f32_e32 v121, v123, v154
	v_mul_f32_e32 v120, 0xbfb8aa3b, v120
	v_max_f32_e32 v121, 0xc2a00000, v121
	v_exp_f32_e32 v120, v120
	v_mul_f32_e32 v121, 0xbfb8aa3b, v121
	v_exp_f32_e32 v122, v121
	v_sub_f32_e32 v171, 1.0, v132
	v_sub_f32_e32 v170, 1.0, v133
	v_add_f32_e32 v120, 1.0, v120
	v_fma_f32 v160, v171, v160, v132
	v_fma_f32 v161, v170, v161, v133
	v_rcp_f32_e32 v120, v120
	v_add_f32_e32 v122, 1.0, v122
	v_log_f32_e32 v160, v160
	v_log_f32_e32 v161, v161
	v_rcp_f32_e32 v123, v122
	v_sub_f32_e32 v121, 1.0, v130
	v_rcp_f32_e32 v117, v117
	v_fma_f32 v120, v121, v120, v130
	v_sub_f32_e32 v122, 1.0, v131
	v_cvt_pk_f16_f32 v196, v160, v161
	v_log_f32_e32 v160, v120
	v_fma_f32 v120, v122, v123, v131
	v_sub_f32_e32 v123, 1.0, v124
	v_log_f32_e32 v161, v120
	v_fma_f32 v116, v123, v116, v124
	v_sub_f32_e32 v120, 1.0, v125
	v_log_f32_e32 v181, v116
	v_fma_f32 v116, v120, v117, v125
	v_log_f32_e32 v182, v116
	v_mul_f32_e32 v116, v118, v154
	v_max_f32_e32 v116, 0xc2a00000, v116
	v_mul_f32_e32 v117, v119, v154
	v_mul_f32_e32 v116, 0xbfb8aa3b, v116
	v_max_f32_e32 v117, 0xc2a00000, v117
	v_exp_f32_e32 v116, v116
	v_mul_f32_e32 v117, 0xbfb8aa3b, v117
	v_exp_f32_e32 v117, v117
	v_sub_f32_e32 v118, 1.0, v126
	v_add_f32_e32 v116, 1.0, v116
	v_rcp_f32_e32 v116, v116
	v_add_f32_e32 v117, 1.0, v117
	v_rcp_f32_e32 v117, v117
	v_sub_f32_e32 v119, 1.0, v127
	v_fma_f32 v116, v118, v116, v126
	v_log_f32_e32 v154, v116
	v_fma_f32 v116, v119, v117, v127
	v_log_f32_e32 v183, v116
	ds_read2_b32 v[116:117], v176 offset0:16 offset1:32
	ds_bpermute_b32 v238, v250, v194
	ds_bpermute_b32 v239, v250, v195
	ds_bpermute_b32 v240, v250, v196
	ds_bpermute_b32 v241, v250, v197
	ds_bpermute_b32 v242, v250, v166
	s_waitcnt lgkmcnt(0)
	v_mul_f32_e32 v106, v106, v116
	v_max_f32_e32 v106, 0xc2a00000, v106
	v_mul_f32_e32 v106, 0xbfb8aa3b, v106
	v_exp_f32_e32 v106, v106
	v_mul_f32_e32 v110, v110, v116
	v_max_f32_e32 v110, 0xc2a00000, v110
	v_mul_f32_e32 v111, v111, v116
	v_mul_f32_e32 v110, 0xbfb8aa3b, v110
	v_max_f32_e32 v111, 0xc2a00000, v111
	v_mul_f32_e32 v107, v107, v116
	v_exp_f32_e32 v110, v110
	v_mul_f32_e32 v111, 0xbfb8aa3b, v111
	v_add_f32_e32 v106, 1.0, v106
	v_max_f32_e32 v107, 0xc2a00000, v107
	v_exp_f32_e32 v111, v111
	v_rcp_f32_e32 v106, v106
	v_mul_f32_e32 v107, 0xbfb8aa3b, v107
	v_exp_f32_e32 v107, v107
	v_cvt_pk_f16_f32 v194, v158, v159
	v_or_b32_e32 v158, 16, v152
	v_add_f32_e32 v110, 1.0, v110
	v_mul_f32_e32 v112, v112, v116
	v_mul_f32_e32 v113, v113, v116
	v_cvt_pk_f16_f32 v197, v154, v183
	v_ashrrev_i32_e32 v159, 31, v158
	v_rcp_f32_e32 v154, v110
	v_add_f32_e32 v110, 1.0, v111
	v_max_f32_e32 v112, 0xc2a00000, v112
	v_max_f32_e32 v113, 0xc2a00000, v113
	v_fma_f32 v106, v171, v106, v132
	v_cvt_pk_f16_f32 v195, v160, v161
	v_rcp_f32_e32 v160, v110
	v_lshlrev_b64 v[110:111], 12, v[158:159]
	v_mul_f32_e32 v112, 0xbfb8aa3b, v112
	v_mul_f32_e32 v113, 0xbfb8aa3b, v113
	v_log_f32_e32 v159, v106
	v_add_f32_e32 v106, 1.0, v107
	v_mul_f32_e32 v107, v108, v116
	v_exp_f32_e32 v112, v112
	v_exp_f32_e32 v113, v113
	v_max_f32_e32 v107, 0xc2a00000, v107
	v_mul_f32_e32 v108, v109, v116
	v_mul_f32_e32 v107, 0xbfb8aa3b, v107
	v_max_f32_e32 v108, 0xc2a00000, v108
	v_exp_f32_e32 v107, v107
	v_mul_f32_e32 v108, 0xbfb8aa3b, v108
	v_exp_f32_e32 v108, v108
	v_add_f32_e32 v112, 1.0, v112
	v_add_f32_e32 v113, 1.0, v113
	v_rcp_f32_e32 v112, v112
	v_rcp_f32_e32 v113, v113
	v_mul_f32_e32 v98, v98, v116
	v_rcp_f32_e32 v106, v106
	v_add_f32_e32 v107, 1.0, v107
	v_max_f32_e32 v98, 0xc2a00000, v98
	v_rcp_f32_e32 v107, v107
	v_add_f32_e32 v108, 1.0, v108
	v_mul_f32_e32 v98, 0xbfb8aa3b, v98
	v_rcp_f32_e32 v108, v108
	v_exp_f32_e32 v98, v98
	v_fma_f32 v112, v178, v112, v138
	v_fma_f32 v113, v177, v113, v139
	v_log_f32_e32 v112, v112
	v_log_f32_e32 v113, v113
	v_fma_f32 v106, v170, v106, v133
	v_log_f32_e32 v109, v106
	v_fma_f32 v106, v169, v107, v134
	v_mul_f32_e32 v102, v102, v116
	v_mul_f32_e32 v99, v99, v116
	v_fma_f32 v154, v180, v154, v136
	v_fma_f32 v158, v179, v160, v137
	v_log_f32_e32 v160, v106
	v_fma_f32 v106, v155, v108, v135
	v_max_f32_e32 v102, 0xc2a00000, v102
	v_add_f32_e32 v98, 1.0, v98
	v_max_f32_e32 v99, 0xc2a00000, v99
	v_log_f32_e32 v154, v154
	v_log_f32_e32 v158, v158
	v_log_f32_e32 v161, v106
	v_mul_f32_e32 v102, 0xbfb8aa3b, v102
	v_rcp_f32_e32 v98, v98
	v_mul_f32_e32 v99, 0xbfb8aa3b, v99
	v_cvt_pk_f16_f32 v107, v112, v113
	v_exp_f32_e32 v112, v102
	v_mul_f32_e32 v102, v103, v116
	v_exp_f32_e32 v99, v99
	v_max_f32_e32 v102, 0xc2a00000, v102
	v_lshl_add_u64 v[110:111], s[42:43], 0, v[110:111]
	v_mul_f32_e32 v102, 0xbfb8aa3b, v102
	v_cvt_pk_f16_f32 v106, v154, v158
	v_cvt_pk_f16_f32 v108, v159, v109
	v_cvt_pk_f16_f32 v109, v160, v161
	v_exp_f32_e32 v113, v102
	v_lshl_add_u64 v[102:103], v[110:111], 0, v[114:115]
	v_fma_f32 v98, v123, v98, v124
	ds_bpermute_b32 v244, v250, v106
	ds_bpermute_b32 v245, v250, v107
	ds_bpermute_b32 v246, v250, v108
	ds_bpermute_b32 v247, v250, v109
	ds_bpermute_b32 v248, v250, v102
	v_mul_f32_e32 v104, v104, v116
	v_mul_f32_e32 v105, v105, v116
	v_log_f32_e32 v108, v98
	v_add_f32_e32 v98, 1.0, v99
	v_mul_f32_e32 v99, v100, v116
	v_max_f32_e32 v99, 0xc2a00000, v99
	v_mul_f32_e32 v100, v101, v116
	v_max_f32_e32 v104, 0xc2a00000, v104
	v_max_f32_e32 v105, 0xc2a00000, v105
	v_mul_f32_e32 v99, 0xbfb8aa3b, v99
	v_max_f32_e32 v100, 0xc2a00000, v100
	v_mul_f32_e32 v104, 0xbfb8aa3b, v104
	v_mul_f32_e32 v105, 0xbfb8aa3b, v105
	v_exp_f32_e32 v99, v99
	v_mul_f32_e32 v100, 0xbfb8aa3b, v100
	v_exp_f32_e32 v104, v104
	v_exp_f32_e32 v105, v105
	v_exp_f32_e32 v100, v100
	v_rcp_f32_e32 v98, v98
	v_add_f32_e32 v99, 1.0, v99
	v_add_f32_e32 v110, 1.0, v112
	v_add_f32_e32 v111, 1.0, v113
	v_add_f32_e32 v104, 1.0, v104
	v_add_f32_e32 v105, 1.0, v105
	v_rcp_f32_e32 v99, v99
	v_add_f32_e32 v100, 1.0, v100
	v_rcp_f32_e32 v110, v110
	v_rcp_f32_e32 v111, v111
	v_rcp_f32_e32 v104, v104
	v_rcp_f32_e32 v105, v105
	v_rcp_f32_e32 v100, v100
	v_mul_f32_e32 v90, v90, v117
	v_fma_f32 v98, v120, v98, v125
	v_mul_f32_e32 v94, v94, v117
	v_max_f32_e32 v90, 0xc2a00000, v90
	v_log_f32_e32 v101, v98
	v_fma_f32 v98, v118, v99, v126
	v_max_f32_e32 v94, 0xc2a00000, v94
	v_mul_f32_e32 v90, 0xbfb8aa3b, v90
	v_fma_f32 v106, v153, v110, v128
	v_fma_f32 v107, v168, v111, v129
	v_fma_f32 v104, v121, v104, v130
	v_fma_f32 v105, v122, v105, v131
	v_log_f32_e32 v109, v98
	v_fma_f32 v98, v119, v100, v127
	v_mul_f32_e32 v94, 0xbfb8aa3b, v94
	v_exp_f32_e32 v90, v90
	v_log_f32_e32 v106, v106
	v_log_f32_e32 v107, v107
	v_log_f32_e32 v104, v104
	v_log_f32_e32 v105, v105
	v_log_f32_e32 v110, v98
	v_exp_f32_e32 v94, v94
	v_mul_f32_e32 v95, v95, v117
	v_max_f32_e32 v95, 0xc2a00000, v95
	v_mul_f32_e32 v91, v91, v117
	v_mul_f32_e32 v95, 0xbfb8aa3b, v95
	v_add_f32_e32 v90, 1.0, v90
	v_max_f32_e32 v91, 0xc2a00000, v91
	v_cvt_pk_f16_f32 v98, v106, v107
	v_cvt_pk_f16_f32 v99, v104, v105
	v_cvt_pk_f16_f32 v100, v108, v101
	v_cvt_pk_f16_f32 v101, v109, v110
	v_exp_f32_e32 v95, v95
	v_add_f32_e32 v94, 1.0, v94
	v_rcp_f32_e32 v90, v90
	v_mul_f32_e32 v91, 0xbfb8aa3b, v91
	s_waitcnt lgkmcnt(5)
	v_subrev_u32_e32 v242, s82, v242
	global_store_dwordx4 v242, v[238:241], s[82:83] sc0 sc1
	ds_bpermute_b32 v232, v250, v98
	ds_bpermute_b32 v233, v250, v99
	ds_bpermute_b32 v234, v250, v100
	ds_bpermute_b32 v235, v250, v101
	ds_bpermute_b32 v236, v250, v102
	v_exp_f32_e32 v91, v91
	v_fma_f32 v90, v171, v90, v132
	v_rcp_f32_e32 v100, v94
	v_or_b32_e32 v98, 32, v152
	v_ashrrev_i32_e32 v99, 31, v98
	v_add_f32_e32 v94, 1.0, v95
	v_rcp_f32_e32 v101, v94
	v_lshlrev_b64 v[94:95], 12, v[98:99]
	v_fma_f32 v98, v180, v100, v136
	v_log_f32_e32 v100, v90
	v_add_f32_e32 v90, 1.0, v91
	v_mul_f32_e32 v91, v92, v117
	v_mul_f32_e32 v96, v96, v117
	v_mul_f32_e32 v97, v97, v117
	v_max_f32_e32 v91, 0xc2a00000, v91
	v_mul_f32_e32 v92, v93, v117
	v_max_f32_e32 v96, 0xc2a00000, v96
	v_max_f32_e32 v97, 0xc2a00000, v97
	v_mul_f32_e32 v91, 0xbfb8aa3b, v91
	v_max_f32_e32 v92, 0xc2a00000, v92
	v_mul_f32_e32 v96, 0xbfb8aa3b, v96
	v_mul_f32_e32 v97, 0xbfb8aa3b, v97
	v_exp_f32_e32 v91, v91
	v_mul_f32_e32 v92, 0xbfb8aa3b, v92
	v_exp_f32_e32 v96, v96
	v_exp_f32_e32 v97, v97
	v_exp_f32_e32 v92, v92
	v_mul_f32_e32 v82, v82, v117
	v_rcp_f32_e32 v90, v90
	v_add_f32_e32 v91, 1.0, v91
	v_max_f32_e32 v82, 0xc2a00000, v82
	v_add_f32_e32 v96, 1.0, v96
	v_add_f32_e32 v97, 1.0, v97
	v_rcp_f32_e32 v91, v91
	v_add_f32_e32 v92, 1.0, v92
	v_mul_f32_e32 v82, 0xbfb8aa3b, v82
	v_rcp_f32_e32 v96, v96
	v_rcp_f32_e32 v97, v97
	v_rcp_f32_e32 v92, v92
	v_exp_f32_e32 v82, v82
	v_fma_f32 v90, v170, v90, v133
	v_log_f32_e32 v93, v90
	v_fma_f32 v90, v169, v91, v134
	v_mul_f32_e32 v83, v83, v117
	v_fma_f32 v99, v179, v101, v137
	v_fma_f32 v96, v178, v96, v138
	v_fma_f32 v97, v177, v97, v139
	v_log_f32_e32 v101, v90
	v_fma_f32 v90, v155, v92, v135
	v_add_f32_e32 v82, 1.0, v82
	v_max_f32_e32 v83, 0xc2a00000, v83
	v_log_f32_e32 v98, v98
	v_log_f32_e32 v99, v99
	v_log_f32_e32 v96, v96
	v_log_f32_e32 v97, v97
	v_log_f32_e32 v102, v90
	v_rcp_f32_e32 v82, v82
	v_mul_f32_e32 v83, 0xbfb8aa3b, v83
	v_exp_f32_e32 v83, v83
	v_lshl_add_u64 v[94:95], s[42:43], 0, v[94:95]
	v_cvt_pk_f16_f32 v90, v98, v99
	v_cvt_pk_f16_f32 v91, v96, v97
	v_cvt_pk_f16_f32 v92, v100, v93
	v_cvt_pk_f16_f32 v93, v101, v102
	v_lshl_add_u64 v[94:95], v[94:95], 0, v[114:115]
	v_fma_f32 v82, v123, v82, v124
	s_waitcnt lgkmcnt(5)
	v_subrev_u32_e32 v248, s82, v248
	global_store_dwordx4 v248, v[244:247], s[82:83] sc0 sc1
	ds_bpermute_b32 v238, v250, v90
	ds_bpermute_b32 v239, v250, v91
	ds_bpermute_b32 v240, v250, v92
	ds_bpermute_b32 v241, v250, v93
	ds_bpermute_b32 v242, v250, v94
	v_mul_f32_e32 v86, v86, v117
	v_mul_f32_e32 v87, v87, v117
	v_log_f32_e32 v90, v82
	v_add_f32_e32 v82, 1.0, v83
	v_mul_f32_e32 v83, v84, v117
	v_max_f32_e32 v83, 0xc2a00000, v83
	v_mul_f32_e32 v84, v85, v117
	v_mul_f32_e32 v83, 0xbfb8aa3b, v83
	v_max_f32_e32 v84, 0xc2a00000, v84
	v_exp_f32_e32 v83, v83
	v_mul_f32_e32 v84, 0xbfb8aa3b, v84
	v_exp_f32_e32 v84, v84
	v_rcp_f32_e32 v82, v82
	v_add_f32_e32 v83, 1.0, v83
	v_rcp_f32_e32 v83, v83
	v_add_f32_e32 v84, 1.0, v84
	v_rcp_f32_e32 v84, v84
	v_mul_f32_e32 v88, v88, v117
	v_mul_f32_e32 v89, v89, v117
	v_max_f32_e32 v86, 0xc2a00000, v86
	v_max_f32_e32 v87, 0xc2a00000, v87
	v_max_f32_e32 v88, 0xc2a00000, v88
	v_max_f32_e32 v89, 0xc2a00000, v89
	v_fma_f32 v82, v120, v82, v125
	v_mul_f32_e32 v86, 0xbfb8aa3b, v86
	v_mul_f32_e32 v87, 0xbfb8aa3b, v87
	v_mul_f32_e32 v88, 0xbfb8aa3b, v88
	v_mul_f32_e32 v89, 0xbfb8aa3b, v89
	v_log_f32_e32 v91, v82
	v_fma_f32 v82, v118, v83, v126
	v_exp_f32_e32 v86, v86
	v_exp_f32_e32 v87, v87
	v_exp_f32_e32 v88, v88
	v_exp_f32_e32 v89, v89
	v_log_f32_e32 v92, v82
	v_fma_f32 v82, v119, v84, v127
	v_log_f32_e32 v93, v82
	ds_read2_b32 v[82:83], v176 offset0:48 offset1:128
	v_add_f32_e32 v86, 1.0, v86
	v_add_f32_e32 v87, 1.0, v87
	v_add_f32_e32 v88, 1.0, v88
	v_add_f32_e32 v89, 1.0, v89
	v_rcp_f32_e32 v86, v86
	v_rcp_f32_e32 v87, v87
	v_rcp_f32_e32 v88, v88
	v_rcp_f32_e32 v89, v89
	s_waitcnt lgkmcnt(0)
	v_mul_f32_e32 v74, v74, v82
	v_mul_f32_e32 v78, v78, v82
	v_max_f32_e32 v74, 0xc2a00000, v74
	v_max_f32_e32 v78, 0xc2a00000, v78
	v_mul_f32_e32 v74, 0xbfb8aa3b, v74
	v_fma_f32 v86, v153, v86, v128
	v_fma_f32 v87, v168, v87, v129
	v_fma_f32 v88, v121, v88, v130
	v_fma_f32 v89, v122, v89, v131
	v_mul_f32_e32 v78, 0xbfb8aa3b, v78
	v_exp_f32_e32 v74, v74
	v_log_f32_e32 v86, v86
	v_log_f32_e32 v87, v87
	v_log_f32_e32 v88, v88
	v_log_f32_e32 v89, v89
	v_exp_f32_e32 v78, v78
	v_mul_f32_e32 v79, v79, v82
	v_max_f32_e32 v79, 0xc2a00000, v79
	v_mul_f32_e32 v75, v75, v82
	v_mul_f32_e32 v79, 0xbfb8aa3b, v79
	v_add_f32_e32 v74, 1.0, v74
	v_max_f32_e32 v75, 0xc2a00000, v75
	v_cvt_pk_f16_f32 v84, v86, v87
	v_cvt_pk_f16_f32 v85, v88, v89
	v_cvt_pk_f16_f32 v86, v90, v91
	v_cvt_pk_f16_f32 v87, v92, v93
	v_exp_f32_e32 v79, v79
	v_add_f32_e32 v78, 1.0, v78
	v_rcp_f32_e32 v74, v74
	v_mul_f32_e32 v75, 0xbfb8aa3b, v75
	s_waitcnt lgkmcnt(6)
	v_subrev_u32_e32 v236, s82, v236
	global_store_dwordx4 v236, v[232:235], s[82:83] offset:64 sc0 sc1
	ds_bpermute_b32 v244, v250, v84
	ds_bpermute_b32 v245, v250, v85
	ds_bpermute_b32 v246, v250, v86
	ds_bpermute_b32 v247, v250, v87
	ds_bpermute_b32 v248, v250, v94
	v_exp_f32_e32 v75, v75
	v_mul_f32_e32 v80, v80, v82
	v_rcp_f32_e32 v86, v78
	v_or_b32_e32 v84, 48, v152
	v_mul_f32_e32 v81, v81, v82
	v_ashrrev_i32_e32 v85, 31, v84
	v_add_f32_e32 v78, 1.0, v79
	v_max_f32_e32 v80, 0xc2a00000, v80
	v_max_f32_e32 v81, 0xc2a00000, v81
	v_fma_f32 v74, v171, v74, v132
	v_rcp_f32_e32 v87, v78
	v_lshlrev_b64 v[78:79], 12, v[84:85]
	v_fma_f32 v84, v180, v86, v136
	v_mul_f32_e32 v80, 0xbfb8aa3b, v80
	v_mul_f32_e32 v81, 0xbfb8aa3b, v81
	v_log_f32_e32 v86, v74
	v_add_f32_e32 v74, 1.0, v75
	v_mul_f32_e32 v75, v76, v82
	v_exp_f32_e32 v80, v80
	v_exp_f32_e32 v81, v81
	v_max_f32_e32 v75, 0xc2a00000, v75
	v_mul_f32_e32 v76, v77, v82
	v_mul_f32_e32 v75, 0xbfb8aa3b, v75
	v_max_f32_e32 v76, 0xc2a00000, v76
	v_exp_f32_e32 v75, v75
	v_mul_f32_e32 v76, 0xbfb8aa3b, v76
	v_exp_f32_e32 v76, v76
	v_add_f32_e32 v80, 1.0, v80
	v_add_f32_e32 v81, 1.0, v81
	v_rcp_f32_e32 v80, v80
	v_rcp_f32_e32 v81, v81
	v_mul_f32_e32 v66, v66, v82
	v_rcp_f32_e32 v74, v74
	v_add_f32_e32 v75, 1.0, v75
	v_max_f32_e32 v66, 0xc2a00000, v66
	v_rcp_f32_e32 v75, v75
	v_add_f32_e32 v76, 1.0, v76
	v_mul_f32_e32 v66, 0xbfb8aa3b, v66
	v_rcp_f32_e32 v76, v76
	v_exp_f32_e32 v66, v66
	v_fma_f32 v80, v178, v80, v138
	v_fma_f32 v81, v177, v81, v139
	v_log_f32_e32 v80, v80
	v_log_f32_e32 v81, v81
	v_fma_f32 v74, v170, v74, v133
	v_log_f32_e32 v77, v74
	v_fma_f32 v74, v169, v75, v134
	v_mul_f32_e32 v70, v70, v82
	v_mul_f32_e32 v67, v67, v82
	v_fma_f32 v85, v179, v87, v137
	v_log_f32_e32 v87, v74
	v_fma_f32 v74, v155, v76, v135
	v_max_f32_e32 v70, 0xc2a00000, v70
	v_add_f32_e32 v66, 1.0, v66
	v_max_f32_e32 v67, 0xc2a00000, v67
	v_log_f32_e32 v84, v84
	v_log_f32_e32 v85, v85
	v_log_f32_e32 v88, v74
	v_mul_f32_e32 v70, 0xbfb8aa3b, v70
	v_rcp_f32_e32 v66, v66
	v_mul_f32_e32 v67, 0xbfb8aa3b, v67
	v_cvt_pk_f16_f32 v75, v80, v81
	v_exp_f32_e32 v80, v70
	v_mul_f32_e32 v70, v71, v82
	v_exp_f32_e32 v67, v67
	v_max_f32_e32 v70, 0xc2a00000, v70
	v_lshl_add_u64 v[78:79], s[42:43], 0, v[78:79]
	v_mul_f32_e32 v70, 0xbfb8aa3b, v70
	v_cvt_pk_f16_f32 v74, v84, v85
	v_cvt_pk_f16_f32 v76, v86, v77
	v_cvt_pk_f16_f32 v77, v87, v88
	v_exp_f32_e32 v81, v70
	v_lshl_add_u64 v[70:71], v[78:79], 0, v[114:115]
	v_fma_f32 v66, v123, v66, v124
	s_waitcnt lgkmcnt(6)
	v_subrev_u32_e32 v242, s82, v242
	global_store_dwordx4 v242, v[238:241], s[82:83] sc0 sc1
	ds_bpermute_b32 v232, v250, v74
	ds_bpermute_b32 v233, v250, v75
	ds_bpermute_b32 v234, v250, v76
	ds_bpermute_b32 v235, v250, v77
	ds_bpermute_b32 v236, v250, v70
	v_mul_f32_e32 v72, v72, v82
	v_mul_f32_e32 v73, v73, v82
	v_log_f32_e32 v76, v66
	v_add_f32_e32 v66, 1.0, v67
	v_mul_f32_e32 v67, v68, v82
	v_max_f32_e32 v67, 0xc2a00000, v67
	v_mul_f32_e32 v68, v69, v82
	v_max_f32_e32 v72, 0xc2a00000, v72
	v_max_f32_e32 v73, 0xc2a00000, v73
	v_mul_f32_e32 v67, 0xbfb8aa3b, v67
	v_max_f32_e32 v68, 0xc2a00000, v68
	v_mul_f32_e32 v72, 0xbfb8aa3b, v72
	v_mul_f32_e32 v73, 0xbfb8aa3b, v73
	v_exp_f32_e32 v67, v67
	v_mul_f32_e32 v68, 0xbfb8aa3b, v68
	v_exp_f32_e32 v72, v72
	v_exp_f32_e32 v73, v73
	v_exp_f32_e32 v68, v68
	v_mul_f32_e32 v58, v58, v83
	v_rcp_f32_e32 v66, v66
	v_add_f32_e32 v67, 1.0, v67
	v_max_f32_e32 v58, 0xc2a00000, v58
	v_add_f32_e32 v78, 1.0, v80
	v_add_f32_e32 v79, 1.0, v81
	v_add_f32_e32 v72, 1.0, v72
	v_add_f32_e32 v73, 1.0, v73
	v_rcp_f32_e32 v67, v67
	v_add_f32_e32 v68, 1.0, v68
	v_mul_f32_e32 v58, 0xbfb8aa3b, v58
	v_rcp_f32_e32 v78, v78
	v_rcp_f32_e32 v79, v79
	v_rcp_f32_e32 v72, v72
	v_rcp_f32_e32 v73, v73
	v_rcp_f32_e32 v68, v68
	v_exp_f32_e32 v58, v58
	v_fma_f32 v66, v120, v66, v125
	v_log_f32_e32 v69, v66
	v_fma_f32 v66, v118, v67, v126
	v_mul_f32_e32 v59, v59, v83
	v_fma_f32 v74, v153, v78, v128
	v_fma_f32 v75, v168, v79, v129
	v_fma_f32 v72, v121, v72, v130
	v_fma_f32 v73, v122, v73, v131
	v_log_f32_e32 v77, v66
	v_fma_f32 v66, v119, v68, v127
	v_add_f32_e32 v58, 1.0, v58
	v_max_f32_e32 v59, 0xc2a00000, v59
	v_log_f32_e32 v74, v74
	v_log_f32_e32 v75, v75
	v_log_f32_e32 v72, v72
	v_log_f32_e32 v73, v73
	v_log_f32_e32 v78, v66
	v_rcp_f32_e32 v58, v58
	v_mul_f32_e32 v59, 0xbfb8aa3b, v59
	v_exp_f32_e32 v59, v59
	v_mul_f32_e32 v64, v64, v83
	v_mul_f32_e32 v65, v65, v83
	v_max_f32_e32 v64, 0xc2a00000, v64
	v_max_f32_e32 v65, 0xc2a00000, v65
	v_cvt_pk_f16_f32 v66, v74, v75
	v_cvt_pk_f16_f32 v67, v72, v73
	v_cvt_pk_f16_f32 v68, v76, v69
	v_mul_f32_e32 v62, v62, v83
	v_mul_f32_e32 v63, v63, v83
	v_cvt_pk_f16_f32 v69, v77, v78
	v_mul_f32_e32 v64, 0xbfb8aa3b, v64
	v_mul_f32_e32 v65, 0xbfb8aa3b, v65
	v_fma_f32 v58, v171, v58, v132
	v_max_f32_e32 v62, 0xc2a00000, v62
	v_max_f32_e32 v63, 0xc2a00000, v63
	s_waitcnt lgkmcnt(5)
	v_subrev_u32_e32 v248, s82, v248
	global_store_dwordx4 v248, v[244:247], s[82:83] offset:64 sc0 sc1
	ds_bpermute_b32 v238, v250, v66
	ds_bpermute_b32 v239, v250, v67
	ds_bpermute_b32 v240, v250, v68
	ds_bpermute_b32 v241, v250, v69
	ds_bpermute_b32 v242, v250, v70
	v_exp_f32_e32 v64, v64
	v_exp_f32_e32 v65, v65
	v_log_f32_e32 v66, v58
	v_add_f32_e32 v58, 1.0, v59
	v_mul_f32_e32 v59, v60, v83
	v_mul_f32_e32 v62, 0xbfb8aa3b, v62
	v_mul_f32_e32 v63, 0xbfb8aa3b, v63
	v_max_f32_e32 v59, 0xc2a00000, v59
	v_mul_f32_e32 v60, v61, v83
	v_exp_f32_e32 v62, v62
	v_exp_f32_e32 v63, v63
	v_mul_f32_e32 v59, 0xbfb8aa3b, v59
	v_max_f32_e32 v60, 0xc2a00000, v60
	v_exp_f32_e32 v59, v59
	v_mul_f32_e32 v60, 0xbfb8aa3b, v60
	v_add_f32_e32 v64, 1.0, v64
	v_add_f32_e32 v65, 1.0, v65
	v_exp_f32_e32 v60, v60
	v_rcp_f32_e32 v64, v64
	v_rcp_f32_e32 v65, v65
	v_add_f32_e32 v62, 1.0, v62
	v_add_f32_e32 v63, 1.0, v63
	v_mul_f32_e32 v50, v50, v83
	v_rcp_f32_e32 v62, v62
	v_rcp_f32_e32 v63, v63
	v_rcp_f32_e32 v58, v58
	v_add_f32_e32 v59, 1.0, v59
	v_max_f32_e32 v50, 0xc2a00000, v50
	v_rcp_f32_e32 v59, v59
	v_add_f32_e32 v60, 1.0, v60
	v_mul_f32_e32 v50, 0xbfb8aa3b, v50
	v_fma_f32 v64, v178, v64, v138
	v_fma_f32 v65, v177, v65, v139
	v_rcp_f32_e32 v60, v60
	v_exp_f32_e32 v50, v50
	v_log_f32_e32 v64, v64
	v_log_f32_e32 v65, v65
	v_fma_f32 v62, v180, v62, v136
	v_fma_f32 v63, v179, v63, v137
	v_fma_f32 v58, v170, v58, v133
	v_mul_f32_e32 v54, v54, v83
	v_log_f32_e32 v62, v62
	v_log_f32_e32 v63, v63
	v_log_f32_e32 v61, v58
	v_fma_f32 v58, v169, v59, v134
	v_max_f32_e32 v54, 0xc2a00000, v54
	v_mul_f32_e32 v51, v51, v83
	v_log_f32_e32 v67, v58
	v_fma_f32 v58, v155, v60, v135
	v_mul_f32_e32 v54, 0xbfb8aa3b, v54
	v_add_f32_e32 v50, 1.0, v50
	v_max_f32_e32 v51, 0xc2a00000, v51
	v_log_f32_e32 v68, v58
	v_cvt_pk_f16_f32 v59, v64, v65
	v_exp_f32_e32 v64, v54
	v_mul_f32_e32 v54, v55, v83
	v_rcp_f32_e32 v50, v50
	v_mul_f32_e32 v51, 0xbfb8aa3b, v51
	v_max_f32_e32 v54, 0xc2a00000, v54
	v_exp_f32_e32 v51, v51
	v_cvt_pk_f16_f32 v58, v62, v63
	v_lshl_add_u64 v[62:63], v[166:167], 0, s[14:15]
	v_mul_f32_e32 v54, 0xbfb8aa3b, v54
	s_mov_b32 s14, 0x80000
	v_exp_f32_e32 v65, v54
	v_add_co_u32_e32 v54, vcc, s14, v166
	v_cvt_pk_f16_f32 v60, v66, v61
	v_cvt_pk_f16_f32 v61, v67, v68
	v_addc_co_u32_e32 v55, vcc, 0, v167, vcc
	v_fma_f32 v50, v123, v50, v124
	s_waitcnt lgkmcnt(5)
	v_subrev_u32_e32 v236, s82, v236
	global_store_dwordx4 v236, v[232:235], s[82:83] sc0 sc1
	ds_bpermute_b32 v244, v250, v58
	ds_bpermute_b32 v245, v250, v59
	ds_bpermute_b32 v246, v250, v60
	ds_bpermute_b32 v247, v250, v61
	ds_bpermute_b32 v248, v250, v54
	v_mul_f32_e32 v56, v56, v83
	v_mul_f32_e32 v57, v57, v83
	v_log_f32_e32 v58, v50
	v_add_f32_e32 v50, 1.0, v51
	v_mul_f32_e32 v51, v52, v83
	v_max_f32_e32 v51, 0xc2a00000, v51
	v_mul_f32_e32 v51, 0xbfb8aa3b, v51
	v_exp_f32_e32 v51, v51
	v_rcp_f32_e32 v50, v50
	v_mul_f32_e32 v52, v53, v83
	v_max_f32_e32 v56, 0xc2a00000, v56
	v_add_f32_e32 v51, 1.0, v51
	v_rcp_f32_e32 v51, v51
	v_fma_f32 v50, v120, v50, v125
	v_log_f32_e32 v59, v50
	v_max_f32_e32 v57, 0xc2a00000, v57
	v_fma_f32 v50, v118, v51, v126
	v_log_f32_e32 v60, v50
	ds_read2_b32 v[50:51], v176 offset0:144 offset1:160
	v_max_f32_e32 v52, 0xc2a00000, v52
	v_mul_f32_e32 v56, 0xbfb8aa3b, v56
	v_mul_f32_e32 v57, 0xbfb8aa3b, v57
	v_mul_f32_e32 v52, 0xbfb8aa3b, v52
	v_exp_f32_e32 v56, v56
	v_exp_f32_e32 v57, v57
	v_exp_f32_e32 v52, v52
	s_waitcnt lgkmcnt(0)
	v_mul_f32_e32 v42, v42, v50
	v_max_f32_e32 v42, 0xc2a00000, v42
	v_add_f32_e32 v64, 1.0, v64
	v_add_f32_e32 v65, 1.0, v65
	v_add_f32_e32 v56, 1.0, v56
	v_add_f32_e32 v57, 1.0, v57
	v_add_f32_e32 v52, 1.0, v52
	v_mul_f32_e32 v42, 0xbfb8aa3b, v42
	v_rcp_f32_e32 v64, v64
	v_rcp_f32_e32 v65, v65
	v_rcp_f32_e32 v56, v56
	v_rcp_f32_e32 v57, v57
	v_rcp_f32_e32 v52, v52
	v_exp_f32_e32 v42, v42
	v_mul_f32_e32 v43, v43, v50
	v_fma_f32 v54, v153, v64, v128
	v_fma_f32 v55, v168, v65, v129
	v_fma_f32 v56, v121, v56, v130
	v_fma_f32 v57, v122, v57, v131
	v_fma_f32 v52, v119, v52, v127
	v_add_f32_e32 v42, 1.0, v42
	v_max_f32_e32 v43, 0xc2a00000, v43
	v_log_f32_e32 v54, v54
	v_log_f32_e32 v55, v55
	v_log_f32_e32 v56, v56
	v_log_f32_e32 v57, v57
	v_log_f32_e32 v61, v52
	v_rcp_f32_e32 v42, v42
	v_mul_f32_e32 v43, 0xbfb8aa3b, v43
	v_exp_f32_e32 v43, v43
	v_mul_f32_e32 v48, v48, v50
	v_mul_f32_e32 v49, v49, v50
	v_max_f32_e32 v48, 0xc2a00000, v48
	v_max_f32_e32 v49, 0xc2a00000, v49
	v_cvt_pk_f16_f32 v52, v54, v55
	v_cvt_pk_f16_f32 v53, v56, v57
	v_cvt_pk_f16_f32 v54, v58, v59
	v_mul_f32_e32 v46, v46, v50
	v_mul_f32_e32 v47, v47, v50
	v_cvt_pk_f16_f32 v55, v60, v61
	v_mul_f32_e32 v48, 0xbfb8aa3b, v48
	v_mul_f32_e32 v49, 0xbfb8aa3b, v49
	v_fma_f32 v42, v171, v42, v132
	v_max_f32_e32 v46, 0xc2a00000, v46
	v_max_f32_e32 v47, 0xc2a00000, v47
	s_waitcnt lgkmcnt(6)
	v_subrev_u32_e32 v242, s82, v242
	global_store_dwordx4 v242, v[238:241], s[82:83] offset:64 sc0 sc1
	ds_bpermute_b32 v232, v250, v52
	ds_bpermute_b32 v233, v250, v53
	ds_bpermute_b32 v234, v250, v54
	ds_bpermute_b32 v235, v250, v55
	ds_bpermute_b32 v236, v250, v62
	v_exp_f32_e32 v48, v48
	v_exp_f32_e32 v49, v49
	v_log_f32_e32 v52, v42
	v_add_f32_e32 v42, 1.0, v43
	v_mul_f32_e32 v43, v44, v50
	v_mul_f32_e32 v46, 0xbfb8aa3b, v46
	v_mul_f32_e32 v47, 0xbfb8aa3b, v47
	v_max_f32_e32 v43, 0xc2a00000, v43
	v_mul_f32_e32 v44, v45, v50
	v_exp_f32_e32 v46, v46
	v_exp_f32_e32 v47, v47
	v_mul_f32_e32 v43, 0xbfb8aa3b, v43
	v_max_f32_e32 v44, 0xc2a00000, v44
	v_exp_f32_e32 v43, v43
	v_mul_f32_e32 v44, 0xbfb8aa3b, v44
	v_add_f32_e32 v48, 1.0, v48
	v_add_f32_e32 v49, 1.0, v49
	v_exp_f32_e32 v44, v44
	v_rcp_f32_e32 v48, v48
	v_rcp_f32_e32 v49, v49
	v_add_f32_e32 v46, 1.0, v46
	v_add_f32_e32 v47, 1.0, v47
	v_mul_f32_e32 v34, v34, v50
	v_rcp_f32_e32 v46, v46
	v_rcp_f32_e32 v47, v47
	v_rcp_f32_e32 v42, v42
	v_add_f32_e32 v43, 1.0, v43
	v_max_f32_e32 v34, 0xc2a00000, v34
	v_rcp_f32_e32 v43, v43
	v_add_f32_e32 v44, 1.0, v44
	v_mul_f32_e32 v34, 0xbfb8aa3b, v34
	v_fma_f32 v48, v178, v48, v138
	v_fma_f32 v49, v177, v49, v139
	v_rcp_f32_e32 v44, v44
	v_exp_f32_e32 v34, v34
	v_log_f32_e32 v48, v48
	v_log_f32_e32 v49, v49
	v_fma_f32 v46, v180, v46, v136
	v_fma_f32 v47, v179, v47, v137
	v_fma_f32 v42, v170, v42, v133
	v_mul_f32_e32 v38, v38, v50
	v_log_f32_e32 v46, v46
	v_log_f32_e32 v47, v47
	v_log_f32_e32 v45, v42
	v_fma_f32 v42, v169, v43, v134
	v_max_f32_e32 v38, 0xc2a00000, v38
	v_mul_f32_e32 v35, v35, v50
	v_log_f32_e32 v53, v42
	v_fma_f32 v42, v155, v44, v135
	v_mul_f32_e32 v38, 0xbfb8aa3b, v38
	v_add_f32_e32 v34, 1.0, v34
	v_max_f32_e32 v35, 0xc2a00000, v35
	v_log_f32_e32 v54, v42
	v_cvt_pk_f16_f32 v43, v48, v49
	v_exp_f32_e32 v48, v38
	v_mul_f32_e32 v38, v39, v50
	v_rcp_f32_e32 v34, v34
	v_mul_f32_e32 v35, 0xbfb8aa3b, v35
	s_mov_b64 s[14:15], 0x90000
	v_max_f32_e32 v38, 0xc2a00000, v38
	v_exp_f32_e32 v35, v35
	v_cvt_pk_f16_f32 v42, v46, v47
	v_lshl_add_u64 v[46:47], v[166:167], 0, s[14:15]
	v_mul_f32_e32 v38, 0xbfb8aa3b, v38
	s_mov_b32 s14, 0x90000
	v_exp_f32_e32 v49, v38
	v_add_co_u32_e32 v38, vcc, s14, v166
	v_cvt_pk_f16_f32 v44, v52, v45
	v_cvt_pk_f16_f32 v45, v53, v54
	v_addc_co_u32_e32 v39, vcc, 0, v167, vcc
	v_fma_f32 v34, v123, v34, v124
	s_waitcnt lgkmcnt(6)
	v_subrev_u32_e32 v248, s82, v248
	global_store_dwordx4 v248, v[244:247], s[82:83] sc0 sc1
	ds_bpermute_b32 v238, v250, v42
	ds_bpermute_b32 v239, v250, v43
	ds_bpermute_b32 v240, v250, v44
	ds_bpermute_b32 v241, v250, v45
	ds_bpermute_b32 v242, v250, v38
	v_mul_f32_e32 v40, v40, v50
	v_mul_f32_e32 v41, v41, v50
	v_log_f32_e32 v42, v34
	v_add_f32_e32 v34, 1.0, v35
	v_mul_f32_e32 v35, v36, v50
	v_max_f32_e32 v35, 0xc2a00000, v35
	v_mul_f32_e32 v36, v37, v50
	v_max_f32_e32 v40, 0xc2a00000, v40
	v_max_f32_e32 v41, 0xc2a00000, v41
	v_mul_f32_e32 v35, 0xbfb8aa3b, v35
	v_max_f32_e32 v36, 0xc2a00000, v36
	v_mul_f32_e32 v40, 0xbfb8aa3b, v40
	v_mul_f32_e32 v41, 0xbfb8aa3b, v41
	v_exp_f32_e32 v35, v35
	v_mul_f32_e32 v36, 0xbfb8aa3b, v36
	v_exp_f32_e32 v40, v40
	v_exp_f32_e32 v41, v41
	v_exp_f32_e32 v36, v36
	v_mul_f32_e32 v26, v26, v51
	v_rcp_f32_e32 v34, v34
	v_add_f32_e32 v35, 1.0, v35
	v_max_f32_e32 v26, 0xc2a00000, v26
	v_add_f32_e32 v48, 1.0, v48
	v_add_f32_e32 v49, 1.0, v49
	v_add_f32_e32 v40, 1.0, v40
	v_add_f32_e32 v41, 1.0, v41
	v_rcp_f32_e32 v35, v35
	v_add_f32_e32 v36, 1.0, v36
	v_mul_f32_e32 v26, 0xbfb8aa3b, v26
	v_rcp_f32_e32 v48, v48
	v_rcp_f32_e32 v49, v49
	v_rcp_f32_e32 v40, v40
	v_rcp_f32_e32 v41, v41
	v_rcp_f32_e32 v36, v36
	v_exp_f32_e32 v26, v26
	v_fma_f32 v34, v120, v34, v125
	v_log_f32_e32 v37, v34
	v_fma_f32 v34, v118, v35, v126
	v_mul_f32_e32 v27, v27, v51
	v_fma_f32 v38, v153, v48, v128
	v_fma_f32 v39, v168, v49, v129
	v_fma_f32 v40, v121, v40, v130
	v_fma_f32 v41, v122, v41, v131
	v_log_f32_e32 v43, v34
	v_fma_f32 v34, v119, v36, v127
	v_add_f32_e32 v26, 1.0, v26
	v_max_f32_e32 v27, 0xc2a00000, v27
	v_log_f32_e32 v38, v38
	v_log_f32_e32 v39, v39
	v_log_f32_e32 v40, v40
	v_log_f32_e32 v41, v41
	v_log_f32_e32 v44, v34
	v_rcp_f32_e32 v26, v26
	v_mul_f32_e32 v27, 0xbfb8aa3b, v27
	v_exp_f32_e32 v27, v27
	v_mul_f32_e32 v32, v32, v51
	v_mul_f32_e32 v33, v33, v51
	v_max_f32_e32 v32, 0xc2a00000, v32
	v_max_f32_e32 v33, 0xc2a00000, v33
	v_cvt_pk_f16_f32 v34, v38, v39
	v_cvt_pk_f16_f32 v35, v40, v41
	v_cvt_pk_f16_f32 v36, v42, v37
	v_mul_f32_e32 v30, v30, v51
	v_mul_f32_e32 v31, v31, v51
	v_cvt_pk_f16_f32 v37, v43, v44
	v_mul_f32_e32 v32, 0xbfb8aa3b, v32
	v_mul_f32_e32 v33, 0xbfb8aa3b, v33
	v_fma_f32 v26, v171, v26, v132
	v_max_f32_e32 v30, 0xc2a00000, v30
	v_max_f32_e32 v31, 0xc2a00000, v31
	s_waitcnt lgkmcnt(5)
	v_subrev_u32_e32 v236, s82, v236
	global_store_dwordx4 v236, v[232:235], s[82:83] offset:64 sc0 sc1
	ds_bpermute_b32 v244, v250, v34
	ds_bpermute_b32 v245, v250, v35
	ds_bpermute_b32 v246, v250, v36
	ds_bpermute_b32 v247, v250, v37
	ds_bpermute_b32 v248, v250, v46
	v_exp_f32_e32 v32, v32
	v_exp_f32_e32 v33, v33
	v_log_f32_e32 v34, v26
	v_add_f32_e32 v26, 1.0, v27
	v_mul_f32_e32 v27, v28, v51
	v_mul_f32_e32 v30, 0xbfb8aa3b, v30
	v_mul_f32_e32 v31, 0xbfb8aa3b, v31
	v_max_f32_e32 v27, 0xc2a00000, v27
	v_mul_f32_e32 v28, v29, v51
	v_exp_f32_e32 v30, v30
	v_exp_f32_e32 v31, v31
	v_mul_f32_e32 v27, 0xbfb8aa3b, v27
	v_max_f32_e32 v28, 0xc2a00000, v28
	v_exp_f32_e32 v27, v27
	v_mul_f32_e32 v28, 0xbfb8aa3b, v28
	v_add_f32_e32 v32, 1.0, v32
	v_add_f32_e32 v33, 1.0, v33
	v_exp_f32_e32 v28, v28
	v_rcp_f32_e32 v32, v32
	v_rcp_f32_e32 v33, v33
	v_add_f32_e32 v30, 1.0, v30
	v_add_f32_e32 v31, 1.0, v31
	v_mul_f32_e32 v18, v18, v51
	v_rcp_f32_e32 v30, v30
	v_rcp_f32_e32 v31, v31
	v_rcp_f32_e32 v26, v26
	v_add_f32_e32 v27, 1.0, v27
	v_max_f32_e32 v18, 0xc2a00000, v18
	v_rcp_f32_e32 v27, v27
	v_add_f32_e32 v28, 1.0, v28
	v_mul_f32_e32 v18, 0xbfb8aa3b, v18
	v_fma_f32 v32, v178, v32, v138
	v_fma_f32 v33, v177, v33, v139
	v_rcp_f32_e32 v28, v28
	v_exp_f32_e32 v18, v18
	v_log_f32_e32 v32, v32
	v_log_f32_e32 v33, v33
	v_fma_f32 v30, v180, v30, v136
	v_fma_f32 v31, v179, v31, v137
	v_fma_f32 v26, v170, v26, v133
	v_mul_f32_e32 v22, v22, v51
	v_log_f32_e32 v30, v30
	v_log_f32_e32 v31, v31
	v_log_f32_e32 v29, v26
	v_fma_f32 v26, v169, v27, v134
	v_max_f32_e32 v22, 0xc2a00000, v22
	v_mul_f32_e32 v19, v19, v51
	v_log_f32_e32 v35, v26
	v_fma_f32 v26, v155, v28, v135
	v_mul_f32_e32 v22, 0xbfb8aa3b, v22
	v_add_f32_e32 v18, 1.0, v18
	v_max_f32_e32 v19, 0xc2a00000, v19
	v_log_f32_e32 v36, v26
	v_cvt_pk_f16_f32 v27, v32, v33
	v_exp_f32_e32 v32, v22
	v_mul_f32_e32 v22, v23, v51
	v_rcp_f32_e32 v18, v18
	v_mul_f32_e32 v19, 0xbfb8aa3b, v19
	s_mov_b64 s[14:15], 0xa0000
	v_max_f32_e32 v22, 0xc2a00000, v22
	v_exp_f32_e32 v19, v19
	v_cvt_pk_f16_f32 v26, v30, v31
	v_lshl_add_u64 v[30:31], v[166:167], 0, s[14:15]
	v_mul_f32_e32 v22, 0xbfb8aa3b, v22
	s_mov_b32 s14, 0xa0000
	v_exp_f32_e32 v33, v22
	v_add_co_u32_e32 v22, vcc, s14, v166
	v_cvt_pk_f16_f32 v28, v34, v29
	v_cvt_pk_f16_f32 v29, v35, v36
	v_addc_co_u32_e32 v23, vcc, 0, v167, vcc
	v_fma_f32 v18, v123, v18, v124
	s_waitcnt lgkmcnt(5)
	v_subrev_u32_e32 v242, s82, v242
	global_store_dwordx4 v242, v[238:241], s[82:83] sc0 sc1
	ds_bpermute_b32 v232, v250, v26
	ds_bpermute_b32 v233, v250, v27
	ds_bpermute_b32 v234, v250, v28
	ds_bpermute_b32 v235, v250, v29
	ds_bpermute_b32 v236, v250, v22
	v_mul_f32_e32 v24, v24, v51
	v_mul_f32_e32 v25, v25, v51
	v_log_f32_e32 v26, v18
	v_add_f32_e32 v18, 1.0, v19
	v_mul_f32_e32 v19, v20, v51
	v_max_f32_e32 v19, 0xc2a00000, v19
	v_mul_f32_e32 v20, v21, v51
	ds_read_b32 v28, v176 offset:704
	v_max_f32_e32 v24, 0xc2a00000, v24
	v_max_f32_e32 v25, 0xc2a00000, v25
	v_mul_f32_e32 v19, 0xbfb8aa3b, v19
	v_max_f32_e32 v20, 0xc2a00000, v20
	v_mul_f32_e32 v24, 0xbfb8aa3b, v24
	v_mul_f32_e32 v25, 0xbfb8aa3b, v25
	v_exp_f32_e32 v19, v19
	v_mul_f32_e32 v20, 0xbfb8aa3b, v20
	v_exp_f32_e32 v24, v24
	v_exp_f32_e32 v25, v25
	v_exp_f32_e32 v20, v20
	s_waitcnt lgkmcnt(0)
	v_mul_f32_e32 v10, v10, v28
	v_rcp_f32_e32 v18, v18
	v_add_f32_e32 v19, 1.0, v19
	v_max_f32_e32 v10, 0xc2a00000, v10
	v_add_f32_e32 v32, 1.0, v32
	v_add_f32_e32 v33, 1.0, v33
	v_add_f32_e32 v24, 1.0, v24
	v_add_f32_e32 v25, 1.0, v25
	v_rcp_f32_e32 v19, v19
	v_add_f32_e32 v20, 1.0, v20
	v_mul_f32_e32 v10, 0xbfb8aa3b, v10
	v_rcp_f32_e32 v32, v32
	v_rcp_f32_e32 v33, v33
	v_rcp_f32_e32 v24, v24
	v_rcp_f32_e32 v25, v25
	v_rcp_f32_e32 v20, v20
	v_exp_f32_e32 v10, v10
	v_fma_f32 v18, v120, v18, v125
	v_log_f32_e32 v21, v18
	v_fma_f32 v18, v118, v19, v126
	v_mul_f32_e32 v11, v11, v28
	v_fma_f32 v22, v153, v32, v128
	v_fma_f32 v23, v168, v33, v129
	v_fma_f32 v24, v121, v24, v130
	v_fma_f32 v25, v122, v25, v131
	v_log_f32_e32 v27, v18
	v_fma_f32 v18, v119, v20, v127
	v_add_f32_e32 v10, 1.0, v10
	v_max_f32_e32 v11, 0xc2a00000, v11
	v_log_f32_e32 v22, v22
	v_log_f32_e32 v23, v23
	v_log_f32_e32 v24, v24
	v_log_f32_e32 v25, v25
	v_log_f32_e32 v29, v18
	v_rcp_f32_e32 v10, v10
	v_mul_f32_e32 v11, 0xbfb8aa3b, v11
	v_mul_f32_e32 v14, v14, v28
	v_mul_f32_e32 v15, v15, v28
	v_exp_f32_e32 v11, v11
	v_max_f32_e32 v14, 0xc2a00000, v14
	v_max_f32_e32 v15, 0xc2a00000, v15
	v_mul_f32_e32 v14, 0xbfb8aa3b, v14
	v_mul_f32_e32 v15, 0xbfb8aa3b, v15
	v_cvt_pk_f16_f32 v18, v22, v23
	v_cvt_pk_f16_f32 v19, v24, v25
	v_cvt_pk_f16_f32 v20, v26, v21
	v_exp_f32_e32 v14, v14
	v_exp_f32_e32 v15, v15
	v_cvt_pk_f16_f32 v21, v27, v29
	v_fma_f32 v10, v171, v10, v132
	s_waitcnt lgkmcnt(6)
	v_subrev_u32_e32 v248, s82, v248
	global_store_dwordx4 v248, v[244:247], s[82:83] offset:64 sc0 sc1
	ds_bpermute_b32 v238, v250, v18
	ds_bpermute_b32 v239, v250, v19
	ds_bpermute_b32 v240, v250, v20
	ds_bpermute_b32 v241, v250, v21
	ds_bpermute_b32 v242, v250, v30
	v_add_f32_e32 v14, 1.0, v14
	v_add_f32_e32 v15, 1.0, v15
	v_log_f32_e32 v18, v10
	v_add_f32_e32 v10, 1.0, v11
	v_mul_f32_e32 v11, v12, v28
	v_max_f32_e32 v11, 0xc2a00000, v11
	v_mul_f32_e32 v11, 0xbfb8aa3b, v11
	v_exp_f32_e32 v11, v11
	v_rcp_f32_e32 v14, v14
	v_rcp_f32_e32 v15, v15
	v_mul_f32_e32 v16, v16, v28
	v_mul_f32_e32 v17, v17, v28
	v_rcp_f32_e32 v10, v10
	v_mul_f32_e32 v12, v13, v28
	v_add_f32_e32 v11, 1.0, v11
	v_fma_f32 v14, v180, v14, v136
	v_fma_f32 v15, v179, v15, v137
	v_max_f32_e32 v16, 0xc2a00000, v16
	v_max_f32_e32 v17, 0xc2a00000, v17
	v_max_f32_e32 v12, 0xc2a00000, v12
	v_rcp_f32_e32 v11, v11
	v_log_f32_e32 v14, v14
	v_mul_f32_e32 v16, 0xbfb8aa3b, v16
	v_mul_f32_e32 v17, 0xbfb8aa3b, v17
	v_log_f32_e32 v15, v15
	v_mul_f32_e32 v12, 0xbfb8aa3b, v12
	v_exp_f32_e32 v16, v16
	v_exp_f32_e32 v17, v17
	v_exp_f32_e32 v12, v12
	v_mul_f32_e32 v6, v6, v28
	v_fma_f32 v10, v170, v10, v133
	v_max_f32_e32 v6, 0xc2a00000, v6
	v_log_f32_e32 v13, v10
	v_fma_f32 v10, v169, v11, v134
	v_mul_f32_e32 v6, 0xbfb8aa3b, v6
	v_log_f32_e32 v19, v10
	v_cvt_pk_f16_f32 v10, v14, v15
	v_exp_f32_e32 v14, v6
	v_mul_f32_e32 v6, v7, v28
	v_mul_f32_e32 v8, v8, v28
	v_mul_f32_e32 v9, v9, v28
	v_mul_f32_e32 v2, v2, v28
	v_mul_f32_e32 v3, v3, v28
	v_mul_f32_e32 v4, v4, v28
	v_mul_f32_e32 v5, v5, v28
	v_add_f32_e32 v16, 1.0, v16
	v_add_f32_e32 v17, 1.0, v17
	v_add_f32_e32 v12, 1.0, v12
	v_max_f32_e32 v6, 0xc2a00000, v6
	v_max_f32_e32 v8, 0xc2a00000, v8
	v_max_f32_e32 v9, 0xc2a00000, v9
	v_max_f32_e32 v2, 0xc2a00000, v2
	v_max_f32_e32 v3, 0xc2a00000, v3
	v_max_f32_e32 v4, 0xc2a00000, v4
	v_max_f32_e32 v5, 0xc2a00000, v5
	v_rcp_f32_e32 v16, v16
	v_rcp_f32_e32 v17, v17
	v_rcp_f32_e32 v12, v12
	v_mul_f32_e32 v6, 0xbfb8aa3b, v6
	v_mul_f32_e32 v8, 0xbfb8aa3b, v8
	v_mul_f32_e32 v9, 0xbfb8aa3b, v9
	v_mul_f32_e32 v2, 0xbfb8aa3b, v2
	v_mul_f32_e32 v3, 0xbfb8aa3b, v3
	v_mul_f32_e32 v4, 0xbfb8aa3b, v4
	v_mul_f32_e32 v5, 0xbfb8aa3b, v5
	v_exp_f32_e32 v15, v6
	v_exp_f32_e32 v8, v8
	v_exp_f32_e32 v9, v9
	v_exp_f32_e32 v2, v2
	v_exp_f32_e32 v3, v3
	v_exp_f32_e32 v4, v4
	v_exp_f32_e32 v5, v5
	v_fma_f32 v16, v178, v16, v138
	v_fmac_f32_e32 v139, v177, v17
	v_fmac_f32_e32 v135, v155, v12
	v_log_f32_e32 v16, v16
	v_log_f32_e32 v17, v139
	v_log_f32_e32 v20, v135
	v_add_f32_e32 v14, 1.0, v14
	v_add_f32_e32 v15, 1.0, v15
	v_add_f32_e32 v8, 1.0, v8
	v_add_f32_e32 v9, 1.0, v9
	v_add_f32_e32 v2, 1.0, v2
	v_add_f32_e32 v3, 1.0, v3
	v_add_f32_e32 v4, 1.0, v4
	v_add_f32_e32 v5, 1.0, v5
	s_mov_b64 s[14:15], 0xb0000
	v_rcp_f32_e32 v14, v14
	v_rcp_f32_e32 v15, v15
	v_rcp_f32_e32 v8, v8
	v_rcp_f32_e32 v9, v9
	v_rcp_f32_e32 v2, v2
	v_rcp_f32_e32 v3, v3
	v_rcp_f32_e32 v4, v4
	v_rcp_f32_e32 v5, v5
	v_lshl_add_u64 v[136:137], v[166:167], 0, s[14:15]
	s_mov_b32 s14, 0xb0000
	v_add_co_u32_e32 v6, vcc, s14, v166
	v_cvt_pk_f16_f32 v11, v16, v17
	v_cvt_pk_f16_f32 v12, v18, v13
	v_cvt_pk_f16_f32 v13, v19, v20
	v_addc_co_u32_e32 v7, vcc, 0, v167, vcc
	s_waitcnt lgkmcnt(6)
	v_subrev_u32_e32 v236, s82, v236
	global_store_dwordx4 v236, v[232:235], s[82:83] sc0 sc1
	ds_bpermute_b32 v244, v250, v10
	ds_bpermute_b32 v245, v250, v11
	ds_bpermute_b32 v246, v250, v12
	ds_bpermute_b32 v247, v250, v13
	ds_bpermute_b32 v248, v250, v6
	v_fma_f32 v6, v153, v14, v128
	v_fma_f32 v7, v168, v15, v129
	v_fma_f32 v8, v121, v8, v130
	v_fmac_f32_e32 v131, v122, v9
	v_fma_f32 v2, v123, v2, v124
	v_fma_f32 v3, v120, v3, v125
	v_fma_f32 v4, v118, v4, v126
	v_fmac_f32_e32 v127, v119, v5
	v_log_f32_e32 v6, v6
	v_log_f32_e32 v7, v7
	v_log_f32_e32 v8, v8
	v_log_f32_e32 v9, v131
	v_log_f32_e32 v2, v2
	v_log_f32_e32 v3, v3
	v_log_f32_e32 v4, v4
	v_log_f32_e32 v5, v127
	v_cvt_pk_f16_f32 v196, v181, v182
	v_cvt_pk_f16_f32 v132, v6, v7
	v_cvt_pk_f16_f32 v133, v8, v9
	v_cvt_pk_f16_f32 v134, v2, v3
	v_cvt_pk_f16_f32 v135, v4, v5
	s_waitcnt lgkmcnt(5)
	v_subrev_u32_e32 v242, s82, v242
	global_store_dwordx4 v242, v[238:241], s[82:83] offset:64 sc0 sc1
	ds_bpermute_b32 v232, v250, v194
	ds_bpermute_b32 v233, v250, v195
	ds_bpermute_b32 v234, v250, v196
	ds_bpermute_b32 v235, v250, v197
	ds_bpermute_b32 v236, v250, v166
	s_andn2_b64 vcc, exec, s[38:39]
	s_mov_b64 s[28:29], -1
	s_waitcnt lgkmcnt(5)
	v_subrev_u32_e32 v248, s82, v248
	global_store_dwordx4 v248, v[244:247], s[82:83] sc0 sc1
	ds_bpermute_b32 v238, v250, v132
	ds_bpermute_b32 v239, v250, v133
	ds_bpermute_b32 v240, v250, v134
	ds_bpermute_b32 v241, v250, v135
	ds_bpermute_b32 v242, v250, v136
	s_waitcnt lgkmcnt(5)
	v_subrev_u32_e32 v236, s82, v236
	global_store_dwordx4 v236, v[232:235], s[82:83] offset:64 sc0 sc1
	s_waitcnt lgkmcnt(0)
	v_subrev_u32_e32 v242, s82, v242
	global_store_dwordx4 v242, v[238:241], s[82:83] offset:64 sc0 sc1
	s_cbranch_vccnz .LBB0_338

.LBB0_509:
	s_ashr_i32 s57, s56, 31
	s_lshl_b64 s[14:15], s[56:57], 25
	s_add_u32 s14, s24, s14
	s_addc_u32 s15, s37, s15
	v_lshlrev_b32_e32 v114, 1, v177
	v_ashrrev_i32_e32 v153, 31, v152
	v_lshl_add_u64 v[132:133], s[14:15], 0, v[114:115]
	v_lshlrev_b64 v[136:137], 12, v[152:153]
	v_mov_b32_e32 v155, v154
	v_lshl_add_u64 v[136:137], v[132:133], 0, v[136:137]
	v_cvt_pk_bf16_f32 v166, v166, v167
	v_cvt_pk_bf16_f32 v167, v134, v135
	v_cvt_pk_bf16_f32 v168, v168, v169
	v_cvt_pk_bf16_f32 v169, v138, v139
	v_mov_b32_e32 v158, v154
	v_mov_b32_e32 v159, v154
	v_cndmask_b32_e64 v114, 0, 1, s[54:55]
	ds_bpermute_b32 v232, v250, v166
	ds_bpermute_b32 v233, v250, v167
	ds_bpermute_b32 v234, v250, v168
	ds_bpermute_b32 v235, v250, v169
	ds_bpermute_b32 v236, v250, v136
	v_pk_mul_f32 v[138:139], v[122:123], v[158:159]
	v_pk_mul_f32 v[134:135], v[120:121], v[154:155]
	v_pk_mul_f32 v[166:167], v[118:119], v[158:159]
	v_cmp_ne_u32_e64 s[40:41], 1, v114
	s_andn2_b64 vcc, exec, s[54:55]
	v_pk_mul_f32 v[168:169], v[116:117], v[154:155]
	s_waitcnt lgkmcnt(0)
	v_subrev_u32_e32 v236, s82, v236
	global_store_dwordx4 v236, v[232:235], s[82:83] sc0 sc1
	s_cbranch_vccnz .LBB0_511
	v_max_f32_e32 v114, v134, v134
	v_max_f32_e32 v134, 0xc2a00000, v114
	v_max_f32_e32 v114, v168, v168
	v_max_f32_e32 v158, 0xc2a00000, v114
	v_mul_f32_e32 v114, 0xbfb8aa3b, v134
	v_exp_f32_e32 v114, v114
	v_mul_f32_e32 v155, 0xbfb8aa3b, v158
	v_exp_f32_e32 v155, v155
	v_max_f32_e32 v135, v135, v135
	v_add_f32_e32 v114, 1.0, v114
	v_rcp_f32_e32 v160, v114
	v_add_f32_e32 v114, 1.0, v155
	v_max_f32_e32 v135, 0xc2a00000, v135
	v_max_f32_e32 v155, v169, v169
	v_max_f32_e32 v159, 0xc2a00000, v155
	v_mul_f32_e32 v155, 0xbfb8aa3b, v135
	v_exp_f32_e32 v155, v155
	v_mul_f32_e32 v161, 0xbfb8aa3b, v159
	v_exp_f32_e32 v169, v161
	v_max_f32_e32 v138, v138, v138
	v_rcp_f32_e32 v168, v114
	v_add_f32_e32 v114, 1.0, v155
	v_max_f32_e32 v138, 0xc2a00000, v138
	v_max_f32_e32 v155, v166, v166
	v_max_f32_e32 v166, 0xc2a00000, v155
	v_mul_f32_e32 v155, 0xbfb8aa3b, v138
	v_exp_f32_e32 v155, v155
	v_rcp_f32_e32 v161, v114
	v_add_f32_e32 v114, 1.0, v169
	v_mul_f32_e32 v169, 0xbfb8aa3b, v166
	v_exp_f32_e32 v171, v169
	v_max_f32_e32 v139, v139, v139
	v_rcp_f32_e32 v169, v114
	v_add_f32_e32 v114, 1.0, v155
	v_max_f32_e32 v139, 0xc2a00000, v139
	v_max_f32_e32 v155, v167, v167
	v_max_f32_e32 v167, 0xc2a00000, v155
	v_mul_f32_e32 v155, 0xbfb8aa3b, v139
	v_rcp_f32_e32 v170, v114
	v_add_f32_e32 v114, 1.0, v171
	v_exp_f32_e32 v155, v155
	v_mul_f32_e32 v171, 0xbfb8aa3b, v167
	v_exp_f32_e32 v179, v171
	v_rcp_f32_e32 v178, v114
	v_add_f32_e32 v114, 1.0, v155
	v_rcp_f32_e32 v171, v114
	v_add_f32_e32 v114, 1.0, v179
	v_rcp_f32_e32 v179, v114
	v_pk_mul_f32 v[134:135], v[134:135], v[160:161]
	v_pk_mul_f32 v[138:139], v[138:139], v[170:171]
	v_pk_mul_f32 v[168:169], v[158:159], v[168:169]
	v_pk_mul_f32 v[166:167], v[166:167], v[178:179]

.LBB0_541:
	s_and_b64 vcc, exec, s[40:41]
	s_cbranch_vccz .LBB0_540
	v_lshlrev_b32_e32 v155, 2, v177
	global_load_dwordx4 v[136:139], v155, s[42:43]
	global_load_dwordx4 v[132:135], v155, s[42:43] offset:16
	s_waitcnt lgkmcnt(0)
	v_mul_f32_e32 v160, v128, v154
	v_mul_f32_e32 v161, v129, v154
	v_mul_f32_e32 v166, v130, v154
	v_mul_f32_e32 v167, v131, v154
	v_mul_f32_e32 v168, v124, v154
	v_mul_f32_e32 v169, v125, v154
	v_mul_f32_e32 v170, v126, v154
	v_mul_f32_e32 v171, v127, v154
	global_load_dwordx4 v[124:127], v155, s[42:43] offset:144
	global_load_dwordx4 v[128:131], v155, s[42:43] offset:128
	v_ashrrev_i32_e32 v153, 31, v152
	v_lshlrev_b64 v[158:159], 12, v[152:153]
	v_max_f32_e32 v153, 0xc2a00000, v160
	v_max_f32_e32 v155, 0xc2a00000, v161
	v_max_f32_e32 v160, 0xc2a00000, v166
	v_max_f32_e32 v161, 0xc2a00000, v167
	v_max_f32_e32 v166, 0xc2a00000, v168
	v_max_f32_e32 v167, 0xc2a00000, v169
	v_max_f32_e32 v168, 0xc2a00000, v170
	v_max_f32_e32 v169, 0xc2a00000, v171
	v_mul_f32_e32 v153, 0xbfb8aa3b, v153
	v_mul_f32_e32 v155, 0xbfb8aa3b, v155
	v_mul_f32_e32 v168, 0xbfb8aa3b, v168
	v_mul_f32_e32 v169, 0xbfb8aa3b, v169
	v_exp_f32_e32 v153, v153
	v_exp_f32_e32 v155, v155
	v_mul_f32_e32 v160, 0xbfb8aa3b, v160
	v_mul_f32_e32 v161, 0xbfb8aa3b, v161
	v_exp_f32_e32 v168, v168
	v_exp_f32_e32 v169, v169
	v_exp_f32_e32 v160, v160
	v_exp_f32_e32 v161, v161
	v_mul_f32_e32 v120, v120, v154
	v_max_f32_e32 v120, 0xc2a00000, v120
	v_add_f32_e32 v153, 1.0, v153
	v_add_f32_e32 v155, 1.0, v155
	v_mul_f32_e32 v121, v121, v154
	v_lshlrev_b32_e32 v114, 1, v177
	v_mul_f32_e32 v166, 0xbfb8aa3b, v166
	v_mul_f32_e32 v167, 0xbfb8aa3b, v167
	v_lshl_add_u64 v[158:159], s[26:27], 0, v[158:159]
	v_add_f32_e32 v168, 1.0, v168
	v_add_f32_e32 v169, 1.0, v169
	v_rcp_f32_e32 v153, v153
	v_rcp_f32_e32 v181, v155
	v_mul_f32_e32 v120, 0xbfb8aa3b, v120
	v_max_f32_e32 v121, 0xc2a00000, v121
	v_exp_f32_e32 v170, v166
	v_exp_f32_e32 v171, v167
	v_lshl_add_u64 v[166:167], v[158:159], 0, v[114:115]
	v_add_f32_e32 v158, 1.0, v160
	v_add_f32_e32 v159, 1.0, v161
	v_rcp_f32_e32 v168, v168
	v_rcp_f32_e32 v182, v169
	v_exp_f32_e32 v120, v120
	v_mul_f32_e32 v121, 0xbfb8aa3b, v121
	v_rcp_f32_e32 v158, v158
	v_rcp_f32_e32 v159, v159
	v_exp_f32_e32 v121, v121
	v_add_f32_e32 v120, 1.0, v120
	v_rcp_f32_e32 v120, v120
	v_mul_f32_e32 v116, v116, v154
	v_add_f32_e32 v121, 1.0, v121
	v_rcp_f32_e32 v121, v121
	v_add_f32_e32 v160, 1.0, v170
	v_add_f32_e32 v161, 1.0, v171
	v_max_f32_e32 v116, 0xc2a00000, v116
	v_mul_f32_e32 v117, v117, v154
	v_rcp_f32_e32 v160, v160
	v_rcp_f32_e32 v161, v161
	v_mul_f32_e32 v116, 0xbfb8aa3b, v116
	v_max_f32_e32 v117, 0xc2a00000, v117
	v_exp_f32_e32 v116, v116
	v_mul_f32_e32 v117, 0xbfb8aa3b, v117
	v_exp_f32_e32 v117, v117
	s_mov_b64 s[14:15], 0x80000
	v_add_f32_e32 v116, 1.0, v116
	v_rcp_f32_e32 v116, v116
	v_add_f32_e32 v117, 1.0, v117
	s_waitcnt vmcnt(0)
	v_sub_f32_e32 v180, 1.0, v136
	v_sub_f32_e32 v179, 1.0, v137
	v_sub_f32_e32 v169, 1.0, v134
	v_sub_f32_e32 v155, 1.0, v135
	v_fma_f32 v153, v180, v153, v136
	v_fma_f32 v181, v179, v181, v137
	v_sub_f32_e32 v178, 1.0, v138
	v_sub_f32_e32 v177, 1.0, v139
	v_fma_f32 v168, v169, v168, v134
	v_fma_f32 v182, v155, v182, v135
	v_log_f32_e32 v153, v153
	v_log_f32_e32 v181, v181
	v_fma_f32 v158, v178, v158, v138
	v_fma_f32 v159, v177, v159, v139
	v_log_f32_e32 v168, v168
	v_log_f32_e32 v182, v182
	v_log_f32_e32 v158, v158
	v_log_f32_e32 v159, v159
	v_cvt_pk_f16_f32 v194, v153, v181
	v_sub_f32_e32 v153, 1.0, v128
	v_cvt_pk_f16_f32 v197, v168, v182
	v_fma_f32 v120, v153, v120, v128
	v_sub_f32_e32 v168, 1.0, v129
	v_cvt_pk_f16_f32 v195, v158, v159
	v_log_f32_e32 v158, v120
	v_fma_f32 v120, v168, v121, v129
	v_log_f32_e32 v159, v120
	v_mul_f32_e32 v120, v122, v154
	v_max_f32_e32 v120, 0xc2a00000, v120
	v_mul_f32_e32 v121, v123, v154
	v_mul_f32_e32 v120, 0xbfb8aa3b, v120
	v_max_f32_e32 v121, 0xc2a00000, v121
	v_exp_f32_e32 v120, v120
	v_mul_f32_e32 v121, 0xbfb8aa3b, v121
	v_exp_f32_e32 v122, v121
	v_sub_f32_e32 v171, 1.0, v132
	v_sub_f32_e32 v170, 1.0, v133
	v_add_f32_e32 v120, 1.0, v120
	v_fma_f32 v160, v171, v160, v132
	v_fma_f32 v161, v170, v161, v133
	v_rcp_f32_e32 v120, v120
	v_add_f32_e32 v122, 1.0, v122
	v_log_f32_e32 v160, v160
	v_log_f32_e32 v161, v161
	v_rcp_f32_e32 v123, v122
	v_sub_f32_e32 v121, 1.0, v130
	v_rcp_f32_e32 v117, v117
	v_fma_f32 v120, v121, v120, v130
	v_sub_f32_e32 v122, 1.0, v131
	v_cvt_pk_f16_f32 v196, v160, v161
	v_log_f32_e32 v160, v120
	v_fma_f32 v120, v122, v123, v131
	v_sub_f32_e32 v123, 1.0, v124
	v_log_f32_e32 v161, v120
	v_fma_f32 v116, v123, v116, v124
	v_sub_f32_e32 v120, 1.0, v125
	v_log_f32_e32 v181, v116
	v_fma_f32 v116, v120, v117, v125
	v_log_f32_e32 v182, v116
	v_mul_f32_e32 v116, v118, v154
	v_max_f32_e32 v116, 0xc2a00000, v116
	v_mul_f32_e32 v117, v119, v154
	v_mul_f32_e32 v116, 0xbfb8aa3b, v116
	v_max_f32_e32 v117, 0xc2a00000, v117
	v_exp_f32_e32 v116, v116
	v_mul_f32_e32 v117, 0xbfb8aa3b, v117
	v_exp_f32_e32 v117, v117
	v_sub_f32_e32 v118, 1.0, v126
	v_add_f32_e32 v116, 1.0, v116
	v_rcp_f32_e32 v116, v116
	v_add_f32_e32 v117, 1.0, v117
	v_rcp_f32_e32 v117, v117
	v_sub_f32_e32 v119, 1.0, v127
	v_fma_f32 v116, v118, v116, v126
	v_log_f32_e32 v154, v116
	v_fma_f32 v116, v119, v117, v127
	v_log_f32_e32 v183, v116
	ds_read2_b32 v[116:117], v176 offset0:16 offset1:32
	ds_bpermute_b32 v238, v250, v194
	ds_bpermute_b32 v239, v250, v195
	ds_bpermute_b32 v240, v250, v196
	ds_bpermute_b32 v241, v250, v197
	ds_bpermute_b32 v242, v250, v166
	s_waitcnt lgkmcnt(0)
	v_mul_f32_e32 v106, v106, v116
	v_max_f32_e32 v106, 0xc2a00000, v106
	v_mul_f32_e32 v106, 0xbfb8aa3b, v106
	v_exp_f32_e32 v106, v106
	v_mul_f32_e32 v110, v110, v116
	v_max_f32_e32 v110, 0xc2a00000, v110
	v_mul_f32_e32 v111, v111, v116
	v_mul_f32_e32 v110, 0xbfb8aa3b, v110
	v_max_f32_e32 v111, 0xc2a00000, v111
	v_mul_f32_e32 v107, v107, v116
	v_exp_f32_e32 v110, v110
	v_mul_f32_e32 v111, 0xbfb8aa3b, v111
	v_add_f32_e32 v106, 1.0, v106
	v_max_f32_e32 v107, 0xc2a00000, v107
	v_exp_f32_e32 v111, v111
	v_rcp_f32_e32 v106, v106
	v_mul_f32_e32 v107, 0xbfb8aa3b, v107
	v_exp_f32_e32 v107, v107
	v_cvt_pk_f16_f32 v194, v158, v159
	v_or_b32_e32 v158, 16, v152
	v_add_f32_e32 v110, 1.0, v110
	v_mul_f32_e32 v112, v112, v116
	v_mul_f32_e32 v113, v113, v116
	v_cvt_pk_f16_f32 v197, v154, v183
	v_ashrrev_i32_e32 v159, 31, v158
	v_rcp_f32_e32 v154, v110
	v_add_f32_e32 v110, 1.0, v111
	v_max_f32_e32 v112, 0xc2a00000, v112
	v_max_f32_e32 v113, 0xc2a00000, v113
	v_fma_f32 v106, v171, v106, v132
	v_cvt_pk_f16_f32 v195, v160, v161
	v_rcp_f32_e32 v160, v110
	v_lshlrev_b64 v[110:111], 12, v[158:159]
	v_mul_f32_e32 v112, 0xbfb8aa3b, v112
	v_mul_f32_e32 v113, 0xbfb8aa3b, v113
	v_log_f32_e32 v159, v106
	v_add_f32_e32 v106, 1.0, v107
	v_mul_f32_e32 v107, v108, v116
	v_exp_f32_e32 v112, v112
	v_exp_f32_e32 v113, v113
	v_max_f32_e32 v107, 0xc2a00000, v107
	v_mul_f32_e32 v108, v109, v116
	v_mul_f32_e32 v107, 0xbfb8aa3b, v107
	v_max_f32_e32 v108, 0xc2a00000, v108
	v_exp_f32_e32 v107, v107
	v_mul_f32_e32 v108, 0xbfb8aa3b, v108
	v_exp_f32_e32 v108, v108
	v_add_f32_e32 v112, 1.0, v112
	v_add_f32_e32 v113, 1.0, v113
	v_rcp_f32_e32 v112, v112
	v_rcp_f32_e32 v113, v113
	v_mul_f32_e32 v98, v98, v116
	v_rcp_f32_e32 v106, v106
	v_add_f32_e32 v107, 1.0, v107
	v_max_f32_e32 v98, 0xc2a00000, v98
	v_rcp_f32_e32 v107, v107
	v_add_f32_e32 v108, 1.0, v108
	v_mul_f32_e32 v98, 0xbfb8aa3b, v98
	v_rcp_f32_e32 v108, v108
	v_exp_f32_e32 v98, v98
	v_fma_f32 v112, v178, v112, v138
	v_fma_f32 v113, v177, v113, v139
	v_log_f32_e32 v112, v112
	v_log_f32_e32 v113, v113
	v_fma_f32 v106, v170, v106, v133
	v_log_f32_e32 v109, v106
	v_fma_f32 v106, v169, v107, v134
	v_mul_f32_e32 v102, v102, v116
	v_mul_f32_e32 v99, v99, v116
	v_fma_f32 v154, v180, v154, v136
	v_fma_f32 v158, v179, v160, v137
	v_log_f32_e32 v160, v106
	v_fma_f32 v106, v155, v108, v135
	v_max_f32_e32 v102, 0xc2a00000, v102
	v_add_f32_e32 v98, 1.0, v98
	v_max_f32_e32 v99, 0xc2a00000, v99
	v_log_f32_e32 v154, v154
	v_log_f32_e32 v158, v158
	v_log_f32_e32 v161, v106
	v_mul_f32_e32 v102, 0xbfb8aa3b, v102
	v_rcp_f32_e32 v98, v98
	v_mul_f32_e32 v99, 0xbfb8aa3b, v99
	v_cvt_pk_f16_f32 v107, v112, v113
	v_exp_f32_e32 v112, v102
	v_mul_f32_e32 v102, v103, v116
	v_exp_f32_e32 v99, v99
	v_max_f32_e32 v102, 0xc2a00000, v102
	v_lshl_add_u64 v[110:111], s[26:27], 0, v[110:111]
	v_mul_f32_e32 v102, 0xbfb8aa3b, v102
	v_cvt_pk_f16_f32 v106, v154, v158
	v_cvt_pk_f16_f32 v108, v159, v109
	v_cvt_pk_f16_f32 v109, v160, v161
	v_exp_f32_e32 v113, v102
	v_lshl_add_u64 v[102:103], v[110:111], 0, v[114:115]
	v_fma_f32 v98, v123, v98, v124
	ds_bpermute_b32 v244, v250, v106
	ds_bpermute_b32 v245, v250, v107
	ds_bpermute_b32 v246, v250, v108
	ds_bpermute_b32 v247, v250, v109
	ds_bpermute_b32 v248, v250, v102
	v_mul_f32_e32 v104, v104, v116
	v_mul_f32_e32 v105, v105, v116
	v_log_f32_e32 v108, v98
	v_add_f32_e32 v98, 1.0, v99
	v_mul_f32_e32 v99, v100, v116
	v_max_f32_e32 v99, 0xc2a00000, v99
	v_mul_f32_e32 v100, v101, v116
	v_max_f32_e32 v104, 0xc2a00000, v104
	v_max_f32_e32 v105, 0xc2a00000, v105
	v_mul_f32_e32 v99, 0xbfb8aa3b, v99
	v_max_f32_e32 v100, 0xc2a00000, v100
	v_mul_f32_e32 v104, 0xbfb8aa3b, v104
	v_mul_f32_e32 v105, 0xbfb8aa3b, v105
	v_exp_f32_e32 v99, v99
	v_mul_f32_e32 v100, 0xbfb8aa3b, v100
	v_exp_f32_e32 v104, v104
	v_exp_f32_e32 v105, v105
	v_exp_f32_e32 v100, v100
	v_rcp_f32_e32 v98, v98
	v_add_f32_e32 v99, 1.0, v99
	v_add_f32_e32 v110, 1.0, v112
	v_add_f32_e32 v111, 1.0, v113
	v_add_f32_e32 v104, 1.0, v104
	v_add_f32_e32 v105, 1.0, v105
	v_rcp_f32_e32 v99, v99
	v_add_f32_e32 v100, 1.0, v100
	v_rcp_f32_e32 v110, v110
	v_rcp_f32_e32 v111, v111
	v_rcp_f32_e32 v104, v104
	v_rcp_f32_e32 v105, v105
	v_rcp_f32_e32 v100, v100
	v_mul_f32_e32 v90, v90, v117
	v_fma_f32 v98, v120, v98, v125
	v_mul_f32_e32 v94, v94, v117
	v_max_f32_e32 v90, 0xc2a00000, v90
	v_log_f32_e32 v101, v98
	v_fma_f32 v98, v118, v99, v126
	v_max_f32_e32 v94, 0xc2a00000, v94
	v_mul_f32_e32 v90, 0xbfb8aa3b, v90
	v_fma_f32 v106, v153, v110, v128
	v_fma_f32 v107, v168, v111, v129
	v_fma_f32 v104, v121, v104, v130
	v_fma_f32 v105, v122, v105, v131
	v_log_f32_e32 v109, v98
	v_fma_f32 v98, v119, v100, v127
	v_mul_f32_e32 v94, 0xbfb8aa3b, v94
	v_exp_f32_e32 v90, v90
	v_log_f32_e32 v106, v106
	v_log_f32_e32 v107, v107
	v_log_f32_e32 v104, v104
	v_log_f32_e32 v105, v105
	v_log_f32_e32 v110, v98
	v_exp_f32_e32 v94, v94
	v_mul_f32_e32 v95, v95, v117
	v_max_f32_e32 v95, 0xc2a00000, v95
	v_mul_f32_e32 v91, v91, v117
	v_mul_f32_e32 v95, 0xbfb8aa3b, v95
	v_add_f32_e32 v90, 1.0, v90
	v_max_f32_e32 v91, 0xc2a00000, v91
	v_cvt_pk_f16_f32 v98, v106, v107
	v_cvt_pk_f16_f32 v99, v104, v105
	v_cvt_pk_f16_f32 v100, v108, v101
	v_cvt_pk_f16_f32 v101, v109, v110
	v_exp_f32_e32 v95, v95
	v_add_f32_e32 v94, 1.0, v94
	v_rcp_f32_e32 v90, v90
	v_mul_f32_e32 v91, 0xbfb8aa3b, v91
	s_waitcnt lgkmcnt(5)
	v_subrev_u32_e32 v242, s82, v242
	global_store_dwordx4 v242, v[238:241], s[82:83] sc0 sc1
	ds_bpermute_b32 v232, v250, v98
	ds_bpermute_b32 v233, v250, v99
	ds_bpermute_b32 v234, v250, v100
	ds_bpermute_b32 v235, v250, v101
	ds_bpermute_b32 v236, v250, v102
	v_exp_f32_e32 v91, v91
	v_fma_f32 v90, v171, v90, v132
	v_rcp_f32_e32 v100, v94
	v_or_b32_e32 v98, 32, v152
	v_ashrrev_i32_e32 v99, 31, v98
	v_add_f32_e32 v94, 1.0, v95
	v_rcp_f32_e32 v101, v94
	v_lshlrev_b64 v[94:95], 12, v[98:99]
	v_fma_f32 v98, v180, v100, v136
	v_log_f32_e32 v100, v90
	v_add_f32_e32 v90, 1.0, v91
	v_mul_f32_e32 v91, v92, v117
	v_mul_f32_e32 v96, v96, v117
	v_mul_f32_e32 v97, v97, v117
	v_max_f32_e32 v91, 0xc2a00000, v91
	v_mul_f32_e32 v92, v93, v117
	v_max_f32_e32 v96, 0xc2a00000, v96
	v_max_f32_e32 v97, 0xc2a00000, v97
	v_mul_f32_e32 v91, 0xbfb8aa3b, v91
	v_max_f32_e32 v92, 0xc2a00000, v92
	v_mul_f32_e32 v96, 0xbfb8aa3b, v96
	v_mul_f32_e32 v97, 0xbfb8aa3b, v97
	v_exp_f32_e32 v91, v91
	v_mul_f32_e32 v92, 0xbfb8aa3b, v92
	v_exp_f32_e32 v96, v96
	v_exp_f32_e32 v97, v97
	v_exp_f32_e32 v92, v92
	v_mul_f32_e32 v82, v82, v117
	v_rcp_f32_e32 v90, v90
	v_add_f32_e32 v91, 1.0, v91
	v_max_f32_e32 v82, 0xc2a00000, v82
	v_add_f32_e32 v96, 1.0, v96
	v_add_f32_e32 v97, 1.0, v97
	v_rcp_f32_e32 v91, v91
	v_add_f32_e32 v92, 1.0, v92
	v_mul_f32_e32 v82, 0xbfb8aa3b, v82
	v_rcp_f32_e32 v96, v96
	v_rcp_f32_e32 v97, v97
	v_rcp_f32_e32 v92, v92
	v_exp_f32_e32 v82, v82
	v_fma_f32 v90, v170, v90, v133
	v_log_f32_e32 v93, v90
	v_fma_f32 v90, v169, v91, v134
	v_mul_f32_e32 v83, v83, v117
	v_fma_f32 v99, v179, v101, v137
	v_fma_f32 v96, v178, v96, v138
	v_fma_f32 v97, v177, v97, v139
	v_log_f32_e32 v101, v90
	v_fma_f32 v90, v155, v92, v135
	v_add_f32_e32 v82, 1.0, v82
	v_max_f32_e32 v83, 0xc2a00000, v83
	v_log_f32_e32 v98, v98
	v_log_f32_e32 v99, v99
	v_log_f32_e32 v96, v96
	v_log_f32_e32 v97, v97
	v_log_f32_e32 v102, v90
	v_rcp_f32_e32 v82, v82
	v_mul_f32_e32 v83, 0xbfb8aa3b, v83
	v_exp_f32_e32 v83, v83
	v_lshl_add_u64 v[94:95], s[26:27], 0, v[94:95]
	v_cvt_pk_f16_f32 v90, v98, v99
	v_cvt_pk_f16_f32 v91, v96, v97
	v_cvt_pk_f16_f32 v92, v100, v93
	v_cvt_pk_f16_f32 v93, v101, v102
	v_lshl_add_u64 v[94:95], v[94:95], 0, v[114:115]
	v_fma_f32 v82, v123, v82, v124
	s_waitcnt lgkmcnt(5)
	v_subrev_u32_e32 v248, s82, v248
	global_store_dwordx4 v248, v[244:247], s[82:83] sc0 sc1
	ds_bpermute_b32 v238, v250, v90
	ds_bpermute_b32 v239, v250, v91
	ds_bpermute_b32 v240, v250, v92
	ds_bpermute_b32 v241, v250, v93
	ds_bpermute_b32 v242, v250, v94
	v_mul_f32_e32 v86, v86, v117
	v_mul_f32_e32 v87, v87, v117
	v_log_f32_e32 v90, v82
	v_add_f32_e32 v82, 1.0, v83
	v_mul_f32_e32 v83, v84, v117
	v_max_f32_e32 v83, 0xc2a00000, v83
	v_mul_f32_e32 v84, v85, v117
	v_mul_f32_e32 v83, 0xbfb8aa3b, v83
	v_max_f32_e32 v84, 0xc2a00000, v84
	v_exp_f32_e32 v83, v83
	v_mul_f32_e32 v84, 0xbfb8aa3b, v84
	v_exp_f32_e32 v84, v84
	v_rcp_f32_e32 v82, v82
	v_add_f32_e32 v83, 1.0, v83
	v_rcp_f32_e32 v83, v83
	v_add_f32_e32 v84, 1.0, v84
	v_rcp_f32_e32 v84, v84
	v_mul_f32_e32 v88, v88, v117
	v_mul_f32_e32 v89, v89, v117
	v_max_f32_e32 v86, 0xc2a00000, v86
	v_max_f32_e32 v87, 0xc2a00000, v87
	v_max_f32_e32 v88, 0xc2a00000, v88
	v_max_f32_e32 v89, 0xc2a00000, v89
	v_fma_f32 v82, v120, v82, v125
	v_mul_f32_e32 v86, 0xbfb8aa3b, v86
	v_mul_f32_e32 v87, 0xbfb8aa3b, v87
	v_mul_f32_e32 v88, 0xbfb8aa3b, v88
	v_mul_f32_e32 v89, 0xbfb8aa3b, v89
	v_log_f32_e32 v91, v82
	v_fma_f32 v82, v118, v83, v126
	v_exp_f32_e32 v86, v86
	v_exp_f32_e32 v87, v87
	v_exp_f32_e32 v88, v88
	v_exp_f32_e32 v89, v89
	v_log_f32_e32 v92, v82
	v_fma_f32 v82, v119, v84, v127
	v_log_f32_e32 v93, v82
	ds_read2_b32 v[82:83], v176 offset0:48 offset1:128
	v_add_f32_e32 v86, 1.0, v86
	v_add_f32_e32 v87, 1.0, v87
	v_add_f32_e32 v88, 1.0, v88
	v_add_f32_e32 v89, 1.0, v89
	v_rcp_f32_e32 v86, v86
	v_rcp_f32_e32 v87, v87
	v_rcp_f32_e32 v88, v88
	v_rcp_f32_e32 v89, v89
	s_waitcnt lgkmcnt(0)
	v_mul_f32_e32 v74, v74, v82
	v_mul_f32_e32 v78, v78, v82
	v_max_f32_e32 v74, 0xc2a00000, v74
	v_max_f32_e32 v78, 0xc2a00000, v78
	v_mul_f32_e32 v74, 0xbfb8aa3b, v74
	v_fma_f32 v86, v153, v86, v128
	v_fma_f32 v87, v168, v87, v129
	v_fma_f32 v88, v121, v88, v130
	v_fma_f32 v89, v122, v89, v131
	v_mul_f32_e32 v78, 0xbfb8aa3b, v78
	v_exp_f32_e32 v74, v74
	v_log_f32_e32 v86, v86
	v_log_f32_e32 v87, v87
	v_log_f32_e32 v88, v88
	v_log_f32_e32 v89, v89
	v_exp_f32_e32 v78, v78
	v_mul_f32_e32 v79, v79, v82
	v_max_f32_e32 v79, 0xc2a00000, v79
	v_mul_f32_e32 v75, v75, v82
	v_mul_f32_e32 v79, 0xbfb8aa3b, v79
	v_add_f32_e32 v74, 1.0, v74
	v_max_f32_e32 v75, 0xc2a00000, v75
	v_cvt_pk_f16_f32 v84, v86, v87
	v_cvt_pk_f16_f32 v85, v88, v89
	v_cvt_pk_f16_f32 v86, v90, v91
	v_cvt_pk_f16_f32 v87, v92, v93
	v_exp_f32_e32 v79, v79
	v_add_f32_e32 v78, 1.0, v78
	v_rcp_f32_e32 v74, v74
	v_mul_f32_e32 v75, 0xbfb8aa3b, v75
	s_waitcnt lgkmcnt(6)
	v_subrev_u32_e32 v236, s82, v236
	global_store_dwordx4 v236, v[232:235], s[82:83] offset:64 sc0 sc1
	ds_bpermute_b32 v244, v250, v84
	ds_bpermute_b32 v245, v250, v85
	ds_bpermute_b32 v246, v250, v86
	ds_bpermute_b32 v247, v250, v87
	ds_bpermute_b32 v248, v250, v94
	v_exp_f32_e32 v75, v75
	v_mul_f32_e32 v80, v80, v82
	v_rcp_f32_e32 v86, v78
	v_or_b32_e32 v84, 48, v152
	v_mul_f32_e32 v81, v81, v82
	v_ashrrev_i32_e32 v85, 31, v84
	v_add_f32_e32 v78, 1.0, v79
	v_max_f32_e32 v80, 0xc2a00000, v80
	v_max_f32_e32 v81, 0xc2a00000, v81
	v_fma_f32 v74, v171, v74, v132
	v_rcp_f32_e32 v87, v78
	v_lshlrev_b64 v[78:79], 12, v[84:85]
	v_fma_f32 v84, v180, v86, v136
	v_mul_f32_e32 v80, 0xbfb8aa3b, v80
	v_mul_f32_e32 v81, 0xbfb8aa3b, v81
	v_log_f32_e32 v86, v74
	v_add_f32_e32 v74, 1.0, v75
	v_mul_f32_e32 v75, v76, v82
	v_exp_f32_e32 v80, v80
	v_exp_f32_e32 v81, v81
	v_max_f32_e32 v75, 0xc2a00000, v75
	v_mul_f32_e32 v76, v77, v82
	v_mul_f32_e32 v75, 0xbfb8aa3b, v75
	v_max_f32_e32 v76, 0xc2a00000, v76
	v_exp_f32_e32 v75, v75
	v_mul_f32_e32 v76, 0xbfb8aa3b, v76
	v_exp_f32_e32 v76, v76
	v_add_f32_e32 v80, 1.0, v80
	v_add_f32_e32 v81, 1.0, v81
	v_rcp_f32_e32 v80, v80
	v_rcp_f32_e32 v81, v81
	v_mul_f32_e32 v66, v66, v82
	v_rcp_f32_e32 v74, v74
	v_add_f32_e32 v75, 1.0, v75
	v_max_f32_e32 v66, 0xc2a00000, v66
	v_rcp_f32_e32 v75, v75
	v_add_f32_e32 v76, 1.0, v76
	v_mul_f32_e32 v66, 0xbfb8aa3b, v66
	v_rcp_f32_e32 v76, v76
	v_exp_f32_e32 v66, v66
	v_fma_f32 v80, v178, v80, v138
	v_fma_f32 v81, v177, v81, v139
	v_log_f32_e32 v80, v80
	v_log_f32_e32 v81, v81
	v_fma_f32 v74, v170, v74, v133
	v_log_f32_e32 v77, v74
	v_fma_f32 v74, v169, v75, v134
	v_mul_f32_e32 v70, v70, v82
	v_mul_f32_e32 v67, v67, v82
	v_fma_f32 v85, v179, v87, v137
	v_log_f32_e32 v87, v74
	v_fma_f32 v74, v155, v76, v135
	v_max_f32_e32 v70, 0xc2a00000, v70
	v_add_f32_e32 v66, 1.0, v66
	v_max_f32_e32 v67, 0xc2a00000, v67
	v_log_f32_e32 v84, v84
	v_log_f32_e32 v85, v85
	v_log_f32_e32 v88, v74
	v_mul_f32_e32 v70, 0xbfb8aa3b, v70
	v_rcp_f32_e32 v66, v66
	v_mul_f32_e32 v67, 0xbfb8aa3b, v67
	v_cvt_pk_f16_f32 v75, v80, v81
	v_exp_f32_e32 v80, v70
	v_mul_f32_e32 v70, v71, v82
	v_exp_f32_e32 v67, v67
	v_max_f32_e32 v70, 0xc2a00000, v70
	v_lshl_add_u64 v[78:79], s[26:27], 0, v[78:79]
	v_mul_f32_e32 v70, 0xbfb8aa3b, v70
	v_cvt_pk_f16_f32 v74, v84, v85
	v_cvt_pk_f16_f32 v76, v86, v77
	v_cvt_pk_f16_f32 v77, v87, v88
	v_exp_f32_e32 v81, v70
	v_lshl_add_u64 v[70:71], v[78:79], 0, v[114:115]
	v_fma_f32 v66, v123, v66, v124
	s_waitcnt lgkmcnt(6)
	v_subrev_u32_e32 v242, s82, v242
	global_store_dwordx4 v242, v[238:241], s[82:83] sc0 sc1
	ds_bpermute_b32 v232, v250, v74
	ds_bpermute_b32 v233, v250, v75
	ds_bpermute_b32 v234, v250, v76
	ds_bpermute_b32 v235, v250, v77
	ds_bpermute_b32 v236, v250, v70
	v_mul_f32_e32 v72, v72, v82
	v_mul_f32_e32 v73, v73, v82
	v_log_f32_e32 v76, v66
	v_add_f32_e32 v66, 1.0, v67
	v_mul_f32_e32 v67, v68, v82
	v_max_f32_e32 v67, 0xc2a00000, v67
	v_mul_f32_e32 v68, v69, v82
	v_max_f32_e32 v72, 0xc2a00000, v72
	v_max_f32_e32 v73, 0xc2a00000, v73
	v_mul_f32_e32 v67, 0xbfb8aa3b, v67
	v_max_f32_e32 v68, 0xc2a00000, v68
	v_mul_f32_e32 v72, 0xbfb8aa3b, v72
	v_mul_f32_e32 v73, 0xbfb8aa3b, v73
	v_exp_f32_e32 v67, v67
	v_mul_f32_e32 v68, 0xbfb8aa3b, v68
	v_exp_f32_e32 v72, v72
	v_exp_f32_e32 v73, v73
	v_exp_f32_e32 v68, v68
	v_mul_f32_e32 v58, v58, v83
	v_rcp_f32_e32 v66, v66
	v_add_f32_e32 v67, 1.0, v67
	v_max_f32_e32 v58, 0xc2a00000, v58
	v_add_f32_e32 v78, 1.0, v80
	v_add_f32_e32 v79, 1.0, v81
	v_add_f32_e32 v72, 1.0, v72
	v_add_f32_e32 v73, 1.0, v73
	v_rcp_f32_e32 v67, v67
	v_add_f32_e32 v68, 1.0, v68
	v_mul_f32_e32 v58, 0xbfb8aa3b, v58
	v_rcp_f32_e32 v78, v78
	v_rcp_f32_e32 v79, v79
	v_rcp_f32_e32 v72, v72
	v_rcp_f32_e32 v73, v73
	v_rcp_f32_e32 v68, v68
	v_exp_f32_e32 v58, v58
	v_fma_f32 v66, v120, v66, v125
	v_log_f32_e32 v69, v66
	v_fma_f32 v66, v118, v67, v126
	v_mul_f32_e32 v59, v59, v83
	v_fma_f32 v74, v153, v78, v128
	v_fma_f32 v75, v168, v79, v129
	v_fma_f32 v72, v121, v72, v130
	v_fma_f32 v73, v122, v73, v131
	v_log_f32_e32 v77, v66
	v_fma_f32 v66, v119, v68, v127
	v_add_f32_e32 v58, 1.0, v58
	v_max_f32_e32 v59, 0xc2a00000, v59
	v_log_f32_e32 v74, v74
	v_log_f32_e32 v75, v75
	v_log_f32_e32 v72, v72
	v_log_f32_e32 v73, v73
	v_log_f32_e32 v78, v66
	v_rcp_f32_e32 v58, v58
	v_mul_f32_e32 v59, 0xbfb8aa3b, v59
	v_exp_f32_e32 v59, v59
	v_mul_f32_e32 v64, v64, v83
	v_mul_f32_e32 v65, v65, v83
	v_max_f32_e32 v64, 0xc2a00000, v64
	v_max_f32_e32 v65, 0xc2a00000, v65
	v_cvt_pk_f16_f32 v66, v74, v75
	v_cvt_pk_f16_f32 v67, v72, v73
	v_cvt_pk_f16_f32 v68, v76, v69
	v_mul_f32_e32 v62, v62, v83
	v_mul_f32_e32 v63, v63, v83
	v_cvt_pk_f16_f32 v69, v77, v78
	v_mul_f32_e32 v64, 0xbfb8aa3b, v64
	v_mul_f32_e32 v65, 0xbfb8aa3b, v65
	v_fma_f32 v58, v171, v58, v132
	v_max_f32_e32 v62, 0xc2a00000, v62
	v_max_f32_e32 v63, 0xc2a00000, v63
	s_waitcnt lgkmcnt(5)
	v_subrev_u32_e32 v248, s82, v248
	global_store_dwordx4 v248, v[244:247], s[82:83] offset:64 sc0 sc1
	ds_bpermute_b32 v238, v250, v66
	ds_bpermute_b32 v239, v250, v67
	ds_bpermute_b32 v240, v250, v68
	ds_bpermute_b32 v241, v250, v69
	ds_bpermute_b32 v242, v250, v70
	v_exp_f32_e32 v64, v64
	v_exp_f32_e32 v65, v65
	v_log_f32_e32 v66, v58
	v_add_f32_e32 v58, 1.0, v59
	v_mul_f32_e32 v59, v60, v83
	v_mul_f32_e32 v62, 0xbfb8aa3b, v62
	v_mul_f32_e32 v63, 0xbfb8aa3b, v63
	v_max_f32_e32 v59, 0xc2a00000, v59
	v_mul_f32_e32 v60, v61, v83
	v_exp_f32_e32 v62, v62
	v_exp_f32_e32 v63, v63
	v_mul_f32_e32 v59, 0xbfb8aa3b, v59
	v_max_f32_e32 v60, 0xc2a00000, v60
	v_exp_f32_e32 v59, v59
	v_mul_f32_e32 v60, 0xbfb8aa3b, v60
	v_add_f32_e32 v64, 1.0, v64
	v_add_f32_e32 v65, 1.0, v65
	v_exp_f32_e32 v60, v60
	v_rcp_f32_e32 v64, v64
	v_rcp_f32_e32 v65, v65
	v_add_f32_e32 v62, 1.0, v62
	v_add_f32_e32 v63, 1.0, v63
	v_mul_f32_e32 v50, v50, v83
	v_rcp_f32_e32 v62, v62
	v_rcp_f32_e32 v63, v63
	v_rcp_f32_e32 v58, v58
	v_add_f32_e32 v59, 1.0, v59
	v_max_f32_e32 v50, 0xc2a00000, v50
	v_rcp_f32_e32 v59, v59
	v_add_f32_e32 v60, 1.0, v60
	v_mul_f32_e32 v50, 0xbfb8aa3b, v50
	v_fma_f32 v64, v178, v64, v138
	v_fma_f32 v65, v177, v65, v139
	v_rcp_f32_e32 v60, v60
	v_exp_f32_e32 v50, v50
	v_log_f32_e32 v64, v64
	v_log_f32_e32 v65, v65
	v_fma_f32 v62, v180, v62, v136
	v_fma_f32 v63, v179, v63, v137
	v_fma_f32 v58, v170, v58, v133
	v_mul_f32_e32 v54, v54, v83
	v_log_f32_e32 v62, v62
	v_log_f32_e32 v63, v63
	v_log_f32_e32 v61, v58
	v_fma_f32 v58, v169, v59, v134
	v_max_f32_e32 v54, 0xc2a00000, v54
	v_mul_f32_e32 v51, v51, v83
	v_log_f32_e32 v67, v58
	v_fma_f32 v58, v155, v60, v135
	v_mul_f32_e32 v54, 0xbfb8aa3b, v54
	v_add_f32_e32 v50, 1.0, v50
	v_max_f32_e32 v51, 0xc2a00000, v51
	v_log_f32_e32 v68, v58
	v_cvt_pk_f16_f32 v59, v64, v65
	v_exp_f32_e32 v64, v54
	v_mul_f32_e32 v54, v55, v83
	v_rcp_f32_e32 v50, v50
	v_mul_f32_e32 v51, 0xbfb8aa3b, v51
	v_max_f32_e32 v54, 0xc2a00000, v54
	v_exp_f32_e32 v51, v51
	v_cvt_pk_f16_f32 v58, v62, v63
	v_lshl_add_u64 v[62:63], v[166:167], 0, s[14:15]
	v_mul_f32_e32 v54, 0xbfb8aa3b, v54
	s_mov_b32 s14, 0x80000
	v_exp_f32_e32 v65, v54
	v_add_co_u32_e32 v54, vcc, s14, v166
	v_cvt_pk_f16_f32 v60, v66, v61
	v_cvt_pk_f16_f32 v61, v67, v68
	v_addc_co_u32_e32 v55, vcc, 0, v167, vcc
	v_fma_f32 v50, v123, v50, v124
	s_waitcnt lgkmcnt(5)
	v_subrev_u32_e32 v236, s82, v236
	global_store_dwordx4 v236, v[232:235], s[82:83] sc0 sc1
	ds_bpermute_b32 v244, v250, v58
	ds_bpermute_b32 v245, v250, v59
	ds_bpermute_b32 v246, v250, v60
	ds_bpermute_b32 v247, v250, v61
	ds_bpermute_b32 v248, v250, v54
	v_mul_f32_e32 v56, v56, v83
	v_mul_f32_e32 v57, v57, v83
	v_log_f32_e32 v58, v50
	v_add_f32_e32 v50, 1.0, v51
	v_mul_f32_e32 v51, v52, v83
	v_max_f32_e32 v51, 0xc2a00000, v51
	v_mul_f32_e32 v51, 0xbfb8aa3b, v51
	v_exp_f32_e32 v51, v51
	v_rcp_f32_e32 v50, v50
	v_mul_f32_e32 v52, v53, v83
	v_max_f32_e32 v56, 0xc2a00000, v56
	v_add_f32_e32 v51, 1.0, v51
	v_rcp_f32_e32 v51, v51
	v_fma_f32 v50, v120, v50, v125
	v_log_f32_e32 v59, v50
	v_max_f32_e32 v57, 0xc2a00000, v57
	v_fma_f32 v50, v118, v51, v126
	v_log_f32_e32 v60, v50
	ds_read2_b32 v[50:51], v176 offset0:144 offset1:160
	v_max_f32_e32 v52, 0xc2a00000, v52
	v_mul_f32_e32 v56, 0xbfb8aa3b, v56
	v_mul_f32_e32 v57, 0xbfb8aa3b, v57
	v_mul_f32_e32 v52, 0xbfb8aa3b, v52
	v_exp_f32_e32 v56, v56
	v_exp_f32_e32 v57, v57
	v_exp_f32_e32 v52, v52
	s_waitcnt lgkmcnt(0)
	v_mul_f32_e32 v42, v42, v50
	v_max_f32_e32 v42, 0xc2a00000, v42
	v_add_f32_e32 v64, 1.0, v64
	v_add_f32_e32 v65, 1.0, v65
	v_add_f32_e32 v56, 1.0, v56
	v_add_f32_e32 v57, 1.0, v57
	v_add_f32_e32 v52, 1.0, v52
	v_mul_f32_e32 v42, 0xbfb8aa3b, v42
	v_rcp_f32_e32 v64, v64
	v_rcp_f32_e32 v65, v65
	v_rcp_f32_e32 v56, v56
	v_rcp_f32_e32 v57, v57
	v_rcp_f32_e32 v52, v52
	v_exp_f32_e32 v42, v42
	v_mul_f32_e32 v43, v43, v50
	v_fma_f32 v54, v153, v64, v128
	v_fma_f32 v55, v168, v65, v129
	v_fma_f32 v56, v121, v56, v130
	v_fma_f32 v57, v122, v57, v131
	v_fma_f32 v52, v119, v52, v127
	v_add_f32_e32 v42, 1.0, v42
	v_max_f32_e32 v43, 0xc2a00000, v43
	v_log_f32_e32 v54, v54
	v_log_f32_e32 v55, v55
	v_log_f32_e32 v56, v56
	v_log_f32_e32 v57, v57
	v_log_f32_e32 v61, v52
	v_rcp_f32_e32 v42, v42
	v_mul_f32_e32 v43, 0xbfb8aa3b, v43
	v_exp_f32_e32 v43, v43
	v_mul_f32_e32 v48, v48, v50
	v_mul_f32_e32 v49, v49, v50
	v_max_f32_e32 v48, 0xc2a00000, v48
	v_max_f32_e32 v49, 0xc2a00000, v49
	v_cvt_pk_f16_f32 v52, v54, v55
	v_cvt_pk_f16_f32 v53, v56, v57
	v_cvt_pk_f16_f32 v54, v58, v59
	v_mul_f32_e32 v46, v46, v50
	v_mul_f32_e32 v47, v47, v50
	v_cvt_pk_f16_f32 v55, v60, v61
	v_mul_f32_e32 v48, 0xbfb8aa3b, v48
	v_mul_f32_e32 v49, 0xbfb8aa3b, v49
	v_fma_f32 v42, v171, v42, v132
	v_max_f32_e32 v46, 0xc2a00000, v46
	v_max_f32_e32 v47, 0xc2a00000, v47
	s_waitcnt lgkmcnt(6)
	v_subrev_u32_e32 v242, s82, v242
	global_store_dwordx4 v242, v[238:241], s[82:83] offset:64 sc0 sc1
	ds_bpermute_b32 v232, v250, v52
	ds_bpermute_b32 v233, v250, v53
	ds_bpermute_b32 v234, v250, v54
	ds_bpermute_b32 v235, v250, v55
	ds_bpermute_b32 v236, v250, v62
	v_exp_f32_e32 v48, v48
	v_exp_f32_e32 v49, v49
	v_log_f32_e32 v52, v42
	v_add_f32_e32 v42, 1.0, v43
	v_mul_f32_e32 v43, v44, v50
	v_mul_f32_e32 v46, 0xbfb8aa3b, v46
	v_mul_f32_e32 v47, 0xbfb8aa3b, v47
	v_max_f32_e32 v43, 0xc2a00000, v43
	v_mul_f32_e32 v44, v45, v50
	v_exp_f32_e32 v46, v46
	v_exp_f32_e32 v47, v47
	v_mul_f32_e32 v43, 0xbfb8aa3b, v43
	v_max_f32_e32 v44, 0xc2a00000, v44
	v_exp_f32_e32 v43, v43
	v_mul_f32_e32 v44, 0xbfb8aa3b, v44
	v_add_f32_e32 v48, 1.0, v48
	v_add_f32_e32 v49, 1.0, v49
	v_exp_f32_e32 v44, v44
	v_rcp_f32_e32 v48, v48
	v_rcp_f32_e32 v49, v49
	v_add_f32_e32 v46, 1.0, v46
	v_add_f32_e32 v47, 1.0, v47
	v_mul_f32_e32 v34, v34, v50
	v_rcp_f32_e32 v46, v46
	v_rcp_f32_e32 v47, v47
	v_rcp_f32_e32 v42, v42
	v_add_f32_e32 v43, 1.0, v43
	v_max_f32_e32 v34, 0xc2a00000, v34
	v_rcp_f32_e32 v43, v43
	v_add_f32_e32 v44, 1.0, v44
	v_mul_f32_e32 v34, 0xbfb8aa3b, v34
	v_fma_f32 v48, v178, v48, v138
	v_fma_f32 v49, v177, v49, v139
	v_rcp_f32_e32 v44, v44
	v_exp_f32_e32 v34, v34
	v_log_f32_e32 v48, v48
	v_log_f32_e32 v49, v49
	v_fma_f32 v46, v180, v46, v136
	v_fma_f32 v47, v179, v47, v137
	v_fma_f32 v42, v170, v42, v133
	v_mul_f32_e32 v38, v38, v50
	v_log_f32_e32 v46, v46
	v_log_f32_e32 v47, v47
	v_log_f32_e32 v45, v42
	v_fma_f32 v42, v169, v43, v134
	v_max_f32_e32 v38, 0xc2a00000, v38
	v_mul_f32_e32 v35, v35, v50
	v_log_f32_e32 v53, v42
	v_fma_f32 v42, v155, v44, v135
	v_mul_f32_e32 v38, 0xbfb8aa3b, v38
	v_add_f32_e32 v34, 1.0, v34
	v_max_f32_e32 v35, 0xc2a00000, v35
	v_log_f32_e32 v54, v42
	v_cvt_pk_f16_f32 v43, v48, v49
	v_exp_f32_e32 v48, v38
	v_mul_f32_e32 v38, v39, v50
	v_rcp_f32_e32 v34, v34
	v_mul_f32_e32 v35, 0xbfb8aa3b, v35
	s_mov_b64 s[14:15], 0x90000
	v_max_f32_e32 v38, 0xc2a00000, v38
	v_exp_f32_e32 v35, v35
	v_cvt_pk_f16_f32 v42, v46, v47
	v_lshl_add_u64 v[46:47], v[166:167], 0, s[14:15]
	v_mul_f32_e32 v38, 0xbfb8aa3b, v38
	s_mov_b32 s14, 0x90000
	v_exp_f32_e32 v49, v38
	v_add_co_u32_e32 v38, vcc, s14, v166
	v_cvt_pk_f16_f32 v44, v52, v45
	v_cvt_pk_f16_f32 v45, v53, v54
	v_addc_co_u32_e32 v39, vcc, 0, v167, vcc
	v_fma_f32 v34, v123, v34, v124
	s_waitcnt lgkmcnt(6)
	v_subrev_u32_e32 v248, s82, v248
	global_store_dwordx4 v248, v[244:247], s[82:83] sc0 sc1
	ds_bpermute_b32 v238, v250, v42
	ds_bpermute_b32 v239, v250, v43
	ds_bpermute_b32 v240, v250, v44
	ds_bpermute_b32 v241, v250, v45
	ds_bpermute_b32 v242, v250, v38
	v_mul_f32_e32 v40, v40, v50
	v_mul_f32_e32 v41, v41, v50
	v_log_f32_e32 v42, v34
	v_add_f32_e32 v34, 1.0, v35
	v_mul_f32_e32 v35, v36, v50
	v_max_f32_e32 v35, 0xc2a00000, v35
	v_mul_f32_e32 v36, v37, v50
	v_max_f32_e32 v40, 0xc2a00000, v40
	v_max_f32_e32 v41, 0xc2a00000, v41
	v_mul_f32_e32 v35, 0xbfb8aa3b, v35
	v_max_f32_e32 v36, 0xc2a00000, v36
	v_mul_f32_e32 v40, 0xbfb8aa3b, v40
	v_mul_f32_e32 v41, 0xbfb8aa3b, v41
	v_exp_f32_e32 v35, v35
	v_mul_f32_e32 v36, 0xbfb8aa3b, v36
	v_exp_f32_e32 v40, v40
	v_exp_f32_e32 v41, v41
	v_exp_f32_e32 v36, v36
	v_mul_f32_e32 v26, v26, v51
	v_rcp_f32_e32 v34, v34
	v_add_f32_e32 v35, 1.0, v35
	v_max_f32_e32 v26, 0xc2a00000, v26
	v_add_f32_e32 v48, 1.0, v48
	v_add_f32_e32 v49, 1.0, v49
	v_add_f32_e32 v40, 1.0, v40
	v_add_f32_e32 v41, 1.0, v41
	v_rcp_f32_e32 v35, v35
	v_add_f32_e32 v36, 1.0, v36
	v_mul_f32_e32 v26, 0xbfb8aa3b, v26
	v_rcp_f32_e32 v48, v48
	v_rcp_f32_e32 v49, v49
	v_rcp_f32_e32 v40, v40
	v_rcp_f32_e32 v41, v41
	v_rcp_f32_e32 v36, v36
	v_exp_f32_e32 v26, v26
	v_fma_f32 v34, v120, v34, v125
	v_log_f32_e32 v37, v34
	v_fma_f32 v34, v118, v35, v126
	v_mul_f32_e32 v27, v27, v51
	v_fma_f32 v38, v153, v48, v128
	v_fma_f32 v39, v168, v49, v129
	v_fma_f32 v40, v121, v40, v130
	v_fma_f32 v41, v122, v41, v131
	v_log_f32_e32 v43, v34
	v_fma_f32 v34, v119, v36, v127
	v_add_f32_e32 v26, 1.0, v26
	v_max_f32_e32 v27, 0xc2a00000, v27
	v_log_f32_e32 v38, v38
	v_log_f32_e32 v39, v39
	v_log_f32_e32 v40, v40
	v_log_f32_e32 v41, v41
	v_log_f32_e32 v44, v34
	v_rcp_f32_e32 v26, v26
	v_mul_f32_e32 v27, 0xbfb8aa3b, v27
	v_exp_f32_e32 v27, v27
	v_mul_f32_e32 v32, v32, v51
	v_mul_f32_e32 v33, v33, v51
	v_max_f32_e32 v32, 0xc2a00000, v32
	v_max_f32_e32 v33, 0xc2a00000, v33
	v_cvt_pk_f16_f32 v34, v38, v39
	v_cvt_pk_f16_f32 v35, v40, v41
	v_cvt_pk_f16_f32 v36, v42, v37
	v_mul_f32_e32 v30, v30, v51
	v_mul_f32_e32 v31, v31, v51
	v_cvt_pk_f16_f32 v37, v43, v44
	v_mul_f32_e32 v32, 0xbfb8aa3b, v32
	v_mul_f32_e32 v33, 0xbfb8aa3b, v33
	v_fma_f32 v26, v171, v26, v132
	v_max_f32_e32 v30, 0xc2a00000, v30
	v_max_f32_e32 v31, 0xc2a00000, v31
	s_waitcnt lgkmcnt(5)
	v_subrev_u32_e32 v236, s82, v236
	global_store_dwordx4 v236, v[232:235], s[82:83] offset:64 sc0 sc1
	ds_bpermute_b32 v244, v250, v34
	ds_bpermute_b32 v245, v250, v35
	ds_bpermute_b32 v246, v250, v36
	ds_bpermute_b32 v247, v250, v37
	ds_bpermute_b32 v248, v250, v46
	v_exp_f32_e32 v32, v32
	v_exp_f32_e32 v33, v33
	v_log_f32_e32 v34, v26
	v_add_f32_e32 v26, 1.0, v27
	v_mul_f32_e32 v27, v28, v51
	v_mul_f32_e32 v30, 0xbfb8aa3b, v30
	v_mul_f32_e32 v31, 0xbfb8aa3b, v31
	v_max_f32_e32 v27, 0xc2a00000, v27
	v_mul_f32_e32 v28, v29, v51
	v_exp_f32_e32 v30, v30
	v_exp_f32_e32 v31, v31
	v_mul_f32_e32 v27, 0xbfb8aa3b, v27
	v_max_f32_e32 v28, 0xc2a00000, v28
	v_exp_f32_e32 v27, v27
	v_mul_f32_e32 v28, 0xbfb8aa3b, v28
	v_add_f32_e32 v32, 1.0, v32
	v_add_f32_e32 v33, 1.0, v33
	v_exp_f32_e32 v28, v28
	v_rcp_f32_e32 v32, v32
	v_rcp_f32_e32 v33, v33
	v_add_f32_e32 v30, 1.0, v30
	v_add_f32_e32 v31, 1.0, v31
	v_mul_f32_e32 v18, v18, v51
	v_rcp_f32_e32 v30, v30
	v_rcp_f32_e32 v31, v31
	v_rcp_f32_e32 v26, v26
	v_add_f32_e32 v27, 1.0, v27
	v_max_f32_e32 v18, 0xc2a00000, v18
	v_rcp_f32_e32 v27, v27
	v_add_f32_e32 v28, 1.0, v28
	v_mul_f32_e32 v18, 0xbfb8aa3b, v18
	v_fma_f32 v32, v178, v32, v138
	v_fma_f32 v33, v177, v33, v139
	v_rcp_f32_e32 v28, v28
	v_exp_f32_e32 v18, v18
	v_log_f32_e32 v32, v32
	v_log_f32_e32 v33, v33
	v_fma_f32 v30, v180, v30, v136
	v_fma_f32 v31, v179, v31, v137
	v_fma_f32 v26, v170, v26, v133
	v_mul_f32_e32 v22, v22, v51
	v_log_f32_e32 v30, v30
	v_log_f32_e32 v31, v31
	v_log_f32_e32 v29, v26
	v_fma_f32 v26, v169, v27, v134
	v_max_f32_e32 v22, 0xc2a00000, v22
	v_mul_f32_e32 v19, v19, v51
	v_log_f32_e32 v35, v26
	v_fma_f32 v26, v155, v28, v135
	v_mul_f32_e32 v22, 0xbfb8aa3b, v22
	v_add_f32_e32 v18, 1.0, v18
	v_max_f32_e32 v19, 0xc2a00000, v19
	v_log_f32_e32 v36, v26
	v_cvt_pk_f16_f32 v27, v32, v33
	v_exp_f32_e32 v32, v22
	v_mul_f32_e32 v22, v23, v51
	v_rcp_f32_e32 v18, v18
	v_mul_f32_e32 v19, 0xbfb8aa3b, v19
	s_mov_b64 s[14:15], 0xa0000
	v_max_f32_e32 v22, 0xc2a00000, v22
	v_exp_f32_e32 v19, v19
	v_cvt_pk_f16_f32 v26, v30, v31
	v_lshl_add_u64 v[30:31], v[166:167], 0, s[14:15]
	v_mul_f32_e32 v22, 0xbfb8aa3b, v22
	s_mov_b32 s14, 0xa0000
	v_exp_f32_e32 v33, v22
	v_add_co_u32_e32 v22, vcc, s14, v166
	v_cvt_pk_f16_f32 v28, v34, v29
	v_cvt_pk_f16_f32 v29, v35, v36
	v_addc_co_u32_e32 v23, vcc, 0, v167, vcc
	v_fma_f32 v18, v123, v18, v124
	s_waitcnt lgkmcnt(5)
	v_subrev_u32_e32 v242, s82, v242
	global_store_dwordx4 v242, v[238:241], s[82:83] sc0 sc1
	ds_bpermute_b32 v232, v250, v26
	ds_bpermute_b32 v233, v250, v27
	ds_bpermute_b32 v234, v250, v28
	ds_bpermute_b32 v235, v250, v29
	ds_bpermute_b32 v236, v250, v22
	v_mul_f32_e32 v24, v24, v51
	v_mul_f32_e32 v25, v25, v51
	v_log_f32_e32 v26, v18
	v_add_f32_e32 v18, 1.0, v19
	v_mul_f32_e32 v19, v20, v51
	v_max_f32_e32 v19, 0xc2a00000, v19
	v_mul_f32_e32 v20, v21, v51
	ds_read_b32 v28, v176 offset:704
	v_max_f32_e32 v24, 0xc2a00000, v24
	v_max_f32_e32 v25, 0xc2a00000, v25
	v_mul_f32_e32 v19, 0xbfb8aa3b, v19
	v_max_f32_e32 v20, 0xc2a00000, v20
	v_mul_f32_e32 v24, 0xbfb8aa3b, v24
	v_mul_f32_e32 v25, 0xbfb8aa3b, v25
	v_exp_f32_e32 v19, v19
	v_mul_f32_e32 v20, 0xbfb8aa3b, v20
	v_exp_f32_e32 v24, v24
	v_exp_f32_e32 v25, v25
	v_exp_f32_e32 v20, v20
	s_waitcnt lgkmcnt(0)
	v_mul_f32_e32 v10, v10, v28
	v_rcp_f32_e32 v18, v18
	v_add_f32_e32 v19, 1.0, v19
	v_max_f32_e32 v10, 0xc2a00000, v10
	v_add_f32_e32 v32, 1.0, v32
	v_add_f32_e32 v33, 1.0, v33
	v_add_f32_e32 v24, 1.0, v24
	v_add_f32_e32 v25, 1.0, v25
	v_rcp_f32_e32 v19, v19
	v_add_f32_e32 v20, 1.0, v20
	v_mul_f32_e32 v10, 0xbfb8aa3b, v10
	v_rcp_f32_e32 v32, v32
	v_rcp_f32_e32 v33, v33
	v_rcp_f32_e32 v24, v24
	v_rcp_f32_e32 v25, v25
	v_rcp_f32_e32 v20, v20
	v_exp_f32_e32 v10, v10
	v_fma_f32 v18, v120, v18, v125
	v_log_f32_e32 v21, v18
	v_fma_f32 v18, v118, v19, v126
	v_mul_f32_e32 v11, v11, v28
	v_fma_f32 v22, v153, v32, v128
	v_fma_f32 v23, v168, v33, v129
	v_fma_f32 v24, v121, v24, v130
	v_fma_f32 v25, v122, v25, v131
	v_log_f32_e32 v27, v18
	v_fma_f32 v18, v119, v20, v127
	v_add_f32_e32 v10, 1.0, v10
	v_max_f32_e32 v11, 0xc2a00000, v11
	v_log_f32_e32 v22, v22
	v_log_f32_e32 v23, v23
	v_log_f32_e32 v24, v24
	v_log_f32_e32 v25, v25
	v_log_f32_e32 v29, v18
	v_rcp_f32_e32 v10, v10
	v_mul_f32_e32 v11, 0xbfb8aa3b, v11
	v_mul_f32_e32 v14, v14, v28
	v_mul_f32_e32 v15, v15, v28
	v_exp_f32_e32 v11, v11
	v_max_f32_e32 v14, 0xc2a00000, v14
	v_max_f32_e32 v15, 0xc2a00000, v15
	v_mul_f32_e32 v14, 0xbfb8aa3b, v14
	v_mul_f32_e32 v15, 0xbfb8aa3b, v15
	v_cvt_pk_f16_f32 v18, v22, v23
	v_cvt_pk_f16_f32 v19, v24, v25
	v_cvt_pk_f16_f32 v20, v26, v21
	v_exp_f32_e32 v14, v14
	v_exp_f32_e32 v15, v15
	v_cvt_pk_f16_f32 v21, v27, v29
	v_fma_f32 v10, v171, v10, v132
	s_waitcnt lgkmcnt(6)
	v_subrev_u32_e32 v248, s82, v248
	global_store_dwordx4 v248, v[244:247], s[82:83] offset:64 sc0 sc1
	ds_bpermute_b32 v238, v250, v18
	ds_bpermute_b32 v239, v250, v19
	ds_bpermute_b32 v240, v250, v20
	ds_bpermute_b32 v241, v250, v21
	ds_bpermute_b32 v242, v250, v30
	v_add_f32_e32 v14, 1.0, v14
	v_add_f32_e32 v15, 1.0, v15
	v_log_f32_e32 v18, v10
	v_add_f32_e32 v10, 1.0, v11
	v_mul_f32_e32 v11, v12, v28
	v_max_f32_e32 v11, 0xc2a00000, v11
	v_mul_f32_e32 v11, 0xbfb8aa3b, v11
	v_exp_f32_e32 v11, v11
	v_rcp_f32_e32 v14, v14
	v_rcp_f32_e32 v15, v15
	v_mul_f32_e32 v16, v16, v28
	v_mul_f32_e32 v17, v17, v28
	v_rcp_f32_e32 v10, v10
	v_mul_f32_e32 v12, v13, v28
	v_add_f32_e32 v11, 1.0, v11
	v_fma_f32 v14, v180, v14, v136
	v_fma_f32 v15, v179, v15, v137
	v_max_f32_e32 v16, 0xc2a00000, v16
	v_max_f32_e32 v17, 0xc2a00000, v17
	v_max_f32_e32 v12, 0xc2a00000, v12
	v_rcp_f32_e32 v11, v11
	v_log_f32_e32 v14, v14
	v_mul_f32_e32 v16, 0xbfb8aa3b, v16
	v_mul_f32_e32 v17, 0xbfb8aa3b, v17
	v_log_f32_e32 v15, v15
	v_mul_f32_e32 v12, 0xbfb8aa3b, v12
	v_exp_f32_e32 v16, v16
	v_exp_f32_e32 v17, v17
	v_exp_f32_e32 v12, v12
	v_mul_f32_e32 v6, v6, v28
	v_fma_f32 v10, v170, v10, v133
	v_max_f32_e32 v6, 0xc2a00000, v6
	v_log_f32_e32 v13, v10
	v_fma_f32 v10, v169, v11, v134
	v_mul_f32_e32 v6, 0xbfb8aa3b, v6
	v_log_f32_e32 v19, v10
	v_cvt_pk_f16_f32 v10, v14, v15
	v_exp_f32_e32 v14, v6
	v_mul_f32_e32 v6, v7, v28
	v_mul_f32_e32 v8, v8, v28
	v_mul_f32_e32 v9, v9, v28
	v_mul_f32_e32 v2, v2, v28
	v_mul_f32_e32 v3, v3, v28
	v_mul_f32_e32 v4, v4, v28
	v_mul_f32_e32 v5, v5, v28
	v_add_f32_e32 v16, 1.0, v16
	v_add_f32_e32 v17, 1.0, v17
	v_add_f32_e32 v12, 1.0, v12
	v_max_f32_e32 v6, 0xc2a00000, v6
	v_max_f32_e32 v8, 0xc2a00000, v8
	v_max_f32_e32 v9, 0xc2a00000, v9
	v_max_f32_e32 v2, 0xc2a00000, v2
	v_max_f32_e32 v3, 0xc2a00000, v3
	v_max_f32_e32 v4, 0xc2a00000, v4
	v_max_f32_e32 v5, 0xc2a00000, v5
	v_rcp_f32_e32 v16, v16
	v_rcp_f32_e32 v17, v17
	v_rcp_f32_e32 v12, v12
	v_mul_f32_e32 v6, 0xbfb8aa3b, v6
	v_mul_f32_e32 v8, 0xbfb8aa3b, v8
	v_mul_f32_e32 v9, 0xbfb8aa3b, v9
	v_mul_f32_e32 v2, 0xbfb8aa3b, v2
	v_mul_f32_e32 v3, 0xbfb8aa3b, v3
	v_mul_f32_e32 v4, 0xbfb8aa3b, v4
	v_mul_f32_e32 v5, 0xbfb8aa3b, v5
	v_exp_f32_e32 v15, v6
	v_exp_f32_e32 v8, v8
	v_exp_f32_e32 v9, v9
	v_exp_f32_e32 v2, v2
	v_exp_f32_e32 v3, v3
	v_exp_f32_e32 v4, v4
	v_exp_f32_e32 v5, v5
	v_fma_f32 v16, v178, v16, v138
	v_fmac_f32_e32 v139, v177, v17
	v_fmac_f32_e32 v135, v155, v12
	v_log_f32_e32 v16, v16
	v_log_f32_e32 v17, v139
	v_log_f32_e32 v20, v135
	v_add_f32_e32 v14, 1.0, v14
	v_add_f32_e32 v15, 1.0, v15
	v_add_f32_e32 v8, 1.0, v8
	v_add_f32_e32 v9, 1.0, v9
	v_add_f32_e32 v2, 1.0, v2
	v_add_f32_e32 v3, 1.0, v3
	v_add_f32_e32 v4, 1.0, v4
	v_add_f32_e32 v5, 1.0, v5
	s_mov_b64 s[14:15], 0xb0000
	v_rcp_f32_e32 v14, v14
	v_rcp_f32_e32 v15, v15
	v_rcp_f32_e32 v8, v8
	v_rcp_f32_e32 v9, v9
	v_rcp_f32_e32 v2, v2
	v_rcp_f32_e32 v3, v3
	v_rcp_f32_e32 v4, v4
	v_rcp_f32_e32 v5, v5
	v_lshl_add_u64 v[136:137], v[166:167], 0, s[14:15]
	s_mov_b32 s14, 0xb0000
	v_add_co_u32_e32 v6, vcc, s14, v166
	v_cvt_pk_f16_f32 v11, v16, v17
	v_cvt_pk_f16_f32 v12, v18, v13
	v_cvt_pk_f16_f32 v13, v19, v20
	v_addc_co_u32_e32 v7, vcc, 0, v167, vcc
	s_waitcnt lgkmcnt(6)
	v_subrev_u32_e32 v236, s82, v236
	global_store_dwordx4 v236, v[232:235], s[82:83] sc0 sc1
	ds_bpermute_b32 v244, v250, v10
	ds_bpermute_b32 v245, v250, v11
	ds_bpermute_b32 v246, v250, v12
	ds_bpermute_b32 v247, v250, v13
	ds_bpermute_b32 v248, v250, v6
	v_fma_f32 v6, v153, v14, v128
	v_fma_f32 v7, v168, v15, v129
	v_fma_f32 v8, v121, v8, v130
	v_fmac_f32_e32 v131, v122, v9
	v_fma_f32 v2, v123, v2, v124
	v_fma_f32 v3, v120, v3, v125
	v_fma_f32 v4, v118, v4, v126
	v_fmac_f32_e32 v127, v119, v5
	v_log_f32_e32 v6, v6
	v_log_f32_e32 v7, v7
	v_log_f32_e32 v8, v8
	v_log_f32_e32 v9, v131
	v_log_f32_e32 v2, v2
	v_log_f32_e32 v3, v3
	v_log_f32_e32 v4, v4
	v_log_f32_e32 v5, v127
	v_cvt_pk_f16_f32 v196, v181, v182
	v_cvt_pk_f16_f32 v132, v6, v7
	v_cvt_pk_f16_f32 v133, v8, v9
	v_cvt_pk_f16_f32 v134, v2, v3
	v_cvt_pk_f16_f32 v135, v4, v5
	s_waitcnt lgkmcnt(5)
	v_subrev_u32_e32 v242, s82, v242
	global_store_dwordx4 v242, v[238:241], s[82:83] offset:64 sc0 sc1
	ds_bpermute_b32 v232, v250, v194
	ds_bpermute_b32 v233, v250, v195
	ds_bpermute_b32 v234, v250, v196
	ds_bpermute_b32 v235, v250, v197
	ds_bpermute_b32 v236, v250, v166
	s_andn2_b64 vcc, exec, s[38:39]
	s_mov_b64 s[28:29], -1
	s_waitcnt lgkmcnt(5)
	v_subrev_u32_e32 v248, s82, v248
	global_store_dwordx4 v248, v[244:247], s[82:83] sc0 sc1
	ds_bpermute_b32 v238, v250, v132
	ds_bpermute_b32 v239, v250, v133
	ds_bpermute_b32 v240, v250, v134
	ds_bpermute_b32 v241, v250, v135
	ds_bpermute_b32 v242, v250, v136
	s_waitcnt lgkmcnt(5)
	v_subrev_u32_e32 v236, s82, v236
	global_store_dwordx4 v236, v[232:235], s[82:83] offset:64 sc0 sc1
	s_waitcnt lgkmcnt(0)
	v_subrev_u32_e32 v242, s82, v242
	global_store_dwordx4 v242, v[238:241], s[82:83] offset:64 sc0 sc1
	s_cbranch_vccnz .LBB0_495
